# v29: v25 + K-loop latch scalar updates executed before the trip's last barrier (back-edge work out of the load segment's head)
# baseline (speedup 1.0000x reference)
; #define PG8_STAGE(bufoff, gbase, voff) do { _Pragma("unroll") for (int _i = 0; _i < 2; ++_i) \
;         __builtin_amdgcn_global_load_lds((const unsigned*)((const char*)(gbase) + (voff)[_i]), (LAS unsigned*)(lds + (bufoff) + ldsw + _i * 8192), 16, 0, 0); } while (0)
; #define PG8_LDA(dst, b, h) do { if constexpr (F8) { _Pragma("unroll") for (int m = 0; m < 4; ++m) dst##8[m] = PG8_LD8(lds, PG8_SA(b, h) + aoff + m * 2048); } \
;         else { _Pragma("unroll") for (int m = 0; m < 4; ++m) _Pragma("unroll") for (int k = 0; k < 2; ++k) dst[m][k] = *(const LAS bf16x8*)(lds + PG8_SA(b, h) + aoff + m * 2048 + k * 1024); } } while (0)
; #define PG8_LDB(dst, b, h) do { if constexpr (F8) { _Pragma("unroll") for (int n = 0; n < 2; ++n) dst##8[n] = PG8_LD8(ldsB, PG8_SBR(b, h) + boff + n * 2048); } \
;         else { _Pragma("unroll") for (int n = 0; n < 2; ++n) _Pragma("unroll") for (int k = 0; k < 2; ++k) dst[n][k] = *(const LAS bf16x8*)(ldsB + PG8_SBR(b, h) + boff + n * 2048 + k * 1024); } } while (0)
; #define PG8_WAIT_V(n) asm volatile("s_waitcnt vmcnt(" #n ")" ::: "memory")
; #define PG8_WAIT_L(n) asm volatile("s_waitcnt lgkmcnt(" #n ")" ::: "memory")
; #define PG8_BAR __builtin_amdgcn_s_barrier()
; #define PG8_SCHED __builtin_amdgcn_sched_barrier(0)
; template <bool GATHER, bool F8, class Epi, class Sched>
; __device__ __forceinline__ void gemm_phase(LAS unsigned char* lds, const int nt, const unsigned lda, const unsigned ldb, const Sched& S, const Epi& E) {
;     ...
;             PG8_LDB(B0, 0, 0); PG8_LDB(B1, 0, 1); PG8_SCHED; PG8_LDA(At, 0, 0); PG8_STAGE(PG8_SA(1, 1), a1 + hA, vA1);
;             PG8_WAIT_V(8); PG8_WAIT_L(0); PG8_BAR; PG8_MMA(0, 0, At, B0); PG8_MMA(0, 1, At, B1); PG8_BAR; PG8_SCHED;
;             PG8_LDA(At, 0, 1); PG8_STAGE(PG8_SB(0, 0), b2, voffB); PG8_STAGE(PG8_SB(0, 1), b2 + hB, voffB); PG8_STAGE(PG8_SA(0, 0), a2, w0);
;             PG8_WAIT_V(8); PG8_WAIT_L(0); PG8_BAR; PG8_MMA(1, 0, At, B0); PG8_MMA(1, 1, At, B1); PG8_BAR; PG8_SCHED;
.LBB0_247:
	ds_read_b128 v[148:151], v181
	ds_read_b128 v[152:155], v181 offset:1024
	ds_read_b128 v[156:159], v181 offset:2048
	ds_read_b128 v[160:163], v181 offset:3072
	ds_read_b128 v[190:193], v182
	ds_read_b128 v[194:197], v182 offset:1024
	ds_read_b128 v[200:203], v182 offset:2048
	ds_read_b128 v[204:207], v182 offset:3072
	s_add_u32 s34, s10, 0xfff80080
	s_addc_u32 s35, s11, -1
	s_cmp_eq_u32 s33, 28
	s_cselect_b32 s37, s1, s35
	s_cselect_b32 s36, s0, s34
	s_cselect_b32 s35, s31, s27
	s_cselect_b32 s34, s30, s14
	s_add_i32 m0, s42, 0xc000
	ds_read_b128 v[208:211], v183
	ds_read_b128 v[212:215], v183 offset:1024
	ds_read_b128 v[216:219], v183 offset:2048
	ds_read_b128 v[220:223], v183 offset:3072
	ds_read_b128 v[224:227], v183 offset:4096
	ds_read_b128 v[228:231], v183 offset:5120
	ds_read_b128 v[232:235], v183 offset:6144
	ds_read_b128 v[236:239], v183 offset:7168
	global_load_lds_dwordx4 v140, s[10:11]
	s_add_i32 m0, s42, 0xe000
	s_nop 0
	global_load_lds_dwordx4 v142, s[10:11]
	s_waitcnt vmcnt(8)
	s_waitcnt lgkmcnt(0)
	s_barrier
	s_setprio 1
	s_waitcnt lgkmcnt(0)
	v_mfma_f32_16x16x32_bf16 v[126:129], v[148:151], v[208:211], v[126:129]
	v_mfma_f32_16x16x32_bf16 v[122:125], v[156:159], v[208:211], v[122:125]
	v_mfma_f32_16x16x32_bf16 v[110:113], v[148:151], v[216:219], v[110:113]
	v_mfma_f32_16x16x32_bf16 v[106:109], v[156:159], v[216:219], v[106:109]
	v_mfma_f32_16x16x32_bf16 v[94:97], v[148:151], v[224:227], v[94:97]
	v_mfma_f32_16x16x32_bf16 v[90:93], v[156:159], v[224:227], v[90:93]
	v_mfma_f32_16x16x32_bf16 v[78:81], v[148:151], v[232:235], v[78:81]
	v_mfma_f32_16x16x32_bf16 v[74:77], v[156:159], v[232:235], v[74:77]
	v_mfma_f32_16x16x32_bf16 v[126:129], v[152:155], v[212:215], v[126:129]
	v_mfma_f32_16x16x32_bf16 v[122:125], v[160:163], v[212:215], v[122:125]
	v_mfma_f32_16x16x32_bf16 v[110:113], v[152:155], v[220:223], v[110:113]
	v_mfma_f32_16x16x32_bf16 v[106:109], v[160:163], v[220:223], v[106:109]
	v_mfma_f32_16x16x32_bf16 v[94:97], v[152:155], v[228:231], v[94:97]
	v_mfma_f32_16x16x32_bf16 v[90:93], v[160:163], v[228:231], v[90:93]
	v_mfma_f32_16x16x32_bf16 v[78:81], v[152:155], v[236:239], v[78:81]
	v_mfma_f32_16x16x32_bf16 v[74:77], v[160:163], v[236:239], v[74:77]
	s_setprio 0
	s_setprio 1
	v_mfma_f32_16x16x32_bf16 v[118:121], v[190:193], v[208:211], v[118:121]
	v_mfma_f32_16x16x32_bf16 v[114:117], v[200:203], v[208:211], v[114:117]
	v_mfma_f32_16x16x32_bf16 v[102:105], v[190:193], v[216:219], v[102:105]
	v_mfma_f32_16x16x32_bf16 v[98:101], v[200:203], v[216:219], v[98:101]
	v_mfma_f32_16x16x32_bf16 v[86:89], v[190:193], v[224:227], v[86:89]
	v_mfma_f32_16x16x32_bf16 v[82:85], v[200:203], v[224:227], v[82:85]
	v_mfma_f32_16x16x32_bf16 v[70:73], v[190:193], v[232:235], v[70:73]
	v_mfma_f32_16x16x32_bf16 v[66:69], v[200:203], v[232:235], v[66:69]
	v_mfma_f32_16x16x32_bf16 v[118:121], v[194:197], v[212:215], v[118:121]
	v_mfma_f32_16x16x32_bf16 v[114:117], v[204:207], v[212:215], v[114:117]
	v_mfma_f32_16x16x32_bf16 v[102:105], v[194:197], v[220:223], v[102:105]
	v_mfma_f32_16x16x32_bf16 v[98:101], v[204:207], v[220:223], v[98:101]
	v_mfma_f32_16x16x32_bf16 v[86:89], v[194:197], v[228:231], v[86:89]
	v_mfma_f32_16x16x32_bf16 v[82:85], v[204:207], v[228:231], v[82:85]
	v_mfma_f32_16x16x32_bf16 v[70:73], v[194:197], v[236:239], v[70:73]
	v_mfma_f32_16x16x32_bf16 v[66:69], v[204:207], v[236:239], v[66:69]
	s_setprio 0
	s_barrier
	s_add_i32 s38, s58, s29
	s_mov_b32 m0, s38
	ds_read_b128 v[208:211], v183 offset:16384
	ds_read_b128 v[212:215], v183 offset:17408
	ds_read_b128 v[216:219], v183 offset:18432
	ds_read_b128 v[220:223], v183 offset:19456
	ds_read_b128 v[224:227], v183 offset:20480
	ds_read_b128 v[228:231], v183 offset:21504
	ds_read_b128 v[232:235], v183 offset:22528
	ds_read_b128 v[236:239], v183 offset:23552
	global_load_lds_dwordx4 v132, s[34:35]
	s_add_i32 m0, s38, 0x2000
	s_add_u32 s64, s34, 0x80000
	s_addc_u32 s65, s35, 0
	s_add_i32 s38, s59, s29
	global_load_lds_dwordx4 v136, s[34:35]
	s_mov_b32 m0, s38
	s_nop 0
	global_load_lds_dwordx4 v132, s[64:65]
	s_add_i32 m0, s38, 0x2000
	s_nop 0
	global_load_lds_dwordx4 v136, s[64:65]
	s_mov_b32 m0, s42
	s_nop 0
	s_mov_b64 s[98:99], s[36:37]
	global_load_lds_dwordx4 v130, s[36:37]
	s_mov_b32 m0, s43
	s_nop 0
	global_load_lds_dwordx4 v134, s[36:37]
	s_waitcnt vmcnt(8)
	s_waitcnt lgkmcnt(0)
	s_barrier
	s_setprio 1
	s_waitcnt lgkmcnt(0)
	v_mfma_f32_16x16x32_bf16 v[62:65], v[148:151], v[208:211], v[62:65]
	v_mfma_f32_16x16x32_bf16 v[50:53], v[156:159], v[208:211], v[50:53]
	v_mfma_f32_16x16x32_bf16 v[38:41], v[148:151], v[216:219], v[38:41]
	v_mfma_f32_16x16x32_bf16 v[34:37], v[156:159], v[216:219], v[34:37]
	v_mfma_f32_16x16x32_bf16 v[22:25], v[148:151], v[224:227], v[22:25]
	v_mfma_f32_16x16x32_bf16 v[18:21], v[156:159], v[224:227], v[18:21]
	v_mfma_f32_16x16x32_bf16 v[6:9], v[148:151], v[232:235], v[6:9]
	v_mfma_f32_16x16x32_bf16 v[2:5], v[156:159], v[232:235], v[2:5]
	v_mfma_f32_16x16x32_bf16 v[62:65], v[152:155], v[212:215], v[62:65]
	v_mfma_f32_16x16x32_bf16 v[50:53], v[160:163], v[212:215], v[50:53]
	v_mfma_f32_16x16x32_bf16 v[38:41], v[152:155], v[220:223], v[38:41]
	v_mfma_f32_16x16x32_bf16 v[34:37], v[160:163], v[220:223], v[34:37]
	v_mfma_f32_16x16x32_bf16 v[22:25], v[152:155], v[228:231], v[22:25]
	v_mfma_f32_16x16x32_bf16 v[18:21], v[160:163], v[228:231], v[18:21]
	v_mfma_f32_16x16x32_bf16 v[6:9], v[152:155], v[236:239], v[6:9]
	v_mfma_f32_16x16x32_bf16 v[2:5], v[160:163], v[236:239], v[2:5]
	s_setprio 0
	s_setprio 1
	v_mfma_f32_16x16x32_bf16 v[58:61], v[190:193], v[208:211], v[58:61]
	v_mfma_f32_16x16x32_bf16 v[54:57], v[200:203], v[208:211], v[54:57]
	v_mfma_f32_16x16x32_bf16 v[46:49], v[190:193], v[216:219], v[46:49]
	v_mfma_f32_16x16x32_bf16 v[42:45], v[200:203], v[216:219], v[42:45]
	v_mfma_f32_16x16x32_bf16 v[30:33], v[190:193], v[224:227], v[30:33]
	v_mfma_f32_16x16x32_bf16 v[26:29], v[200:203], v[224:227], v[26:29]
	v_mfma_f32_16x16x32_bf16 v[14:17], v[190:193], v[232:235], v[14:17]
	v_mfma_f32_16x16x32_bf16 v[10:13], v[200:203], v[232:235], v[10:13]
	v_mfma_f32_16x16x32_bf16 v[58:61], v[194:197], v[212:215], v[58:61]
	v_mfma_f32_16x16x32_bf16 v[54:57], v[204:207], v[212:215], v[54:57]
	v_mfma_f32_16x16x32_bf16 v[46:49], v[194:197], v[220:223], v[46:49]
	v_mfma_f32_16x16x32_bf16 v[42:45], v[204:207], v[220:223], v[42:45]
	v_mfma_f32_16x16x32_bf16 v[30:33], v[194:197], v[228:231], v[30:33]
	v_mfma_f32_16x16x32_bf16 v[26:29], v[204:207], v[228:231], v[26:29]
	v_mfma_f32_16x16x32_bf16 v[14:17], v[194:197], v[236:239], v[14:17]
	v_mfma_f32_16x16x32_bf16 v[10:13], v[204:207], v[236:239], v[10:13]
	s_setprio 0
	s_barrier
; #define PG8_STAGE(bufoff, gbase, voff) do { _Pragma("unroll") for (int _i = 0; _i < 2; ++_i) \
;         __builtin_amdgcn_global_load_lds((const unsigned*)((const char*)(gbase) + (voff)[_i]), (LAS unsigned*)(lds + (bufoff) + ldsw + _i * 8192), 16, 0, 0); } while (0)
; #define PG8_LDA(dst, b, h) do { if constexpr (F8) { _Pragma("unroll") for (int m = 0; m < 4; ++m) dst##8[m] = PG8_LD8(lds, PG8_SA(b, h) + aoff + m * 2048); } \
;         else { _Pragma("unroll") for (int m = 0; m < 4; ++m) _Pragma("unroll") for (int k = 0; k < 2; ++k) dst[m][k] = *(const LAS bf16x8*)(lds + PG8_SA(b, h) + aoff + m * 2048 + k * 1024); } } while (0)
; #define PG8_LDB(dst, b, h) do { if constexpr (F8) { _Pragma("unroll") for (int n = 0; n < 2; ++n) dst##8[n] = PG8_LD8(ldsB, PG8_SBR(b, h) + boff + n * 2048); } \
;         else { _Pragma("unroll") for (int n = 0; n < 2; ++n) _Pragma("unroll") for (int k = 0; k < 2; ++k) dst[n][k] = *(const LAS bf16x8*)(ldsB + PG8_SBR(b, h) + boff + n * 2048 + k * 1024); } } while (0)
; #define PG8_WAIT_V(n) asm volatile("s_waitcnt vmcnt(" #n ")" ::: "memory")
; #define PG8_WAIT_L(n) asm volatile("s_waitcnt lgkmcnt(" #n ")" ::: "memory")
; #define PG8_BAR __builtin_amdgcn_s_barrier()
; #define PG8_SCHED __builtin_amdgcn_sched_barrier(0)
; template <bool GATHER, bool F8, class Epi, class Sched>
; __device__ __forceinline__ void gemm_phase(LAS unsigned char* lds, const int nt, const unsigned lda, const unsigned ldb, const Sched& S, const Epi& E) {
;     ...
;             PG8_LDB(B0, 1, 0); PG8_LDB(B1, 1, 1); PG8_SCHED; PG8_LDA(At, 1, 0); PG8_STAGE(PG8_SA(0, 1), a2 + hA, w1);
;             PG8_WAIT_V(8); PG8_WAIT_L(0); PG8_BAR; PG8_MMA(0, 0, At, B0); PG8_MMA(0, 1, At, B1); PG8_BAR; PG8_SCHED;
;             PG8_LDA(At, 1, 1); PG8_STAGE(PG8_SB(1, 0), b3, voffB); PG8_STAGE(PG8_SB(1, 1), b3 + hB, voffB); PG8_STAGE(PG8_SA(1, 0), a3, w0);
;             PG8_WAIT_V(8); PG8_WAIT_L(0); PG8_BAR; PG8_MMA(1, 0, At, B0); PG8_MMA(1, 1, At, B1); PG8_BAR; PG8_SCHED;
;         }
	s_add_i32 s38, 0, 0x18000
	v_add_u32_e32 v138, s38, v178
	s_add_i32 s64, 0, 0x1c000
	ds_read_b128 v[148:151], v138
	ds_read_b128 v[152:155], v138 offset:1024
	ds_read_b128 v[156:159], v138 offset:2048
	ds_read_b128 v[160:163], v138 offset:3072
	v_add_u32_e32 v138, s64, v178
	ds_read_b128 v[190:193], v138
	ds_read_b128 v[194:197], v138 offset:1024
	ds_read_b128 v[200:203], v138 offset:2048
	ds_read_b128 v[204:207], v138 offset:3072
	s_add_u32 s36, s36, 0x80000
	s_addc_u32 s37, s37, 0
	s_mov_b32 m0, s44
	ds_read_b128 v[208:211], v183 offset:32768
	ds_read_b128 v[212:215], v183 offset:33792
	ds_read_b128 v[216:219], v183 offset:34816
	ds_read_b128 v[220:223], v183 offset:35840
	ds_read_b128 v[224:227], v183 offset:36864
	ds_read_b128 v[228:231], v183 offset:37888
	ds_read_b128 v[232:235], v183 offset:38912
	ds_read_b128 v[236:239], v183 offset:39936
	global_load_lds_dwordx4 v130, s[36:37]
	s_mov_b32 m0, s45
	s_nop 0
	global_load_lds_dwordx4 v134, s[36:37]
	s_waitcnt vmcnt(8)
	s_waitcnt lgkmcnt(0)
	s_barrier
	s_setprio 1
	s_waitcnt lgkmcnt(0)
	v_mfma_f32_16x16x32_bf16 v[126:129], v[148:151], v[208:211], v[126:129]
	v_mfma_f32_16x16x32_bf16 v[122:125], v[156:159], v[208:211], v[122:125]
	v_mfma_f32_16x16x32_bf16 v[110:113], v[148:151], v[216:219], v[110:113]
	v_mfma_f32_16x16x32_bf16 v[106:109], v[156:159], v[216:219], v[106:109]
	v_mfma_f32_16x16x32_bf16 v[94:97], v[148:151], v[224:227], v[94:97]
	v_mfma_f32_16x16x32_bf16 v[90:93], v[156:159], v[224:227], v[90:93]
	v_mfma_f32_16x16x32_bf16 v[78:81], v[148:151], v[232:235], v[78:81]
	v_mfma_f32_16x16x32_bf16 v[74:77], v[156:159], v[232:235], v[74:77]
	v_mfma_f32_16x16x32_bf16 v[126:129], v[152:155], v[212:215], v[126:129]
	v_mfma_f32_16x16x32_bf16 v[122:125], v[160:163], v[212:215], v[122:125]
	v_mfma_f32_16x16x32_bf16 v[110:113], v[152:155], v[220:223], v[110:113]
	v_mfma_f32_16x16x32_bf16 v[106:109], v[160:163], v[220:223], v[106:109]
	v_mfma_f32_16x16x32_bf16 v[94:97], v[152:155], v[228:231], v[94:97]
	v_mfma_f32_16x16x32_bf16 v[90:93], v[160:163], v[228:231], v[90:93]
	v_mfma_f32_16x16x32_bf16 v[78:81], v[152:155], v[236:239], v[78:81]
	v_mfma_f32_16x16x32_bf16 v[74:77], v[160:163], v[236:239], v[74:77]
	s_setprio 0
	s_setprio 1
	v_mfma_f32_16x16x32_bf16 v[118:121], v[190:193], v[208:211], v[118:121]
	v_mfma_f32_16x16x32_bf16 v[114:117], v[200:203], v[208:211], v[114:117]
	v_mfma_f32_16x16x32_bf16 v[102:105], v[190:193], v[216:219], v[102:105]
	v_mfma_f32_16x16x32_bf16 v[98:101], v[200:203], v[216:219], v[98:101]
	v_mfma_f32_16x16x32_bf16 v[86:89], v[190:193], v[224:227], v[86:89]
	v_mfma_f32_16x16x32_bf16 v[82:85], v[200:203], v[224:227], v[82:85]
	v_mfma_f32_16x16x32_bf16 v[70:73], v[190:193], v[232:235], v[70:73]
	v_mfma_f32_16x16x32_bf16 v[66:69], v[200:203], v[232:235], v[66:69]
	v_mfma_f32_16x16x32_bf16 v[118:121], v[194:197], v[212:215], v[118:121]
	v_mfma_f32_16x16x32_bf16 v[114:117], v[204:207], v[212:215], v[114:117]
	v_mfma_f32_16x16x32_bf16 v[102:105], v[194:197], v[220:223], v[102:105]
	v_mfma_f32_16x16x32_bf16 v[98:101], v[204:207], v[220:223], v[98:101]
	v_mfma_f32_16x16x32_bf16 v[86:89], v[194:197], v[228:231], v[86:89]
	v_mfma_f32_16x16x32_bf16 v[82:85], v[204:207], v[228:231], v[82:85]
	v_mfma_f32_16x16x32_bf16 v[70:73], v[194:197], v[236:239], v[70:73]
	v_mfma_f32_16x16x32_bf16 v[66:69], v[204:207], v[236:239], v[66:69]
	s_setprio 0
	s_barrier
	s_add_i32 s36, s38, s29
	s_add_i32 m0, s36, 0xffffff80
	ds_read_b128 v[208:211], v183 offset:49152
	ds_read_b128 v[212:215], v183 offset:50176
	ds_read_b128 v[216:219], v183 offset:51200
	ds_read_b128 v[220:223], v183 offset:52224
	ds_read_b128 v[224:227], v183 offset:53248
	ds_read_b128 v[228:231], v183 offset:54272
	ds_read_b128 v[232:235], v183 offset:55296
	ds_read_b128 v[236:239], v183 offset:56320
	global_load_lds_dwordx4 v132, s[34:35] offset:128
	s_add_i32 m0, s36, 0x1f80
	s_add_i32 s36, s64, s29
	global_load_lds_dwordx4 v136, s[34:35] offset:128
	s_add_u32 s34, s34, 0x80080
	s_addc_u32 s35, s35, 0
	s_mov_b32 m0, s36
	s_nop 0
	global_load_lds_dwordx4 v132, s[34:35]
	s_add_i32 m0, s36, 0x2000
	s_nop 0
	global_load_lds_dwordx4 v136, s[34:35]
	s_add_i32 m0, s46, 0xffffff80
	s_nop 0
	global_load_lds_dwordx4 v130, s[98:99] offset:128
	s_add_i32 m0, s47, 0xffffff80
	s_nop 0
	global_load_lds_dwordx4 v134, s[98:99] offset:128
	s_waitcnt vmcnt(8)
	s_waitcnt lgkmcnt(0)
	s_barrier
	s_setprio 1
	s_waitcnt lgkmcnt(0)
	v_mfma_f32_16x16x32_bf16 v[62:65], v[148:151], v[208:211], v[62:65]
	v_mfma_f32_16x16x32_bf16 v[50:53], v[156:159], v[208:211], v[50:53]
	v_mfma_f32_16x16x32_bf16 v[38:41], v[148:151], v[216:219], v[38:41]
	v_mfma_f32_16x16x32_bf16 v[34:37], v[156:159], v[216:219], v[34:37]
	v_mfma_f32_16x16x32_bf16 v[22:25], v[148:151], v[224:227], v[22:25]
	v_mfma_f32_16x16x32_bf16 v[18:21], v[156:159], v[224:227], v[18:21]
	v_mfma_f32_16x16x32_bf16 v[6:9], v[148:151], v[232:235], v[6:9]
	v_mfma_f32_16x16x32_bf16 v[2:5], v[156:159], v[232:235], v[2:5]
	v_mfma_f32_16x16x32_bf16 v[62:65], v[152:155], v[212:215], v[62:65]
	v_mfma_f32_16x16x32_bf16 v[50:53], v[160:163], v[212:215], v[50:53]
	v_mfma_f32_16x16x32_bf16 v[38:41], v[152:155], v[220:223], v[38:41]
	v_mfma_f32_16x16x32_bf16 v[34:37], v[160:163], v[220:223], v[34:37]
	v_mfma_f32_16x16x32_bf16 v[22:25], v[152:155], v[228:231], v[22:25]
	v_mfma_f32_16x16x32_bf16 v[18:21], v[160:163], v[228:231], v[18:21]
	v_mfma_f32_16x16x32_bf16 v[6:9], v[152:155], v[236:239], v[6:9]
	v_mfma_f32_16x16x32_bf16 v[2:5], v[160:163], v[236:239], v[2:5]
	s_setprio 0
	s_setprio 1
	v_mfma_f32_16x16x32_bf16 v[58:61], v[190:193], v[208:211], v[58:61]
	v_mfma_f32_16x16x32_bf16 v[54:57], v[200:203], v[208:211], v[54:57]
	v_mfma_f32_16x16x32_bf16 v[46:49], v[190:193], v[216:219], v[46:49]
	v_mfma_f32_16x16x32_bf16 v[42:45], v[200:203], v[216:219], v[42:45]
	v_mfma_f32_16x16x32_bf16 v[30:33], v[190:193], v[224:227], v[30:33]
	v_mfma_f32_16x16x32_bf16 v[26:29], v[200:203], v[224:227], v[26:29]
	v_mfma_f32_16x16x32_bf16 v[14:17], v[190:193], v[232:235], v[14:17]
	v_mfma_f32_16x16x32_bf16 v[10:13], v[200:203], v[232:235], v[10:13]
	v_mfma_f32_16x16x32_bf16 v[58:61], v[194:197], v[212:215], v[58:61]
	v_mfma_f32_16x16x32_bf16 v[54:57], v[204:207], v[212:215], v[54:57]
	v_mfma_f32_16x16x32_bf16 v[46:49], v[194:197], v[220:223], v[46:49]
	v_mfma_f32_16x16x32_bf16 v[42:45], v[204:207], v[220:223], v[42:45]
	v_mfma_f32_16x16x32_bf16 v[30:33], v[194:197], v[228:231], v[30:33]
	v_mfma_f32_16x16x32_bf16 v[26:29], v[204:207], v[228:231], v[26:29]
	v_mfma_f32_16x16x32_bf16 v[14:17], v[194:197], v[236:239], v[14:17]
	v_mfma_f32_16x16x32_bf16 v[10:13], v[204:207], v[236:239], v[10:13]
	s_setprio 0
	s_add_i32 s33, s33, 2
	s_add_u32 s10, s10, 0x100
	s_addc_u32 s11, s11, 0
	s_add_u32 s14, s14, 0x100
	s_addc_u32 s27, s27, 0
	s_cmp_gt_u32 s33, 29
	s_barrier
	s_cbranch_scc0 .LBB0_247
	s_and_b64 vcc, exec, s[20:21]
	s_cbranch_vccz .LBB0_251
	s_barrier
	v_lshl_add_u32 v148, s26, 8, v177
	s_cmp_gt_i32 s28, 11
	s_mov_b64 s[10:11], -1
	s_cbranch_scc1 .LBB0_252

; #define PG8_STAGE(bufoff, gbase, voff) do { _Pragma("unroll") for (int _i = 0; _i < 2; ++_i) \
;         __builtin_amdgcn_global_load_lds((const unsigned*)((const char*)(gbase) + (voff)[_i]), (LAS unsigned*)(lds + (bufoff) + ldsw + _i * 8192), 16, 0, 0); } while (0)
; #define PG8_LDA(dst, b, h) do { if constexpr (F8) { _Pragma("unroll") for (int m = 0; m < 4; ++m) dst##8[m] = PG8_LD8(lds, PG8_SA(b, h) + aoff + m * 2048); } \
;         else { _Pragma("unroll") for (int m = 0; m < 4; ++m) _Pragma("unroll") for (int k = 0; k < 2; ++k) dst[m][k] = *(const LAS bf16x8*)(lds + PG8_SA(b, h) + aoff + m * 2048 + k * 1024); } } while (0)
; #define PG8_LDB(dst, b, h) do { if constexpr (F8) { _Pragma("unroll") for (int n = 0; n < 2; ++n) dst##8[n] = PG8_LD8(ldsB, PG8_SBR(b, h) + boff + n * 2048); } \
;         else { _Pragma("unroll") for (int n = 0; n < 2; ++n) _Pragma("unroll") for (int k = 0; k < 2; ++k) dst[n][k] = *(const LAS bf16x8*)(ldsB + PG8_SBR(b, h) + boff + n * 2048 + k * 1024); } } while (0)
; #define PG8_WAIT_V(n) asm volatile("s_waitcnt vmcnt(" #n ")" ::: "memory")
; #define PG8_WAIT_L(n) asm volatile("s_waitcnt lgkmcnt(" #n ")" ::: "memory")
; #define PG8_BAR __builtin_amdgcn_s_barrier()
; #define PG8_SCHED __builtin_amdgcn_sched_barrier(0)
; template <bool GATHER, bool F8, class Epi, class Sched>
; __device__ __forceinline__ void gemm_phase(LAS unsigned char* lds, const int nt, const unsigned lda, const unsigned ldb, const Sched& S, const Epi& E) {
;     ...
;             PG8_LDB(B0, 0, 0); PG8_LDB(B1, 0, 1); PG8_SCHED; PG8_LDA(At, 0, 0); PG8_STAGE(PG8_SA(1, 1), a1 + hA, vA1);
;             PG8_WAIT_V(8); PG8_WAIT_L(0); PG8_BAR; PG8_MMA(0, 0, At, B0); PG8_MMA(0, 1, At, B1); PG8_BAR; PG8_SCHED;
;             PG8_LDA(At, 0, 1); PG8_STAGE(PG8_SB(0, 0), b2, voffB); PG8_STAGE(PG8_SB(0, 1), b2 + hB, voffB); PG8_STAGE(PG8_SA(0, 0), a2, w0);
;             PG8_WAIT_V(8); PG8_WAIT_L(0); PG8_BAR; PG8_MMA(1, 0, At, B0); PG8_MMA(1, 1, At, B1); PG8_BAR; PG8_SCHED;
.LBB0_387:
	ds_read_b128 v[18:21], v1
	ds_read_b128 v[22:25], v1 offset:1024
	ds_read_b128 v[26:29], v1 offset:2048
	ds_read_b128 v[30:33], v1 offset:3072
	ds_read_b128 v[2:5], v1 offset:16384
	ds_read_b128 v[6:9], v1 offset:17408
	ds_read_b128 v[10:13], v1 offset:18432
	ds_read_b128 v[14:17], v1 offset:19456
	s_add_u32 s26, s24, 0xfffc0080
	s_addc_u32 s27, s25, -1
	s_cmp_eq_u32 s55, 12
	s_cselect_b32 s29, s1, s27
	s_cselect_b32 s28, s0, s26
	s_cselect_b32 s27, s21, s54
	s_cselect_b32 s26, s20, s30
	s_add_i32 m0, s23, 0xc000
	ds_read_b128 v[180:183], v191
	ds_read_b128 v[184:187], v191 offset:1024
	ds_read_b128 v[200:203], v191 offset:2048
	ds_read_b128 v[204:207], v191 offset:3072
	ds_read_b128 v[208:211], v191 offset:4096
	ds_read_b128 v[212:215], v191 offset:5120
	ds_read_b128 v[216:219], v191 offset:6144
	ds_read_b128 v[220:223], v191 offset:7168
	global_load_lds_dwordx4 v172, s[24:25]
	s_add_i32 m0, s23, 0xe000
	s_nop 0
	global_load_lds_dwordx4 v174, s[24:25]
	s_waitcnt vmcnt(8)
	s_waitcnt lgkmcnt(0)
	s_barrier
	s_setprio 1
	s_waitcnt lgkmcnt(0)
	v_mfma_scale_f32_16x16x128_f8f6f4 v[158:161], v[18:25], v[180:187], v[158:161], v192, v192 op_sel_hi:[0,0,0]
	v_mfma_scale_f32_16x16x128_f8f6f4 v[150:153], v[26:33], v[180:187], v[150:153], v192, v192 op_sel_hi:[0,0,0]
	v_mfma_scale_f32_16x16x128_f8f6f4 v[142:145], v[18:25], v[200:207], v[142:145], v192, v192 op_sel_hi:[0,0,0]
	v_mfma_scale_f32_16x16x128_f8f6f4 v[134:137], v[26:33], v[200:207], v[134:137], v192, v192 op_sel_hi:[0,0,0]
	v_mfma_scale_f32_16x16x128_f8f6f4 v[126:129], v[18:25], v[208:215], v[126:129], v192, v192 op_sel_hi:[0,0,0]
	v_mfma_scale_f32_16x16x128_f8f6f4 v[118:121], v[26:33], v[208:215], v[118:121], v192, v192 op_sel_hi:[0,0,0]
	v_mfma_scale_f32_16x16x128_f8f6f4 v[110:113], v[18:25], v[216:223], v[110:113], v192, v192 op_sel_hi:[0,0,0]
	v_mfma_scale_f32_16x16x128_f8f6f4 v[102:105], v[26:33], v[216:223], v[102:105], v192, v192 op_sel_hi:[0,0,0]
	s_setprio 0
	s_setprio 1
	v_mfma_scale_f32_16x16x128_f8f6f4 v[154:157], v[2:9], v[180:187], v[154:157], v192, v192 op_sel_hi:[0,0,0]
	v_mfma_scale_f32_16x16x128_f8f6f4 v[146:149], v[10:17], v[180:187], v[146:149], v192, v192 op_sel_hi:[0,0,0]
	v_mfma_scale_f32_16x16x128_f8f6f4 v[138:141], v[2:9], v[200:207], v[138:141], v192, v192 op_sel_hi:[0,0,0]
	v_mfma_scale_f32_16x16x128_f8f6f4 v[130:133], v[10:17], v[200:207], v[130:133], v192, v192 op_sel_hi:[0,0,0]
	v_mfma_scale_f32_16x16x128_f8f6f4 v[122:125], v[2:9], v[208:215], v[122:125], v192, v192 op_sel_hi:[0,0,0]
	v_mfma_scale_f32_16x16x128_f8f6f4 v[114:117], v[10:17], v[208:215], v[114:117], v192, v192 op_sel_hi:[0,0,0]
	v_mfma_scale_f32_16x16x128_f8f6f4 v[106:109], v[2:9], v[216:223], v[106:109], v192, v192 op_sel_hi:[0,0,0]
	v_mfma_scale_f32_16x16x128_f8f6f4 v[98:101], v[10:17], v[216:223], v[98:101], v192, v192 op_sel_hi:[0,0,0]
	s_setprio 0
	s_barrier
	s_mov_b32 m0, s38
	s_add_u32 s56, s26, 0x40000
	ds_read_b128 v[200:203], v191 offset:16384
	ds_read_b128 v[204:207], v191 offset:17408
	ds_read_b128 v[208:211], v191 offset:18432
	ds_read_b128 v[212:215], v191 offset:19456
	ds_read_b128 v[216:219], v191 offset:20480
	ds_read_b128 v[220:223], v191 offset:21504
	ds_read_b128 v[224:227], v191 offset:22528
	ds_read_b128 v[228:231], v191 offset:23552
	global_load_lds_dwordx4 v166, s[26:27]
	s_mov_b32 m0, s39
	s_addc_u32 s57, s27, 0
	global_load_lds_dwordx4 v162, s[26:27]
	s_mov_b32 m0, s40
	s_nop 0
	global_load_lds_dwordx4 v166, s[56:57]
	s_mov_b32 m0, s41
	s_nop 0
	global_load_lds_dwordx4 v162, s[56:57]
	s_mov_b32 m0, s23
	s_nop 0
	s_mov_b64 s[98:99], s[28:29]
	global_load_lds_dwordx4 v168, s[28:29]
	s_mov_b32 m0, s42
	s_nop 0
	global_load_lds_dwordx4 v164, s[28:29]
	s_waitcnt vmcnt(8)
	s_waitcnt lgkmcnt(0)
	s_barrier
	s_setprio 1
	s_waitcnt lgkmcnt(0)
	v_mfma_scale_f32_16x16x128_f8f6f4 v[86:89], v[18:25], v[200:207], v[86:89], v192, v192 op_sel_hi:[0,0,0]
	v_mfma_scale_f32_16x16x128_f8f6f4 v[78:81], v[26:33], v[200:207], v[78:81], v192, v192 op_sel_hi:[0,0,0]
	v_mfma_scale_f32_16x16x128_f8f6f4 v[70:73], v[18:25], v[208:215], v[70:73], v192, v192 op_sel_hi:[0,0,0]
	v_mfma_scale_f32_16x16x128_f8f6f4 v[62:65], v[26:33], v[208:215], v[62:65], v192, v192 op_sel_hi:[0,0,0]
	v_mfma_scale_f32_16x16x128_f8f6f4 v[54:57], v[18:25], v[216:223], v[54:57], v192, v192 op_sel_hi:[0,0,0]
	v_mfma_scale_f32_16x16x128_f8f6f4 v[46:49], v[26:33], v[216:223], v[46:49], v192, v192 op_sel_hi:[0,0,0]
	v_mfma_scale_f32_16x16x128_f8f6f4 v[38:41], v[18:25], v[224:231], v[38:41], v192, v192 op_sel_hi:[0,0,0]
	v_mfma_scale_f32_16x16x128_f8f6f4 v[34:37], v[26:33], v[224:231], v[34:37], v192, v192 op_sel_hi:[0,0,0]
	s_setprio 0
	s_setprio 1
	v_mfma_scale_f32_16x16x128_f8f6f4 v[94:97], v[2:9], v[200:207], v[94:97], v192, v192 op_sel_hi:[0,0,0]
	v_mfma_scale_f32_16x16x128_f8f6f4 v[90:93], v[10:17], v[200:207], v[90:93], v192, v192 op_sel_hi:[0,0,0]
	v_mfma_scale_f32_16x16x128_f8f6f4 v[82:85], v[2:9], v[208:215], v[82:85], v192, v192 op_sel_hi:[0,0,0]
	v_mfma_scale_f32_16x16x128_f8f6f4 v[74:77], v[10:17], v[208:215], v[74:77], v192, v192 op_sel_hi:[0,0,0]
	v_mfma_scale_f32_16x16x128_f8f6f4 v[66:69], v[2:9], v[216:223], v[66:69], v192, v192 op_sel_hi:[0,0,0]
	v_mfma_scale_f32_16x16x128_f8f6f4 v[58:61], v[10:17], v[216:223], v[58:61], v192, v192 op_sel_hi:[0,0,0]
	v_mfma_scale_f32_16x16x128_f8f6f4 v[50:53], v[2:9], v[224:231], v[50:53], v192, v192 op_sel_hi:[0,0,0]
	v_mfma_scale_f32_16x16x128_f8f6f4 v[42:45], v[10:17], v[224:231], v[42:45], v192, v192 op_sel_hi:[0,0,0]
	s_setprio 0
	s_barrier
; #define PG8_STAGE(bufoff, gbase, voff) do { _Pragma("unroll") for (int _i = 0; _i < 2; ++_i) \
;         __builtin_amdgcn_global_load_lds((const unsigned*)((const char*)(gbase) + (voff)[_i]), (LAS unsigned*)(lds + (bufoff) + ldsw + _i * 8192), 16, 0, 0); } while (0)
; #define PG8_LDA(dst, b, h) do { if constexpr (F8) { _Pragma("unroll") for (int m = 0; m < 4; ++m) dst##8[m] = PG8_LD8(lds, PG8_SA(b, h) + aoff + m * 2048); } \
;         else { _Pragma("unroll") for (int m = 0; m < 4; ++m) _Pragma("unroll") for (int k = 0; k < 2; ++k) dst[m][k] = *(const LAS bf16x8*)(lds + PG8_SA(b, h) + aoff + m * 2048 + k * 1024); } } while (0)
; #define PG8_LDB(dst, b, h) do { if constexpr (F8) { _Pragma("unroll") for (int n = 0; n < 2; ++n) dst##8[n] = PG8_LD8(ldsB, PG8_SBR(b, h) + boff + n * 2048); } \
;         else { _Pragma("unroll") for (int n = 0; n < 2; ++n) _Pragma("unroll") for (int k = 0; k < 2; ++k) dst[n][k] = *(const LAS bf16x8*)(ldsB + PG8_SBR(b, h) + boff + n * 2048 + k * 1024); } } while (0)
; #define PG8_WAIT_V(n) asm volatile("s_waitcnt vmcnt(" #n ")" ::: "memory")
; #define PG8_WAIT_L(n) asm volatile("s_waitcnt lgkmcnt(" #n ")" ::: "memory")
; #define PG8_BAR __builtin_amdgcn_s_barrier()
; #define PG8_SCHED __builtin_amdgcn_sched_barrier(0)
; template <bool GATHER, bool F8, class Epi, class Sched>
; __device__ __forceinline__ void gemm_phase(LAS unsigned char* lds, const int nt, const unsigned lda, const unsigned ldb, const Sched& S, const Epi& E) {
;     ...
;             PG8_LDB(B0, 1, 0); PG8_LDB(B1, 1, 1); PG8_SCHED; PG8_LDA(At, 1, 0); PG8_STAGE(PG8_SA(0, 1), a2 + hA, w1);
;             PG8_WAIT_V(8); PG8_WAIT_L(0); PG8_BAR; PG8_MMA(0, 0, At, B0); PG8_MMA(0, 1, At, B1); PG8_BAR; PG8_SCHED;
;             PG8_LDA(At, 1, 1); PG8_STAGE(PG8_SB(1, 0), b3, voffB); PG8_STAGE(PG8_SB(1, 1), b3 + hB, voffB); PG8_STAGE(PG8_SA(1, 0), a3, w0);
;             PG8_WAIT_V(8); PG8_WAIT_L(0); PG8_BAR; PG8_MMA(1, 0, At, B0); PG8_MMA(1, 1, At, B1); PG8_BAR; PG8_SCHED;
;         }
;         if (wr == 0) PG8_BAR;
	ds_read_b128 v[2:5], v1 offset:32768
	ds_read_b128 v[6:9], v1 offset:33792
	ds_read_b128 v[10:13], v1 offset:34816
	ds_read_b128 v[14:17], v1 offset:35840
	ds_read_b128 v[18:21], v1 offset:49152
	ds_read_b128 v[22:25], v1 offset:50176
	ds_read_b128 v[26:29], v1 offset:51200
	ds_read_b128 v[30:33], v1 offset:52224
	s_add_u32 s28, s28, 0x40000
	s_addc_u32 s29, s29, 0
	s_mov_b32 m0, s43
	ds_read_b128 v[200:203], v191 offset:32768
	ds_read_b128 v[204:207], v191 offset:33792
	ds_read_b128 v[208:211], v191 offset:34816
	ds_read_b128 v[212:215], v191 offset:35840
	ds_read_b128 v[216:219], v191 offset:36864
	ds_read_b128 v[220:223], v191 offset:37888
	ds_read_b128 v[224:227], v191 offset:38912
	ds_read_b128 v[228:231], v191 offset:39936
	global_load_lds_dwordx4 v168, s[28:29]
	s_mov_b32 m0, s44
	s_nop 0
	global_load_lds_dwordx4 v164, s[28:29]
	s_waitcnt vmcnt(8)
	s_waitcnt lgkmcnt(0)
	s_barrier
	s_setprio 1
	s_waitcnt lgkmcnt(0)
	v_mfma_scale_f32_16x16x128_f8f6f4 v[158:161], v[2:9], v[200:207], v[158:161], v192, v192 op_sel_hi:[0,0,0]
	v_mfma_scale_f32_16x16x128_f8f6f4 v[150:153], v[10:17], v[200:207], v[150:153], v192, v192 op_sel_hi:[0,0,0]
	v_mfma_scale_f32_16x16x128_f8f6f4 v[142:145], v[2:9], v[208:215], v[142:145], v192, v192 op_sel_hi:[0,0,0]
	v_mfma_scale_f32_16x16x128_f8f6f4 v[134:137], v[10:17], v[208:215], v[134:137], v192, v192 op_sel_hi:[0,0,0]
	v_mfma_scale_f32_16x16x128_f8f6f4 v[126:129], v[2:9], v[216:223], v[126:129], v192, v192 op_sel_hi:[0,0,0]
	v_mfma_scale_f32_16x16x128_f8f6f4 v[118:121], v[10:17], v[216:223], v[118:121], v192, v192 op_sel_hi:[0,0,0]
	v_mfma_scale_f32_16x16x128_f8f6f4 v[110:113], v[2:9], v[224:231], v[110:113], v192, v192 op_sel_hi:[0,0,0]
	v_mfma_scale_f32_16x16x128_f8f6f4 v[102:105], v[10:17], v[224:231], v[102:105], v192, v192 op_sel_hi:[0,0,0]
	s_setprio 0
	s_setprio 1
	v_mfma_scale_f32_16x16x128_f8f6f4 v[154:157], v[18:25], v[200:207], v[154:157], v192, v192 op_sel_hi:[0,0,0]
	v_mfma_scale_f32_16x16x128_f8f6f4 v[146:149], v[26:33], v[200:207], v[146:149], v192, v192 op_sel_hi:[0,0,0]
	v_mfma_scale_f32_16x16x128_f8f6f4 v[138:141], v[18:25], v[208:215], v[138:141], v192, v192 op_sel_hi:[0,0,0]
	v_mfma_scale_f32_16x16x128_f8f6f4 v[130:133], v[26:33], v[208:215], v[130:133], v192, v192 op_sel_hi:[0,0,0]
	v_mfma_scale_f32_16x16x128_f8f6f4 v[122:125], v[18:25], v[216:223], v[122:125], v192, v192 op_sel_hi:[0,0,0]
	v_mfma_scale_f32_16x16x128_f8f6f4 v[114:117], v[26:33], v[216:223], v[114:117], v192, v192 op_sel_hi:[0,0,0]
	v_mfma_scale_f32_16x16x128_f8f6f4 v[106:109], v[18:25], v[224:231], v[106:109], v192, v192 op_sel_hi:[0,0,0]
	v_mfma_scale_f32_16x16x128_f8f6f4 v[98:101], v[26:33], v[224:231], v[98:101], v192, v192 op_sel_hi:[0,0,0]
	s_setprio 0
	s_barrier
	s_add_i32 m0, s45, 0xffffff80
	ds_read_b128 v[200:203], v191 offset:49152
	ds_read_b128 v[204:207], v191 offset:50176
	ds_read_b128 v[208:211], v191 offset:51200
	ds_read_b128 v[212:215], v191 offset:52224
	ds_read_b128 v[216:219], v191 offset:53248
	ds_read_b128 v[220:223], v191 offset:54272
	ds_read_b128 v[224:227], v191 offset:55296
	ds_read_b128 v[228:231], v191 offset:56320
	global_load_lds_dwordx4 v166, s[26:27] offset:128
	s_add_i32 m0, s46, 0xffffff80
	s_nop 0
	global_load_lds_dwordx4 v162, s[26:27] offset:128
	s_add_u32 s26, s26, 0x40080
	s_addc_u32 s27, s27, 0
	s_mov_b32 m0, s49
	s_nop 0
	global_load_lds_dwordx4 v166, s[26:27]
	s_mov_b32 m0, s50
	s_nop 0
	global_load_lds_dwordx4 v162, s[26:27]
	s_add_i32 m0, s47, 0xffffff80
	s_nop 0
	global_load_lds_dwordx4 v168, s[98:99] offset:128
	s_add_i32 m0, s48, 0xffffff80
	s_nop 0
	global_load_lds_dwordx4 v164, s[98:99] offset:128
	s_waitcnt vmcnt(8)
	s_waitcnt lgkmcnt(0)
	s_barrier
	s_setprio 1
	s_waitcnt lgkmcnt(0)
	v_mfma_scale_f32_16x16x128_f8f6f4 v[86:89], v[2:9], v[200:207], v[86:89], v192, v192 op_sel_hi:[0,0,0]
	v_mfma_scale_f32_16x16x128_f8f6f4 v[78:81], v[10:17], v[200:207], v[78:81], v192, v192 op_sel_hi:[0,0,0]
	v_mfma_scale_f32_16x16x128_f8f6f4 v[70:73], v[2:9], v[208:215], v[70:73], v192, v192 op_sel_hi:[0,0,0]
	v_mfma_scale_f32_16x16x128_f8f6f4 v[62:65], v[10:17], v[208:215], v[62:65], v192, v192 op_sel_hi:[0,0,0]
	v_mfma_scale_f32_16x16x128_f8f6f4 v[54:57], v[2:9], v[216:223], v[54:57], v192, v192 op_sel_hi:[0,0,0]
	v_mfma_scale_f32_16x16x128_f8f6f4 v[46:49], v[10:17], v[216:223], v[46:49], v192, v192 op_sel_hi:[0,0,0]
	v_mfma_scale_f32_16x16x128_f8f6f4 v[38:41], v[2:9], v[224:231], v[38:41], v192, v192 op_sel_hi:[0,0,0]
	v_mfma_scale_f32_16x16x128_f8f6f4 v[34:37], v[10:17], v[224:231], v[34:37], v192, v192 op_sel_hi:[0,0,0]
	s_setprio 0
	s_setprio 1
	v_mfma_scale_f32_16x16x128_f8f6f4 v[94:97], v[18:25], v[200:207], v[94:97], v192, v192 op_sel_hi:[0,0,0]
	v_mfma_scale_f32_16x16x128_f8f6f4 v[90:93], v[26:33], v[200:207], v[90:93], v192, v192 op_sel_hi:[0,0,0]
	v_mfma_scale_f32_16x16x128_f8f6f4 v[82:85], v[18:25], v[208:215], v[82:85], v192, v192 op_sel_hi:[0,0,0]
	v_mfma_scale_f32_16x16x128_f8f6f4 v[74:77], v[26:33], v[208:215], v[74:77], v192, v192 op_sel_hi:[0,0,0]
	v_mfma_scale_f32_16x16x128_f8f6f4 v[66:69], v[18:25], v[216:223], v[66:69], v192, v192 op_sel_hi:[0,0,0]
	v_mfma_scale_f32_16x16x128_f8f6f4 v[58:61], v[26:33], v[216:223], v[58:61], v192, v192 op_sel_hi:[0,0,0]
	v_mfma_scale_f32_16x16x128_f8f6f4 v[50:53], v[18:25], v[224:231], v[50:53], v192, v192 op_sel_hi:[0,0,0]
	v_mfma_scale_f32_16x16x128_f8f6f4 v[42:45], v[26:33], v[224:231], v[42:45], v192, v192 op_sel_hi:[0,0,0]
	s_setprio 0
	s_add_i32 s55, s55, 2
	s_add_u32 s24, s24, 0x100
	s_addc_u32 s25, s25, 0
	s_add_u32 s30, s30, 0x100
	s_addc_u32 s54, s54, 0
	s_cmp_gt_u32 s55, 13
	s_barrier
	s_cbranch_scc0 .LBB0_387
	s_and_b64 vcc, exec, s[10:11]
	s_cbranch_vccz .LBB0_390
	s_barrier

; #define PG8_STAGE(bufoff, gbase, voff) do { _Pragma("unroll") for (int _i = 0; _i < 2; ++_i) \
;         __builtin_amdgcn_global_load_lds((const unsigned*)((const char*)(gbase) + (voff)[_i]), (LAS unsigned*)(lds + (bufoff) + ldsw + _i * 8192), 16, 0, 0); } while (0)
; #define PG8_LDA(dst, b, h) do { if constexpr (F8) { _Pragma("unroll") for (int m = 0; m < 4; ++m) dst##8[m] = PG8_LD8(lds, PG8_SA(b, h) + aoff + m * 2048); } \
;         else { _Pragma("unroll") for (int m = 0; m < 4; ++m) _Pragma("unroll") for (int k = 0; k < 2; ++k) dst[m][k] = *(const LAS bf16x8*)(lds + PG8_SA(b, h) + aoff + m * 2048 + k * 1024); } } while (0)
; #define PG8_WAIT_V(n) asm volatile("s_waitcnt vmcnt(" #n ")" ::: "memory")
; #define PG8_WAIT_L(n) asm volatile("s_waitcnt lgkmcnt(" #n ")" ::: "memory")
; #define PG8_BAR __builtin_amdgcn_s_barrier()
; #define PG8_SCHED __builtin_amdgcn_sched_barrier(0)
; template <bool GATHER, bool F8, class Epi, class Sched>
; __device__ __forceinline__ void gemm_phase(LAS unsigned char* lds, const int nt, const unsigned lda, const unsigned ldb, const Sched& S, const Epi& E) {
;     ...
;         for (int t = 0; t < nt; t += 2) {
;             const bool last = (t == nt - 2);
;             const char* a1 = cA + (size_t)(t + 1) * kstep;
;             const char* a2 = last ? nA : cA + (size_t)(t + 2) * kstep; const char* b2 = last ? nB : cB + (size_t)(t + 2) * kstep;
;             const char* a3 = a2 + kstep; const char* b3 = b2 + kstep;
;             unsigned w0[2], w1[2];
;             if constexpr (GATHER) {
; #pragma unroll
;                 for (int i = 0; i < 2; ++i) { w0[i] = last ? vN0[i] : vA0[i]; w1[i] = last ? vN1[i] : vA1[i]; }
;             } else {
; #pragma unroll
;                 for (int i = 0; i < 2; ++i) { w0[i] = voffA[i]; w1[i] = voffA[i]; }
;             }
;             PG8_LDB(B0, 0, 0); PG8_LDB(B1, 0, 1); PG8_SCHED; PG8_LDA(At, 0, 0); PG8_STAGE(PG8_SA(1, 1), a1 + hA, vA1);
;             PG8_WAIT_V(8); PG8_WAIT_L(0); PG8_BAR; PG8_MMA(0, 0, At, B0); PG8_MMA(0, 1, At, B1); PG8_BAR; PG8_SCHED;
;             PG8_LDA(At, 0, 1); PG8_STAGE(PG8_SB(0, 0), b2, voffB); PG8_STAGE(PG8_SB(0, 1), b2 + hB, voffB); PG8_STAGE(PG8_SA(0, 0), a2, w0);
;             PG8_WAIT_V(8); PG8_WAIT_L(0); PG8_BAR; PG8_MMA(1, 0, At, B0); PG8_MMA(1, 1, At, B1); PG8_BAR; PG8_SCHED;
.LBB0_891:
	v_add_u32_e32 v3, s47, v199
	ds_read_b128 v[38:41], v3
	ds_read_b128 v[42:45], v3 offset:1024
	ds_read_b128 v[70:73], v3 offset:2048
	ds_read_b128 v[74:77], v3 offset:3072
	v_add_u32_e32 v3, s48, v199
	ds_read_b128 v[102:105], v3
	ds_read_b128 v[106:109], v3 offset:1024
	ds_read_b128 v[134:137], v3 offset:2048
	ds_read_b128 v[138:141], v3 offset:3072
	s_add_u32 s28, s26, 0xfff80080
	s_addc_u32 s29, s27, -1
	s_cmp_eq_u32 s52, 12
	s_cselect_b32 s31, s1, s29
	s_cselect_b32 s30, s0, s28
	s_cselect_b32 s29, s23, s34
	s_cselect_b32 s28, s22, s25
	s_add_i32 m0, s40, 0xc000
	ds_read_b128 v[158:161], v217
	ds_read_b128 v[162:165], v217 offset:1024
	ds_read_b128 v[174:177], v217 offset:2048
	ds_read_b128 v[178:181], v217 offset:3072
	ds_read_b128 v[182:185], v217 offset:4096
	ds_read_b128 v[186:189], v217 offset:5120
	ds_read_b128 v[190:193], v217 offset:6144
	ds_read_b128 v[194:197], v217 offset:7168
	global_load_lds_dwordx4 v208, s[26:27]
	s_add_i32 m0, s40, 0xe000
	s_nop 0
	global_load_lds_dwordx4 v210, s[26:27]
	s_waitcnt vmcnt(8)
	s_waitcnt lgkmcnt(0)
	s_barrier
	s_setprio 1
	s_waitcnt lgkmcnt(0)
	v_mfma_f32_16x16x32_bf16 v[66:69], v[38:41], v[158:161], v[66:69]
	v_mfma_f32_16x16x32_bf16 v[62:65], v[70:73], v[158:161], v[62:65]
	v_mfma_f32_16x16x32_bf16 v[98:101], v[38:41], v[174:177], v[98:101]
	v_mfma_f32_16x16x32_bf16 v[94:97], v[70:73], v[174:177], v[94:97]
	v_mfma_f32_16x16x32_bf16 v[122:125], v[38:41], v[182:185], v[122:125]
	v_mfma_f32_16x16x32_bf16 v[118:121], v[70:73], v[182:185], v[118:121]
	v_mfma_f32_16x16x32_bf16 v[130:133], v[38:41], v[190:193], v[130:133]
	v_mfma_f32_16x16x32_bf16 v[126:129], v[70:73], v[190:193], v[126:129]
	v_mfma_f32_16x16x32_bf16 v[66:69], v[42:45], v[162:165], v[66:69]
	v_mfma_f32_16x16x32_bf16 v[62:65], v[74:77], v[162:165], v[62:65]
	v_mfma_f32_16x16x32_bf16 v[98:101], v[42:45], v[178:181], v[98:101]
	v_mfma_f32_16x16x32_bf16 v[94:97], v[74:77], v[178:181], v[94:97]
	v_mfma_f32_16x16x32_bf16 v[122:125], v[42:45], v[186:189], v[122:125]
	v_mfma_f32_16x16x32_bf16 v[118:121], v[74:77], v[186:189], v[118:121]
	v_mfma_f32_16x16x32_bf16 v[130:133], v[42:45], v[194:197], v[130:133]
	v_mfma_f32_16x16x32_bf16 v[126:129], v[74:77], v[194:197], v[126:129]
	s_setprio 0
	s_setprio 1
	v_mfma_f32_16x16x32_bf16 v[170:173], v[102:105], v[158:161], v[170:173]
	v_mfma_f32_16x16x32_bf16 v[154:157], v[102:105], v[174:177], v[154:157]
	v_mfma_f32_16x16x32_bf16 v[150:153], v[134:137], v[174:177], v[150:153]
	v_mfma_f32_16x16x32_bf16 v[146:149], v[102:105], v[182:185], v[146:149]
	v_mfma_f32_16x16x32_bf16 v[142:145], v[134:137], v[182:185], v[142:145]
	v_mfma_f32_16x16x32_bf16 v[114:117], v[102:105], v[190:193], v[114:117]
	v_mfma_f32_16x16x32_bf16 v[110:113], v[134:137], v[190:193], v[110:113]
	v_mfma_f32_16x16x32_bf16 v[170:173], v[106:109], v[162:165], v[170:173]
	v_mfma_f32_16x16x32_bf16 v[158:161], v[134:137], v[158:161], v[166:169]
	v_mfma_f32_16x16x32_bf16 v[154:157], v[106:109], v[178:181], v[154:157]
	v_mfma_f32_16x16x32_bf16 v[150:153], v[138:141], v[178:181], v[150:153]
	v_mfma_f32_16x16x32_bf16 v[146:149], v[106:109], v[186:189], v[146:149]
	v_mfma_f32_16x16x32_bf16 v[142:145], v[138:141], v[186:189], v[142:145]
	v_mfma_f32_16x16x32_bf16 v[114:117], v[106:109], v[194:197], v[114:117]
	v_mfma_f32_16x16x32_bf16 v[110:113], v[138:141], v[194:197], v[110:113]
	v_mfma_f32_16x16x32_bf16 v[158:161], v[138:141], v[162:165], v[158:161]
	s_setprio 0
	s_barrier
	s_add_i32 s53, s47, s39
	s_mov_b32 m0, s53
	ds_read_b128 v[162:165], v217 offset:16384
	ds_read_b128 v[166:169], v217 offset:17408
	ds_read_b128 v[174:177], v217 offset:18432
	ds_read_b128 v[178:181], v217 offset:19456
	ds_read_b128 v[182:185], v217 offset:20480
	ds_read_b128 v[186:189], v217 offset:21504
	ds_read_b128 v[190:193], v217 offset:22528
	ds_read_b128 v[194:197], v217 offset:23552
	global_load_lds_dwordx4 v202, s[28:29]
	s_add_i32 m0, s53, 0x2000
	s_add_u32 s54, s28, 0x80000
	s_addc_u32 s55, s29, 0
	s_add_i32 s53, s48, s39
	global_load_lds_dwordx4 v206, s[28:29]
	s_mov_b32 m0, s53
	s_nop 0
	global_load_lds_dwordx4 v202, s[54:55]
	s_add_i32 m0, s53, 0x2000
	s_nop 0
	global_load_lds_dwordx4 v206, s[54:55]
	s_mov_b32 m0, s40
	s_nop 0
	s_mov_b64 s[98:99], s[30:31]
	global_load_lds_dwordx4 v200, s[30:31]
	s_mov_b32 m0, s41
	s_nop 0
	global_load_lds_dwordx4 v204, s[30:31]
	s_waitcnt vmcnt(8)
	s_waitcnt lgkmcnt(0)
	s_barrier
	s_setprio 1
	s_waitcnt lgkmcnt(0)
	v_mfma_f32_16x16x32_bf16 v[90:93], v[38:41], v[162:165], v[90:93]
	v_mfma_f32_16x16x32_bf16 v[86:89], v[70:73], v[162:165], v[86:89]
	v_mfma_f32_16x16x32_bf16 v[58:61], v[38:41], v[174:177], v[58:61]
	v_mfma_f32_16x16x32_bf16 v[54:57], v[70:73], v[174:177], v[54:57]
	v_mfma_f32_16x16x32_bf16 v[34:37], v[38:41], v[182:185], v[34:37]
	v_mfma_f32_16x16x32_bf16 v[30:33], v[70:73], v[182:185], v[30:33]
	v_mfma_f32_16x16x32_bf16 v[18:21], v[38:41], v[190:193], v[18:21]
	v_mfma_f32_16x16x32_bf16 v[14:17], v[70:73], v[190:193], v[14:17]
	v_mfma_f32_16x16x32_bf16 v[90:93], v[42:45], v[166:169], v[90:93]
	v_mfma_f32_16x16x32_bf16 v[86:89], v[74:77], v[166:169], v[86:89]
	v_mfma_f32_16x16x32_bf16 v[58:61], v[42:45], v[178:181], v[58:61]
	v_mfma_f32_16x16x32_bf16 v[54:57], v[74:77], v[178:181], v[54:57]
	v_mfma_f32_16x16x32_bf16 v[34:37], v[42:45], v[186:189], v[34:37]
	v_mfma_f32_16x16x32_bf16 v[30:33], v[74:77], v[186:189], v[30:33]
	v_mfma_f32_16x16x32_bf16 v[18:21], v[42:45], v[194:197], v[18:21]
	v_mfma_f32_16x16x32_bf16 v[14:17], v[74:77], v[194:197], v[14:17]
	s_setprio 0
	s_setprio 1
	v_mfma_f32_16x16x32_bf16 v[46:49], v[102:105], v[174:177], v[46:49]
	v_mfma_f32_16x16x32_bf16 v[50:53], v[134:137], v[174:177], v[50:53]
	v_mfma_f32_16x16x32_bf16 v[22:25], v[102:105], v[182:185], v[22:25]
	v_mfma_f32_16x16x32_bf16 v[26:29], v[134:137], v[182:185], v[26:29]
	v_mfma_f32_16x16x32_bf16 v[4:7], v[102:105], v[190:193], v[6:9]
	v_mfma_f32_16x16x32_bf16 v[8:11], v[134:137], v[190:193], v[10:13]
	v_mfma_f32_16x16x32_bf16 v[38:41], v[102:105], v[162:165], v[78:81]
	v_mfma_f32_16x16x32_bf16 v[42:45], v[134:137], v[162:165], v[82:85]
	v_mfma_f32_16x16x32_bf16 v[46:49], v[106:109], v[178:181], v[46:49]
	v_mfma_f32_16x16x32_bf16 v[50:53], v[138:141], v[178:181], v[50:53]
	v_mfma_f32_16x16x32_bf16 v[22:25], v[106:109], v[186:189], v[22:25]
	v_mfma_f32_16x16x32_bf16 v[26:29], v[138:141], v[186:189], v[26:29]
	v_mfma_f32_16x16x32_bf16 v[4:7], v[106:109], v[194:197], v[4:7]
	v_mfma_f32_16x16x32_bf16 v[10:13], v[138:141], v[194:197], v[8:11]
	v_mfma_f32_16x16x32_bf16 v[38:41], v[106:109], v[166:169], v[38:41]
	v_mfma_f32_16x16x32_bf16 v[42:45], v[138:141], v[166:169], v[42:45]
	s_setprio 0
	s_barrier
; #define PG8_STAGE(bufoff, gbase, voff) do { _Pragma("unroll") for (int _i = 0; _i < 2; ++_i) \
;         __builtin_amdgcn_global_load_lds((const unsigned*)((const char*)(gbase) + (voff)[_i]), (LAS unsigned*)(lds + (bufoff) + ldsw + _i * 8192), 16, 0, 0); } while (0)
; #define PG8_LDA(dst, b, h) do { if constexpr (F8) { _Pragma("unroll") for (int m = 0; m < 4; ++m) dst##8[m] = PG8_LD8(lds, PG8_SA(b, h) + aoff + m * 2048); } \
;         else { _Pragma("unroll") for (int m = 0; m < 4; ++m) _Pragma("unroll") for (int k = 0; k < 2; ++k) dst[m][k] = *(const LAS bf16x8*)(lds + PG8_SA(b, h) + aoff + m * 2048 + k * 1024); } } while (0)
; #define PG8_LDB(dst, b, h) do { if constexpr (F8) { _Pragma("unroll") for (int n = 0; n < 2; ++n) dst##8[n] = PG8_LD8(ldsB, PG8_SBR(b, h) + boff + n * 2048); } \
;         else { _Pragma("unroll") for (int n = 0; n < 2; ++n) _Pragma("unroll") for (int k = 0; k < 2; ++k) dst[n][k] = *(const LAS bf16x8*)(ldsB + PG8_SBR(b, h) + boff + n * 2048 + k * 1024); } } while (0)
; #define PG8_WAIT_V(n) asm volatile("s_waitcnt vmcnt(" #n ")" ::: "memory")
; #define PG8_WAIT_L(n) asm volatile("s_waitcnt lgkmcnt(" #n ")" ::: "memory")
; #define PG8_BAR __builtin_amdgcn_s_barrier()
; #define PG8_SCHED __builtin_amdgcn_sched_barrier(0)
; template <bool GATHER, bool F8, class Epi, class Sched>
; __device__ __forceinline__ void gemm_phase(LAS unsigned char* lds, const int nt, const unsigned lda, const unsigned ldb, const Sched& S, const Epi& E) {
;     ...
;             PG8_LDB(B0, 1, 0); PG8_LDB(B1, 1, 1); PG8_SCHED; PG8_LDA(At, 1, 0); PG8_STAGE(PG8_SA(0, 1), a2 + hA, w1);
;             PG8_WAIT_V(8); PG8_WAIT_L(0); PG8_BAR; PG8_MMA(0, 0, At, B0); PG8_MMA(0, 1, At, B1); PG8_BAR; PG8_SCHED;
;             PG8_LDA(At, 1, 1); PG8_STAGE(PG8_SB(1, 0), b3, voffB); PG8_STAGE(PG8_SB(1, 1), b3 + hB, voffB); PG8_STAGE(PG8_SA(1, 0), a3, w0);
;             PG8_WAIT_V(8); PG8_WAIT_L(0); PG8_BAR; PG8_MMA(1, 0, At, B0); PG8_MMA(1, 1, At, B1); PG8_BAR; PG8_SCHED;
;         }
;         if (wr == 0) PG8_BAR;
	s_add_i32 s53, 0, 0x18000
	v_add_u32_e32 v3, s53, v199
	s_add_i32 s54, 0, 0x1c000
	ds_read_b128 v[70:73], v3
	ds_read_b128 v[74:77], v3 offset:1024
	ds_read_b128 v[78:81], v3 offset:2048
	ds_read_b128 v[82:85], v3 offset:3072
	v_add_u32_e32 v3, s54, v199
	ds_read_b128 v[102:105], v3
	ds_read_b128 v[106:109], v3 offset:1024
	ds_read_b128 v[134:137], v3 offset:2048
	ds_read_b128 v[138:141], v3 offset:3072
	s_add_u32 s30, s30, 0x80000
	s_addc_u32 s31, s31, 0
	s_mov_b32 m0, s42
	ds_read_b128 v[162:165], v217 offset:32768
	ds_read_b128 v[166:169], v217 offset:33792
	ds_read_b128 v[174:177], v217 offset:34816
	ds_read_b128 v[178:181], v217 offset:35840
	ds_read_b128 v[182:185], v217 offset:36864
	ds_read_b128 v[186:189], v217 offset:37888
	ds_read_b128 v[190:193], v217 offset:38912
	ds_read_b128 v[194:197], v217 offset:39936
	global_load_lds_dwordx4 v200, s[30:31]
	s_mov_b32 m0, s43
	s_nop 0
	global_load_lds_dwordx4 v204, s[30:31]
	s_waitcnt vmcnt(8)
	s_waitcnt lgkmcnt(0)
	s_barrier
	s_setprio 1
	s_waitcnt lgkmcnt(0)
	v_mfma_f32_16x16x32_bf16 v[66:69], v[70:73], v[162:165], v[66:69]
	v_mfma_f32_16x16x32_bf16 v[62:65], v[78:81], v[162:165], v[62:65]
	v_mfma_f32_16x16x32_bf16 v[98:101], v[70:73], v[174:177], v[98:101]
	v_mfma_f32_16x16x32_bf16 v[94:97], v[78:81], v[174:177], v[94:97]
	v_mfma_f32_16x16x32_bf16 v[122:125], v[70:73], v[182:185], v[122:125]
	v_mfma_f32_16x16x32_bf16 v[118:121], v[78:81], v[182:185], v[118:121]
	v_mfma_f32_16x16x32_bf16 v[130:133], v[70:73], v[190:193], v[130:133]
	v_mfma_f32_16x16x32_bf16 v[126:129], v[78:81], v[190:193], v[126:129]
	v_mfma_f32_16x16x32_bf16 v[66:69], v[74:77], v[166:169], v[66:69]
	v_mfma_f32_16x16x32_bf16 v[62:65], v[82:85], v[166:169], v[62:65]
	v_mfma_f32_16x16x32_bf16 v[98:101], v[74:77], v[178:181], v[98:101]
	v_mfma_f32_16x16x32_bf16 v[94:97], v[82:85], v[178:181], v[94:97]
	v_mfma_f32_16x16x32_bf16 v[122:125], v[74:77], v[186:189], v[122:125]
	v_mfma_f32_16x16x32_bf16 v[118:121], v[82:85], v[186:189], v[118:121]
	v_mfma_f32_16x16x32_bf16 v[130:133], v[74:77], v[194:197], v[130:133]
	v_mfma_f32_16x16x32_bf16 v[126:129], v[82:85], v[194:197], v[126:129]
	s_setprio 0
	s_setprio 1
	v_mfma_f32_16x16x32_bf16 v[170:173], v[102:105], v[162:165], v[170:173]
	v_mfma_f32_16x16x32_bf16 v[158:161], v[134:137], v[162:165], v[158:161]
	v_mfma_f32_16x16x32_bf16 v[154:157], v[102:105], v[174:177], v[154:157]
	v_mfma_f32_16x16x32_bf16 v[150:153], v[134:137], v[174:177], v[150:153]
	v_mfma_f32_16x16x32_bf16 v[146:149], v[102:105], v[182:185], v[146:149]
	v_mfma_f32_16x16x32_bf16 v[142:145], v[134:137], v[182:185], v[142:145]
	v_mfma_f32_16x16x32_bf16 v[114:117], v[102:105], v[190:193], v[114:117]
	v_mfma_f32_16x16x32_bf16 v[110:113], v[134:137], v[190:193], v[110:113]
	v_mfma_f32_16x16x32_bf16 v[170:173], v[106:109], v[166:169], v[170:173]
	v_mfma_f32_16x16x32_bf16 v[166:169], v[138:141], v[166:169], v[158:161]
	v_mfma_f32_16x16x32_bf16 v[154:157], v[106:109], v[178:181], v[154:157]
	v_mfma_f32_16x16x32_bf16 v[150:153], v[138:141], v[178:181], v[150:153]
	v_mfma_f32_16x16x32_bf16 v[146:149], v[106:109], v[186:189], v[146:149]
	v_mfma_f32_16x16x32_bf16 v[142:145], v[138:141], v[186:189], v[142:145]
	v_mfma_f32_16x16x32_bf16 v[114:117], v[106:109], v[194:197], v[114:117]
	v_mfma_f32_16x16x32_bf16 v[110:113], v[138:141], v[194:197], v[110:113]
	s_setprio 0
	s_barrier
	s_add_i32 s30, s53, s39
	s_add_i32 m0, s30, 0xffffff80
	ds_read_b128 v[158:161], v217 offset:49152
	ds_read_b128 v[162:165], v217 offset:50176
	ds_read_b128 v[174:177], v217 offset:51200
	ds_read_b128 v[178:181], v217 offset:52224
	ds_read_b128 v[182:185], v217 offset:53248
	ds_read_b128 v[186:189], v217 offset:54272
	ds_read_b128 v[190:193], v217 offset:55296
	ds_read_b128 v[194:197], v217 offset:56320
	global_load_lds_dwordx4 v202, s[28:29] offset:128
	s_add_i32 m0, s30, 0x1f80
	s_add_i32 s30, s54, s39
	global_load_lds_dwordx4 v206, s[28:29] offset:128
	s_add_u32 s28, s28, 0x80080
	s_addc_u32 s29, s29, 0
	s_mov_b32 m0, s30
	s_nop 0
	global_load_lds_dwordx4 v202, s[28:29]
	s_add_i32 m0, s30, 0x2000
	s_nop 0
	global_load_lds_dwordx4 v206, s[28:29]
	s_add_i32 m0, s45, 0xffffff80
	s_nop 0
	global_load_lds_dwordx4 v200, s[98:99] offset:128
	s_add_i32 m0, s46, 0xffffff80
	s_nop 0
	global_load_lds_dwordx4 v204, s[98:99] offset:128
	s_waitcnt vmcnt(8)
	s_waitcnt lgkmcnt(0)
	s_barrier
	s_setprio 1
	s_waitcnt lgkmcnt(0)
	v_mfma_f32_16x16x32_bf16 v[90:93], v[70:73], v[158:161], v[90:93]
	v_mfma_f32_16x16x32_bf16 v[86:89], v[78:81], v[158:161], v[86:89]
	v_mfma_f32_16x16x32_bf16 v[58:61], v[70:73], v[174:177], v[58:61]
	v_mfma_f32_16x16x32_bf16 v[54:57], v[78:81], v[174:177], v[54:57]
	v_mfma_f32_16x16x32_bf16 v[34:37], v[70:73], v[182:185], v[34:37]
	v_mfma_f32_16x16x32_bf16 v[30:33], v[78:81], v[182:185], v[30:33]
	v_mfma_f32_16x16x32_bf16 v[18:21], v[70:73], v[190:193], v[18:21]
	v_mfma_f32_16x16x32_bf16 v[14:17], v[78:81], v[190:193], v[14:17]
	v_mfma_f32_16x16x32_bf16 v[90:93], v[74:77], v[162:165], v[90:93]
	v_mfma_f32_16x16x32_bf16 v[86:89], v[82:85], v[162:165], v[86:89]
	v_mfma_f32_16x16x32_bf16 v[58:61], v[74:77], v[178:181], v[58:61]
	v_mfma_f32_16x16x32_bf16 v[54:57], v[82:85], v[178:181], v[54:57]
	v_mfma_f32_16x16x32_bf16 v[34:37], v[74:77], v[186:189], v[34:37]
	v_mfma_f32_16x16x32_bf16 v[30:33], v[82:85], v[186:189], v[30:33]
	v_mfma_f32_16x16x32_bf16 v[18:21], v[74:77], v[194:197], v[18:21]
	v_mfma_f32_16x16x32_bf16 v[14:17], v[82:85], v[194:197], v[14:17]
	s_setprio 0
	s_setprio 1
	v_mfma_f32_16x16x32_bf16 v[38:41], v[102:105], v[158:161], v[38:41]
	v_mfma_f32_16x16x32_bf16 v[78:81], v[106:109], v[162:165], v[38:41]
	v_mfma_f32_16x16x32_bf16 v[38:41], v[134:137], v[158:161], v[42:45]
	v_mfma_f32_16x16x32_bf16 v[82:85], v[138:141], v[162:165], v[38:41]
	v_mfma_f32_16x16x32_bf16 v[38:41], v[102:105], v[174:177], v[46:49]
	v_mfma_f32_16x16x32_bf16 v[46:49], v[106:109], v[178:181], v[38:41]
	v_mfma_f32_16x16x32_bf16 v[38:41], v[134:137], v[174:177], v[50:53]
	v_mfma_f32_16x16x32_bf16 v[22:25], v[102:105], v[182:185], v[22:25]
	v_mfma_f32_16x16x32_bf16 v[26:29], v[134:137], v[182:185], v[26:29]
	v_mfma_f32_16x16x32_bf16 v[4:7], v[102:105], v[190:193], v[4:7]
	v_mfma_f32_16x16x32_bf16 v[10:13], v[134:137], v[190:193], v[10:13]
	v_mfma_f32_16x16x32_bf16 v[50:53], v[138:141], v[178:181], v[38:41]
	v_mfma_f32_16x16x32_bf16 v[22:25], v[106:109], v[186:189], v[22:25]
	v_mfma_f32_16x16x32_bf16 v[26:29], v[138:141], v[186:189], v[26:29]
	v_mfma_f32_16x16x32_bf16 v[6:9], v[106:109], v[194:197], v[4:7]
	v_mfma_f32_16x16x32_bf16 v[10:13], v[138:141], v[194:197], v[10:13]
	s_setprio 0
	s_add_i32 s52, s52, 2
	s_add_u32 s26, s26, 0x100
	s_addc_u32 s27, s27, 0
	s_add_u32 s25, s25, 0x100
	s_addc_u32 s34, s34, 0
	s_cmp_gt_u32 s52, 13
	s_barrier
	s_cbranch_scc0 .LBB0_891
	s_and_b64 vcc, exec, s[12:13]
	s_cbranch_vccz .LBB0_894
	s_barrier

; #define PG8_STAGE(bufoff, gbase, voff) do { _Pragma("unroll") for (int _i = 0; _i < 2; ++_i) \
;         __builtin_amdgcn_global_load_lds((const unsigned*)((const char*)(gbase) + (voff)[_i]), (LAS unsigned*)(lds + (bufoff) + ldsw + _i * 8192), 16, 0, 0); } while (0)
; #define PG8_LDA(dst, b, h) do { if constexpr (F8) { _Pragma("unroll") for (int m = 0; m < 4; ++m) dst##8[m] = PG8_LD8(lds, PG8_SA(b, h) + aoff + m * 2048); } \
;         else { _Pragma("unroll") for (int m = 0; m < 4; ++m) _Pragma("unroll") for (int k = 0; k < 2; ++k) dst[m][k] = *(const LAS bf16x8*)(lds + PG8_SA(b, h) + aoff + m * 2048 + k * 1024); } } while (0)
; #define PG8_WAIT_V(n) asm volatile("s_waitcnt vmcnt(" #n ")" ::: "memory")
; #define PG8_WAIT_L(n) asm volatile("s_waitcnt lgkmcnt(" #n ")" ::: "memory")
; #define PG8_BAR __builtin_amdgcn_s_barrier()
; #define PG8_SCHED __builtin_amdgcn_sched_barrier(0)
; template <bool GATHER, bool F8, class Epi, class Sched>
; __device__ __forceinline__ void gemm_phase(LAS unsigned char* lds, const int nt, const unsigned lda, const unsigned ldb, const Sched& S, const Epi& E) {
;     ...
;         for (int t = 0; t < nt; t += 2) {
;             const bool last = (t == nt - 2);
;             const char* a1 = cA + (size_t)(t + 1) * kstep;
;             const char* a2 = last ? nA : cA + (size_t)(t + 2) * kstep; const char* b2 = last ? nB : cB + (size_t)(t + 2) * kstep;
;             const char* a3 = a2 + kstep; const char* b3 = b2 + kstep;
;             unsigned w0[2], w1[2];
;             if constexpr (GATHER) {
; #pragma unroll
;                 for (int i = 0; i < 2; ++i) { w0[i] = last ? vN0[i] : vA0[i]; w1[i] = last ? vN1[i] : vA1[i]; }
;             } else {
; #pragma unroll
;                 for (int i = 0; i < 2; ++i) { w0[i] = voffA[i]; w1[i] = voffA[i]; }
;             }
;             PG8_LDB(B0, 0, 0); PG8_LDB(B1, 0, 1); PG8_SCHED; PG8_LDA(At, 0, 0); PG8_STAGE(PG8_SA(1, 1), a1 + hA, vA1);
;             PG8_WAIT_V(8); PG8_WAIT_L(0); PG8_BAR; PG8_MMA(0, 0, At, B0); PG8_MMA(0, 1, At, B1); PG8_BAR; PG8_SCHED;
;             PG8_LDA(At, 0, 1); PG8_STAGE(PG8_SB(0, 0), b2, voffB); PG8_STAGE(PG8_SB(0, 1), b2 + hB, voffB); PG8_STAGE(PG8_SA(0, 0), a2, w0);
;             PG8_WAIT_V(8); PG8_WAIT_L(0); PG8_BAR; PG8_MMA(1, 0, At, B0); PG8_MMA(1, 1, At, B1); PG8_BAR; PG8_SCHED;
.LBB0_1034:
	ds_read_b128 v[130:133], v209
	ds_read_b128 v[134:137], v209 offset:1024
	ds_read_b128 v[138:141], v209 offset:2048
	ds_read_b128 v[142:145], v209 offset:3072
	ds_read_b128 v[146:149], v210
	ds_read_b128 v[150:153], v210 offset:1024
	ds_read_b128 v[154:157], v210 offset:2048
	ds_read_b128 v[158:161], v210 offset:3072
	s_add_u32 s24, s22, 0xfff80080
	s_addc_u32 s25, s23, -1
	s_cmp_eq_u32 s48, 28
	s_cselect_b32 s27, s1, s25
	s_cselect_b32 s26, s0, s24
	s_cselect_b32 s25, s19, s28
	s_cselect_b32 s24, s18, s21
	s_add_i32 m0, s36, 0xc000
	ds_read_b128 v[162:165], v211
	ds_read_b128 v[166:169], v211 offset:1024
	ds_read_b128 v[170:173], v211 offset:2048
	ds_read_b128 v[174:177], v211 offset:3072
	ds_read_b128 v[194:197], v211 offset:4096
	ds_read_b128 v[200:203], v211 offset:5120
	ds_read_b128 v[204:207], v211 offset:6144
	ds_read_b128 v[214:217], v211 offset:7168
	global_load_lds_dwordx4 v186, s[22:23]
	s_add_i32 m0, s36, 0xe000
	s_nop 0
	global_load_lds_dwordx4 v188, s[22:23]
	s_waitcnt vmcnt(8)
	s_waitcnt lgkmcnt(0)
	s_barrier
	s_setprio 1
	s_waitcnt lgkmcnt(0)
	v_mfma_f32_16x16x32_bf16 v[126:129], v[130:133], v[162:165], v[126:129]
	v_mfma_f32_16x16x32_bf16 v[122:125], v[138:141], v[162:165], v[122:125]
	v_mfma_f32_16x16x32_bf16 v[110:113], v[130:133], v[170:173], v[110:113]
	v_mfma_f32_16x16x32_bf16 v[106:109], v[138:141], v[170:173], v[106:109]
	v_mfma_f32_16x16x32_bf16 v[94:97], v[130:133], v[194:197], v[94:97]
	v_mfma_f32_16x16x32_bf16 v[90:93], v[138:141], v[194:197], v[90:93]
	v_mfma_f32_16x16x32_bf16 v[78:81], v[130:133], v[204:207], v[78:81]
	v_mfma_f32_16x16x32_bf16 v[74:77], v[138:141], v[204:207], v[74:77]
	v_mfma_f32_16x16x32_bf16 v[126:129], v[134:137], v[166:169], v[126:129]
	v_mfma_f32_16x16x32_bf16 v[122:125], v[142:145], v[166:169], v[122:125]
	v_mfma_f32_16x16x32_bf16 v[110:113], v[134:137], v[174:177], v[110:113]
	v_mfma_f32_16x16x32_bf16 v[106:109], v[142:145], v[174:177], v[106:109]
	v_mfma_f32_16x16x32_bf16 v[94:97], v[134:137], v[200:203], v[94:97]
	v_mfma_f32_16x16x32_bf16 v[90:93], v[142:145], v[200:203], v[90:93]
	v_mfma_f32_16x16x32_bf16 v[78:81], v[134:137], v[214:217], v[78:81]
	v_mfma_f32_16x16x32_bf16 v[74:77], v[142:145], v[214:217], v[74:77]
	s_setprio 0
	s_setprio 1
	v_mfma_f32_16x16x32_bf16 v[118:121], v[146:149], v[162:165], v[118:121]
	v_mfma_f32_16x16x32_bf16 v[114:117], v[154:157], v[162:165], v[114:117]
	v_mfma_f32_16x16x32_bf16 v[102:105], v[146:149], v[170:173], v[102:105]
	v_mfma_f32_16x16x32_bf16 v[98:101], v[154:157], v[170:173], v[98:101]
	v_mfma_f32_16x16x32_bf16 v[86:89], v[146:149], v[194:197], v[86:89]
	v_mfma_f32_16x16x32_bf16 v[82:85], v[154:157], v[194:197], v[82:85]
	v_mfma_f32_16x16x32_bf16 v[70:73], v[146:149], v[204:207], v[70:73]
	v_mfma_f32_16x16x32_bf16 v[66:69], v[154:157], v[204:207], v[66:69]
	v_mfma_f32_16x16x32_bf16 v[118:121], v[150:153], v[166:169], v[118:121]
	v_mfma_f32_16x16x32_bf16 v[114:117], v[158:161], v[166:169], v[114:117]
	v_mfma_f32_16x16x32_bf16 v[102:105], v[150:153], v[174:177], v[102:105]
	v_mfma_f32_16x16x32_bf16 v[98:101], v[158:161], v[174:177], v[98:101]
	v_mfma_f32_16x16x32_bf16 v[86:89], v[150:153], v[200:203], v[86:89]
	v_mfma_f32_16x16x32_bf16 v[82:85], v[158:161], v[200:203], v[82:85]
	v_mfma_f32_16x16x32_bf16 v[70:73], v[150:153], v[214:217], v[70:73]
	v_mfma_f32_16x16x32_bf16 v[66:69], v[158:161], v[214:217], v[66:69]
	s_setprio 0
	s_barrier
	s_add_i32 s49, s44, s35
	s_mov_b32 m0, s49
	ds_read_b128 v[162:165], v211 offset:16384
	ds_read_b128 v[166:169], v211 offset:17408
	ds_read_b128 v[170:173], v211 offset:18432
	ds_read_b128 v[174:177], v211 offset:19456
	ds_read_b128 v[194:197], v211 offset:20480
	ds_read_b128 v[200:203], v211 offset:21504
	ds_read_b128 v[204:207], v211 offset:22528
	ds_read_b128 v[214:217], v211 offset:23552
	global_load_lds_dwordx4 v180, s[24:25]
	s_add_i32 m0, s49, 0x2000
	s_add_u32 s50, s24, 0x80000
	s_addc_u32 s51, s25, 0
	s_add_i32 s49, s45, s35
	global_load_lds_dwordx4 v184, s[24:25]
	s_mov_b32 m0, s49
	s_nop 0
	global_load_lds_dwordx4 v180, s[50:51]
	s_add_i32 m0, s49, 0x2000
	s_nop 0
	global_load_lds_dwordx4 v184, s[50:51]
	s_mov_b32 m0, s36
	s_nop 0
	s_mov_b64 s[98:99], s[26:27]
	global_load_lds_dwordx4 v178, s[26:27]
	s_mov_b32 m0, s37
	s_nop 0
	global_load_lds_dwordx4 v182, s[26:27]
	s_waitcnt vmcnt(8)
	s_waitcnt lgkmcnt(0)
	s_barrier
	s_setprio 1
	s_waitcnt lgkmcnt(0)
	v_mfma_f32_16x16x32_bf16 v[54:57], v[130:133], v[162:165], v[54:57]
	v_mfma_f32_16x16x32_bf16 v[50:53], v[138:141], v[162:165], v[50:53]
	v_mfma_f32_16x16x32_bf16 v[38:41], v[130:133], v[170:173], v[38:41]
	v_mfma_f32_16x16x32_bf16 v[34:37], v[138:141], v[170:173], v[34:37]
	v_mfma_f32_16x16x32_bf16 v[22:25], v[130:133], v[194:197], v[22:25]
	v_mfma_f32_16x16x32_bf16 v[18:21], v[138:141], v[194:197], v[18:21]
	v_mfma_f32_16x16x32_bf16 v[6:9], v[130:133], v[204:207], v[6:9]
	v_mfma_f32_16x16x32_bf16 v[2:5], v[138:141], v[204:207], v[2:5]
	v_mfma_f32_16x16x32_bf16 v[54:57], v[134:137], v[166:169], v[54:57]
	v_mfma_f32_16x16x32_bf16 v[50:53], v[142:145], v[166:169], v[50:53]
	v_mfma_f32_16x16x32_bf16 v[38:41], v[134:137], v[174:177], v[38:41]
	v_mfma_f32_16x16x32_bf16 v[34:37], v[142:145], v[174:177], v[34:37]
	v_mfma_f32_16x16x32_bf16 v[22:25], v[134:137], v[200:203], v[22:25]
	v_mfma_f32_16x16x32_bf16 v[18:21], v[142:145], v[200:203], v[18:21]
	v_mfma_f32_16x16x32_bf16 v[6:9], v[134:137], v[214:217], v[6:9]
	v_mfma_f32_16x16x32_bf16 v[2:5], v[142:145], v[214:217], v[2:5]
	s_setprio 0
	s_setprio 1
	v_mfma_f32_16x16x32_bf16 v[62:65], v[146:149], v[162:165], v[62:65]
	v_mfma_f32_16x16x32_bf16 v[58:61], v[154:157], v[162:165], v[58:61]
	v_mfma_f32_16x16x32_bf16 v[46:49], v[146:149], v[170:173], v[46:49]
	v_mfma_f32_16x16x32_bf16 v[42:45], v[154:157], v[170:173], v[42:45]
	v_mfma_f32_16x16x32_bf16 v[30:33], v[146:149], v[194:197], v[30:33]
	v_mfma_f32_16x16x32_bf16 v[26:29], v[154:157], v[194:197], v[26:29]
	v_mfma_f32_16x16x32_bf16 v[14:17], v[146:149], v[204:207], v[14:17]
	v_mfma_f32_16x16x32_bf16 v[10:13], v[154:157], v[204:207], v[10:13]
	v_mfma_f32_16x16x32_bf16 v[62:65], v[150:153], v[166:169], v[62:65]
	v_mfma_f32_16x16x32_bf16 v[58:61], v[158:161], v[166:169], v[58:61]
	v_mfma_f32_16x16x32_bf16 v[46:49], v[150:153], v[174:177], v[46:49]
	v_mfma_f32_16x16x32_bf16 v[42:45], v[158:161], v[174:177], v[42:45]
	v_mfma_f32_16x16x32_bf16 v[30:33], v[150:153], v[200:203], v[30:33]
	v_mfma_f32_16x16x32_bf16 v[26:29], v[158:161], v[200:203], v[26:29]
	v_mfma_f32_16x16x32_bf16 v[14:17], v[150:153], v[214:217], v[14:17]
	v_mfma_f32_16x16x32_bf16 v[10:13], v[158:161], v[214:217], v[10:13]
	s_setprio 0
	s_barrier
; #define PG8_STAGE(bufoff, gbase, voff) do { _Pragma("unroll") for (int _i = 0; _i < 2; ++_i) \
;         __builtin_amdgcn_global_load_lds((const unsigned*)((const char*)(gbase) + (voff)[_i]), (LAS unsigned*)(lds + (bufoff) + ldsw + _i * 8192), 16, 0, 0); } while (0)
; #define PG8_LDA(dst, b, h) do { if constexpr (F8) { _Pragma("unroll") for (int m = 0; m < 4; ++m) dst##8[m] = PG8_LD8(lds, PG8_SA(b, h) + aoff + m * 2048); } \
;         else { _Pragma("unroll") for (int m = 0; m < 4; ++m) _Pragma("unroll") for (int k = 0; k < 2; ++k) dst[m][k] = *(const LAS bf16x8*)(lds + PG8_SA(b, h) + aoff + m * 2048 + k * 1024); } } while (0)
; #define PG8_LDB(dst, b, h) do { if constexpr (F8) { _Pragma("unroll") for (int n = 0; n < 2; ++n) dst##8[n] = PG8_LD8(ldsB, PG8_SBR(b, h) + boff + n * 2048); } \
;         else { _Pragma("unroll") for (int n = 0; n < 2; ++n) _Pragma("unroll") for (int k = 0; k < 2; ++k) dst[n][k] = *(const LAS bf16x8*)(ldsB + PG8_SBR(b, h) + boff + n * 2048 + k * 1024); } } while (0)
; #define PG8_WAIT_V(n) asm volatile("s_waitcnt vmcnt(" #n ")" ::: "memory")
; #define PG8_WAIT_L(n) asm volatile("s_waitcnt lgkmcnt(" #n ")" ::: "memory")
; #define PG8_BAR __builtin_amdgcn_s_barrier()
; #define PG8_SCHED __builtin_amdgcn_sched_barrier(0)
; template <bool GATHER, bool F8, class Epi, class Sched>
; __device__ __forceinline__ void gemm_phase(LAS unsigned char* lds, const int nt, const unsigned lda, const unsigned ldb, const Sched& S, const Epi& E) {
;     ...
;             PG8_LDB(B0, 1, 0); PG8_LDB(B1, 1, 1); PG8_SCHED; PG8_LDA(At, 1, 0); PG8_STAGE(PG8_SA(0, 1), a2 + hA, w1);
;             PG8_WAIT_V(8); PG8_WAIT_L(0); PG8_BAR; PG8_MMA(0, 0, At, B0); PG8_MMA(0, 1, At, B1); PG8_BAR; PG8_SCHED;
;             PG8_LDA(At, 1, 1); PG8_STAGE(PG8_SB(1, 0), b3, voffB); PG8_STAGE(PG8_SB(1, 1), b3 + hB, voffB); PG8_STAGE(PG8_SA(1, 0), a3, w0);
;             PG8_WAIT_V(8); PG8_WAIT_L(0); PG8_BAR; PG8_MMA(1, 0, At, B0); PG8_MMA(1, 1, At, B1); PG8_BAR; PG8_SCHED;
;         }
;         if (wr == 0) PG8_BAR;
	s_add_i32 s49, 0, 0x18000
	s_add_i32 s50, 0, 0x1c000
	v_add_u32_e32 v142, s49, v199
	v_add_u32_e32 v158, s50, v199
	ds_read_b128 v[130:133], v142
	ds_read_b128 v[134:137], v142 offset:1024
	ds_read_b128 v[138:141], v142 offset:2048
	ds_read_b128 v[142:145], v142 offset:3072
	ds_read_b128 v[146:149], v158
	ds_read_b128 v[150:153], v158 offset:1024
	ds_read_b128 v[154:157], v158 offset:2048
	ds_read_b128 v[158:161], v158 offset:3072
	s_add_u32 s26, s26, 0x80000
	s_addc_u32 s27, s27, 0
	s_mov_b32 m0, s38
	ds_read_b128 v[162:165], v211 offset:32768
	ds_read_b128 v[166:169], v211 offset:33792
	ds_read_b128 v[170:173], v211 offset:34816
	ds_read_b128 v[174:177], v211 offset:35840
	ds_read_b128 v[194:197], v211 offset:36864
	ds_read_b128 v[200:203], v211 offset:37888
	ds_read_b128 v[204:207], v211 offset:38912
	ds_read_b128 v[214:217], v211 offset:39936
	global_load_lds_dwordx4 v178, s[26:27]
	s_mov_b32 m0, s39
	s_nop 0
	global_load_lds_dwordx4 v182, s[26:27]
	s_waitcnt vmcnt(8)
	s_waitcnt lgkmcnt(0)
	s_barrier
	s_setprio 1
	s_waitcnt lgkmcnt(0)
	v_mfma_f32_16x16x32_bf16 v[126:129], v[130:133], v[162:165], v[126:129]
	v_mfma_f32_16x16x32_bf16 v[122:125], v[138:141], v[162:165], v[122:125]
	v_mfma_f32_16x16x32_bf16 v[110:113], v[130:133], v[170:173], v[110:113]
	v_mfma_f32_16x16x32_bf16 v[106:109], v[138:141], v[170:173], v[106:109]
	v_mfma_f32_16x16x32_bf16 v[94:97], v[130:133], v[194:197], v[94:97]
	v_mfma_f32_16x16x32_bf16 v[90:93], v[138:141], v[194:197], v[90:93]
	v_mfma_f32_16x16x32_bf16 v[78:81], v[130:133], v[204:207], v[78:81]
	v_mfma_f32_16x16x32_bf16 v[74:77], v[138:141], v[204:207], v[74:77]
	v_mfma_f32_16x16x32_bf16 v[126:129], v[134:137], v[166:169], v[126:129]
	v_mfma_f32_16x16x32_bf16 v[122:125], v[142:145], v[166:169], v[122:125]
	v_mfma_f32_16x16x32_bf16 v[110:113], v[134:137], v[174:177], v[110:113]
	v_mfma_f32_16x16x32_bf16 v[106:109], v[142:145], v[174:177], v[106:109]
	v_mfma_f32_16x16x32_bf16 v[94:97], v[134:137], v[200:203], v[94:97]
	v_mfma_f32_16x16x32_bf16 v[90:93], v[142:145], v[200:203], v[90:93]
	v_mfma_f32_16x16x32_bf16 v[78:81], v[134:137], v[214:217], v[78:81]
	v_mfma_f32_16x16x32_bf16 v[74:77], v[142:145], v[214:217], v[74:77]
	s_setprio 0
	s_setprio 1
	v_mfma_f32_16x16x32_bf16 v[118:121], v[146:149], v[162:165], v[118:121]
	v_mfma_f32_16x16x32_bf16 v[114:117], v[154:157], v[162:165], v[114:117]
	v_mfma_f32_16x16x32_bf16 v[102:105], v[146:149], v[170:173], v[102:105]
	v_mfma_f32_16x16x32_bf16 v[98:101], v[154:157], v[170:173], v[98:101]
	v_mfma_f32_16x16x32_bf16 v[86:89], v[146:149], v[194:197], v[86:89]
	v_mfma_f32_16x16x32_bf16 v[82:85], v[154:157], v[194:197], v[82:85]
	v_mfma_f32_16x16x32_bf16 v[70:73], v[146:149], v[204:207], v[70:73]
	v_mfma_f32_16x16x32_bf16 v[66:69], v[154:157], v[204:207], v[66:69]
	v_mfma_f32_16x16x32_bf16 v[118:121], v[150:153], v[166:169], v[118:121]
	v_mfma_f32_16x16x32_bf16 v[114:117], v[158:161], v[166:169], v[114:117]
	v_mfma_f32_16x16x32_bf16 v[102:105], v[150:153], v[174:177], v[102:105]
	v_mfma_f32_16x16x32_bf16 v[98:101], v[158:161], v[174:177], v[98:101]
	v_mfma_f32_16x16x32_bf16 v[86:89], v[150:153], v[200:203], v[86:89]
	v_mfma_f32_16x16x32_bf16 v[82:85], v[158:161], v[200:203], v[82:85]
	v_mfma_f32_16x16x32_bf16 v[70:73], v[150:153], v[214:217], v[70:73]
	v_mfma_f32_16x16x32_bf16 v[66:69], v[158:161], v[214:217], v[66:69]
	s_setprio 0
	s_barrier
	s_add_i32 s26, s49, s35
	s_add_i32 m0, s26, 0xffffff80
	ds_read_b128 v[162:165], v211 offset:49152
	ds_read_b128 v[166:169], v211 offset:50176
	ds_read_b128 v[170:173], v211 offset:51200
	ds_read_b128 v[174:177], v211 offset:52224
	ds_read_b128 v[194:197], v211 offset:53248
	ds_read_b128 v[200:203], v211 offset:54272
	ds_read_b128 v[204:207], v211 offset:55296
	ds_read_b128 v[214:217], v211 offset:56320
	global_load_lds_dwordx4 v180, s[24:25] offset:128
	s_add_i32 m0, s26, 0x1f80
	s_add_i32 s26, s50, s35
	global_load_lds_dwordx4 v184, s[24:25] offset:128
	s_add_u32 s24, s24, 0x80080
	s_addc_u32 s25, s25, 0
	s_mov_b32 m0, s26
	s_nop 0
	global_load_lds_dwordx4 v180, s[24:25]
	s_add_i32 m0, s26, 0x2000
	s_nop 0
	global_load_lds_dwordx4 v184, s[24:25]
	s_add_i32 m0, s41, 0xffffff80
	s_nop 0
	global_load_lds_dwordx4 v178, s[98:99] offset:128
	s_add_i32 m0, s42, 0xffffff80
	s_nop 0
	global_load_lds_dwordx4 v182, s[98:99] offset:128
	s_waitcnt vmcnt(8)
	s_waitcnt lgkmcnt(0)
	s_barrier
	s_setprio 1
	s_waitcnt lgkmcnt(0)
	v_mfma_f32_16x16x32_bf16 v[54:57], v[130:133], v[162:165], v[54:57]
	v_mfma_f32_16x16x32_bf16 v[50:53], v[138:141], v[162:165], v[50:53]
	v_mfma_f32_16x16x32_bf16 v[38:41], v[130:133], v[170:173], v[38:41]
	v_mfma_f32_16x16x32_bf16 v[34:37], v[138:141], v[170:173], v[34:37]
	v_mfma_f32_16x16x32_bf16 v[22:25], v[130:133], v[194:197], v[22:25]
	v_mfma_f32_16x16x32_bf16 v[18:21], v[138:141], v[194:197], v[18:21]
	v_mfma_f32_16x16x32_bf16 v[6:9], v[130:133], v[204:207], v[6:9]
	v_mfma_f32_16x16x32_bf16 v[2:5], v[138:141], v[204:207], v[2:5]
	v_mfma_f32_16x16x32_bf16 v[54:57], v[134:137], v[166:169], v[54:57]
	v_mfma_f32_16x16x32_bf16 v[50:53], v[142:145], v[166:169], v[50:53]
	v_mfma_f32_16x16x32_bf16 v[38:41], v[134:137], v[174:177], v[38:41]
	v_mfma_f32_16x16x32_bf16 v[34:37], v[142:145], v[174:177], v[34:37]
	v_mfma_f32_16x16x32_bf16 v[22:25], v[134:137], v[200:203], v[22:25]
	v_mfma_f32_16x16x32_bf16 v[18:21], v[142:145], v[200:203], v[18:21]
	v_mfma_f32_16x16x32_bf16 v[6:9], v[134:137], v[214:217], v[6:9]
	v_mfma_f32_16x16x32_bf16 v[2:5], v[142:145], v[214:217], v[2:5]
	s_setprio 0
	s_setprio 1
	v_mfma_f32_16x16x32_bf16 v[62:65], v[146:149], v[162:165], v[62:65]
	v_mfma_f32_16x16x32_bf16 v[58:61], v[154:157], v[162:165], v[58:61]
	v_mfma_f32_16x16x32_bf16 v[46:49], v[146:149], v[170:173], v[46:49]
	v_mfma_f32_16x16x32_bf16 v[42:45], v[154:157], v[170:173], v[42:45]
	v_mfma_f32_16x16x32_bf16 v[30:33], v[146:149], v[194:197], v[30:33]
	v_mfma_f32_16x16x32_bf16 v[26:29], v[154:157], v[194:197], v[26:29]
	v_mfma_f32_16x16x32_bf16 v[14:17], v[146:149], v[204:207], v[14:17]
	v_mfma_f32_16x16x32_bf16 v[10:13], v[154:157], v[204:207], v[10:13]
	v_mfma_f32_16x16x32_bf16 v[62:65], v[150:153], v[166:169], v[62:65]
	v_mfma_f32_16x16x32_bf16 v[58:61], v[158:161], v[166:169], v[58:61]
	v_mfma_f32_16x16x32_bf16 v[46:49], v[150:153], v[174:177], v[46:49]
	v_mfma_f32_16x16x32_bf16 v[42:45], v[158:161], v[174:177], v[42:45]
	v_mfma_f32_16x16x32_bf16 v[30:33], v[150:153], v[200:203], v[30:33]
	v_mfma_f32_16x16x32_bf16 v[26:29], v[158:161], v[200:203], v[26:29]
	v_mfma_f32_16x16x32_bf16 v[14:17], v[150:153], v[214:217], v[14:17]
	v_mfma_f32_16x16x32_bf16 v[10:13], v[158:161], v[214:217], v[10:13]
	s_setprio 0
	s_add_i32 s48, s48, 2
	s_add_u32 s22, s22, 0x100
	s_addc_u32 s23, s23, 0
	s_add_u32 s21, s21, 0x100
	s_addc_u32 s28, s28, 0
	s_cmp_gt_u32 s48, 29
	s_barrier
	s_cbranch_scc0 .LBB0_1034
	s_and_b64 vcc, exec, s[16:17]
	s_cbranch_vccz .LBB0_1037
	s_barrier

; #define PG8_STAGE(bufoff, gbase, voff) do { _Pragma("unroll") for (int _i = 0; _i < 2; ++_i) \
;         __builtin_amdgcn_global_load_lds((const unsigned*)((const char*)(gbase) + (voff)[_i]), (LAS unsigned*)(lds + (bufoff) + ldsw + _i * 8192), 16, 0, 0); } while (0)
; #define PG8_LDA(dst, b, h) do { if constexpr (F8) { _Pragma("unroll") for (int m = 0; m < 4; ++m) dst##8[m] = PG8_LD8(lds, PG8_SA(b, h) + aoff + m * 2048); } \
;         else { _Pragma("unroll") for (int m = 0; m < 4; ++m) _Pragma("unroll") for (int k = 0; k < 2; ++k) dst[m][k] = *(const LAS bf16x8*)(lds + PG8_SA(b, h) + aoff + m * 2048 + k * 1024); } } while (0)
; #define PG8_WAIT_V(n) asm volatile("s_waitcnt vmcnt(" #n ")" ::: "memory")
; #define PG8_WAIT_L(n) asm volatile("s_waitcnt lgkmcnt(" #n ")" ::: "memory")
; #define PG8_BAR __builtin_amdgcn_s_barrier()
; #define PG8_SCHED __builtin_amdgcn_sched_barrier(0)
; template <bool GATHER, bool F8, class Epi, class Sched>
; __device__ __forceinline__ void gemm_phase(LAS unsigned char* lds, const int nt, const unsigned lda, const unsigned ldb, const Sched& S, const Epi& E) {
;     ...
;         for (int t = 0; t < nt; t += 2) {
;             const bool last = (t == nt - 2);
;             const char* a1 = cA + (size_t)(t + 1) * kstep;
;             const char* a2 = last ? nA : cA + (size_t)(t + 2) * kstep; const char* b2 = last ? nB : cB + (size_t)(t + 2) * kstep;
;             const char* a3 = a2 + kstep; const char* b3 = b2 + kstep;
;             unsigned w0[2], w1[2];
;             if constexpr (GATHER) {
; #pragma unroll
;                 for (int i = 0; i < 2; ++i) { w0[i] = last ? vN0[i] : vA0[i]; w1[i] = last ? vN1[i] : vA1[i]; }
;             } else {
; #pragma unroll
;                 for (int i = 0; i < 2; ++i) { w0[i] = voffA[i]; w1[i] = voffA[i]; }
;             }
;             PG8_LDB(B0, 0, 0); PG8_LDB(B1, 0, 1); PG8_SCHED; PG8_LDA(At, 0, 0); PG8_STAGE(PG8_SA(1, 1), a1 + hA, vA1);
;             PG8_WAIT_V(8); PG8_WAIT_L(0); PG8_BAR; PG8_MMA(0, 0, At, B0); PG8_MMA(0, 1, At, B1); PG8_BAR; PG8_SCHED;
;             PG8_LDA(At, 0, 1); PG8_STAGE(PG8_SB(0, 0), b2, voffB); PG8_STAGE(PG8_SB(0, 1), b2 + hB, voffB); PG8_STAGE(PG8_SA(0, 0), a2, w0);
;             PG8_WAIT_V(8); PG8_WAIT_L(0); PG8_BAR; PG8_MMA(1, 0, At, B0); PG8_MMA(1, 1, At, B1); PG8_BAR; PG8_SCHED;
.LBB0_1152:
	ds_read_b128 v[152:155], v146
	ds_read_b128 v[156:159], v146 offset:1024
	ds_read_b128 v[160:163], v146 offset:2048
	ds_read_b128 v[164:167], v146 offset:3072
	ds_read_b128 v[168:171], v148
	ds_read_b128 v[172:175], v148 offset:1024
	ds_read_b128 v[176:179], v148 offset:2048
	ds_read_b128 v[180:183], v148 offset:3072
	s_add_u32 s12, s0, s10
	s_addc_u32 s13, s1, s11
	s_add_u32 s12, s12, 0x100
	s_addc_u32 s13, s13, 0
	s_add_u32 s38, s24, s10
	s_addc_u32 s39, s25, s11
	s_cmpk_eq_i32 s10, 0xf00
	s_cselect_b32 s15, s1, s13
	s_cselect_b32 s14, s0, s12
	s_cselect_b32 s13, s7, s39
	s_cselect_b32 s12, s6, s38
	s_mov_b32 m0, s27
	v_lshl_add_u64 v[196:197], v[140:141], 0, s[10:11]
	ds_read_b128 v[184:187], v149
	ds_read_b128 v[188:191], v149 offset:1024
	ds_read_b128 v[192:195], v149 offset:2048
	ds_read_b128 v[200:203], v149 offset:3072
	ds_read_b128 v[204:207], v149 offset:4096
	ds_read_b128 v[208:211], v149 offset:5120
	ds_read_b128 v[212:215], v149 offset:6144
	ds_read_b128 v[216:219], v149 offset:7168
	global_load_lds_dwordx4 v[196:197], off
	v_lshl_add_u64 v[196:197], v[142:143], 0, s[10:11]
	s_mov_b32 m0, s28
	s_nop 0
	global_load_lds_dwordx4 v[196:197], off
	s_waitcnt vmcnt(8)
	s_waitcnt lgkmcnt(0)
	s_barrier
	s_setprio 1
	s_waitcnt lgkmcnt(0)
	v_mfma_f32_16x16x32_bf16 v[126:129], v[152:155], v[184:187], v[126:129]
	v_mfma_f32_16x16x32_bf16 v[122:125], v[160:163], v[184:187], v[122:125]
	v_mfma_f32_16x16x32_bf16 v[114:117], v[152:155], v[192:195], v[114:117]
	v_mfma_f32_16x16x32_bf16 v[106:109], v[160:163], v[192:195], v[106:109]
	v_mfma_f32_16x16x32_bf16 v[98:101], v[152:155], v[204:207], v[98:101]
	v_mfma_f32_16x16x32_bf16 v[90:93], v[160:163], v[204:207], v[90:93]
	v_mfma_f32_16x16x32_bf16 v[82:85], v[152:155], v[212:215], v[82:85]
	v_mfma_f32_16x16x32_bf16 v[74:77], v[160:163], v[212:215], v[74:77]
	v_mfma_f32_16x16x32_bf16 v[126:129], v[156:159], v[188:191], v[126:129]
	v_mfma_f32_16x16x32_bf16 v[122:125], v[164:167], v[188:191], v[122:125]
	v_mfma_f32_16x16x32_bf16 v[114:117], v[156:159], v[200:203], v[114:117]
	v_mfma_f32_16x16x32_bf16 v[106:109], v[164:167], v[200:203], v[106:109]
	v_mfma_f32_16x16x32_bf16 v[98:101], v[156:159], v[208:211], v[98:101]
	v_mfma_f32_16x16x32_bf16 v[90:93], v[164:167], v[208:211], v[90:93]
	v_mfma_f32_16x16x32_bf16 v[82:85], v[156:159], v[216:219], v[82:85]
	v_mfma_f32_16x16x32_bf16 v[74:77], v[164:167], v[216:219], v[74:77]
	s_setprio 0
	s_setprio 1
	v_mfma_f32_16x16x32_bf16 v[118:121], v[168:171], v[184:187], v[118:121]
	v_mfma_f32_16x16x32_bf16 v[110:113], v[176:179], v[184:187], v[110:113]
	v_mfma_f32_16x16x32_bf16 v[102:105], v[168:171], v[192:195], v[102:105]
	v_mfma_f32_16x16x32_bf16 v[94:97], v[176:179], v[192:195], v[94:97]
	v_mfma_f32_16x16x32_bf16 v[86:89], v[168:171], v[204:207], v[86:89]
	v_mfma_f32_16x16x32_bf16 v[78:81], v[176:179], v[204:207], v[78:81]
	v_mfma_f32_16x16x32_bf16 v[62:65], v[168:171], v[212:215], v[62:65]
	v_mfma_f32_16x16x32_bf16 v[58:61], v[176:179], v[212:215], v[58:61]
	v_mfma_f32_16x16x32_bf16 v[118:121], v[172:175], v[188:191], v[118:121]
	v_mfma_f32_16x16x32_bf16 v[110:113], v[180:183], v[188:191], v[110:113]
	v_mfma_f32_16x16x32_bf16 v[102:105], v[172:175], v[200:203], v[102:105]
	v_mfma_f32_16x16x32_bf16 v[94:97], v[180:183], v[200:203], v[94:97]
	v_mfma_f32_16x16x32_bf16 v[86:89], v[172:175], v[208:211], v[86:89]
	v_mfma_f32_16x16x32_bf16 v[78:81], v[180:183], v[208:211], v[78:81]
	v_mfma_f32_16x16x32_bf16 v[62:65], v[172:175], v[216:219], v[62:65]
	v_mfma_f32_16x16x32_bf16 v[58:61], v[180:183], v[216:219], v[58:61]
	s_setprio 0
	s_barrier
	s_mov_b32 m0, s29
	v_lshl_add_u64 v[196:197], s[12:13], 0, v[134:135]
	s_add_u32 s38, s12, 0x80000
	ds_read_b128 v[184:187], v149 offset:16384
	ds_read_b128 v[188:191], v149 offset:17408
	ds_read_b128 v[192:195], v149 offset:18432
	ds_read_b128 v[200:203], v149 offset:19456
	ds_read_b128 v[204:207], v149 offset:20480
	ds_read_b128 v[208:211], v149 offset:21504
	ds_read_b128 v[212:215], v149 offset:22528
	ds_read_b128 v[216:219], v149 offset:23552
	global_load_lds_dwordx4 v[196:197], off
	v_lshl_add_u64 v[220:221], s[12:13], 0, v[138:139]
	s_mov_b32 m0, s30
	s_addc_u32 s39, s13, 0
	global_load_lds_dwordx4 v[220:221], off
	v_lshl_add_u64 v[222:223], s[38:39], 0, v[134:135]
	s_mov_b32 m0, s31
	v_lshl_add_u64 v[224:225], s[14:15], 0, v[136:137]
	global_load_lds_dwordx4 v[222:223], off
	v_lshl_add_u64 v[222:223], s[38:39], 0, v[138:139]
	s_mov_b32 m0, s33
	s_nop 0
	global_load_lds_dwordx4 v[222:223], off
	v_lshl_add_u64 v[222:223], s[14:15], 0, v[132:133]
	s_mov_b32 m0, s3
	s_nop 0
	global_load_lds_dwordx4 v[222:223], off
	s_mov_b32 m0, s19
	s_nop 0
	global_load_lds_dwordx4 v[224:225], off
	s_waitcnt vmcnt(8)
	s_waitcnt lgkmcnt(0)
	s_barrier
; #define PG8_STAGE(bufoff, gbase, voff) do { _Pragma("unroll") for (int _i = 0; _i < 2; ++_i) \
;         __builtin_amdgcn_global_load_lds((const unsigned*)((const char*)(gbase) + (voff)[_i]), (LAS unsigned*)(lds + (bufoff) + ldsw + _i * 8192), 16, 0, 0); } while (0)
; #define PG8_LDA(dst, b, h) do { if constexpr (F8) { _Pragma("unroll") for (int m = 0; m < 4; ++m) dst##8[m] = PG8_LD8(lds, PG8_SA(b, h) + aoff + m * 2048); } \
;         else { _Pragma("unroll") for (int m = 0; m < 4; ++m) _Pragma("unroll") for (int k = 0; k < 2; ++k) dst[m][k] = *(const LAS bf16x8*)(lds + PG8_SA(b, h) + aoff + m * 2048 + k * 1024); } } while (0)
; #define PG8_LDB(dst, b, h) do { if constexpr (F8) { _Pragma("unroll") for (int n = 0; n < 2; ++n) dst##8[n] = PG8_LD8(ldsB, PG8_SBR(b, h) + boff + n * 2048); } \
;         else { _Pragma("unroll") for (int n = 0; n < 2; ++n) _Pragma("unroll") for (int k = 0; k < 2; ++k) dst[n][k] = *(const LAS bf16x8*)(ldsB + PG8_SBR(b, h) + boff + n * 2048 + k * 1024); } } while (0)
; #define PG8_WAIT_V(n) asm volatile("s_waitcnt vmcnt(" #n ")" ::: "memory")
; #define PG8_WAIT_L(n) asm volatile("s_waitcnt lgkmcnt(" #n ")" ::: "memory")
; #define PG8_BAR __builtin_amdgcn_s_barrier()
; #define PG8_SCHED __builtin_amdgcn_sched_barrier(0)
; template <bool GATHER, bool F8, class Epi, class Sched>
; __device__ __forceinline__ void gemm_phase(LAS unsigned char* lds, const int nt, const unsigned lda, const unsigned ldb, const Sched& S, const Epi& E) {
;     ...
;             PG8_WAIT_V(8); PG8_WAIT_L(0); PG8_BAR; PG8_MMA(0, 0, At, B0); PG8_MMA(0, 1, At, B1); PG8_BAR; PG8_SCHED;
;             PG8_LDA(At, 0, 1); PG8_STAGE(PG8_SB(0, 0), b2, voffB); PG8_STAGE(PG8_SB(0, 1), b2 + hB, voffB); PG8_STAGE(PG8_SA(0, 0), a2, w0);
;             PG8_WAIT_V(8); PG8_WAIT_L(0); PG8_BAR; PG8_MMA(1, 0, At, B0); PG8_MMA(1, 1, At, B1); PG8_BAR; PG8_SCHED;
;             PG8_LDB(B0, 1, 0); PG8_LDB(B1, 1, 1); PG8_SCHED; PG8_LDA(At, 1, 0); PG8_STAGE(PG8_SA(0, 1), a2 + hA, w1);
;             PG8_WAIT_V(8); PG8_WAIT_L(0); PG8_BAR; PG8_MMA(0, 0, At, B0); PG8_MMA(0, 1, At, B1); PG8_BAR; PG8_SCHED;
	s_setprio 1
	s_waitcnt lgkmcnt(0)
	v_mfma_f32_16x16x32_bf16 v[54:57], v[152:155], v[184:187], v[54:57]
	v_mfma_f32_16x16x32_bf16 v[50:53], v[160:163], v[184:187], v[50:53]
	v_mfma_f32_16x16x32_bf16 v[30:33], v[152:155], v[192:195], v[30:33]
	v_mfma_f32_16x16x32_bf16 v[26:29], v[160:163], v[192:195], v[26:29]
	v_mfma_f32_16x16x32_bf16 v[14:17], v[152:155], v[204:207], v[14:17]
	v_mfma_f32_16x16x32_bf16 v[10:13], v[160:163], v[204:207], v[10:13]
	v_mfma_f32_16x16x32_bf16 v[6:9], v[152:155], v[212:215], v[6:9]
	v_mfma_f32_16x16x32_bf16 v[2:5], v[160:163], v[212:215], v[2:5]
	v_mfma_f32_16x16x32_bf16 v[54:57], v[156:159], v[188:191], v[54:57]
	v_mfma_f32_16x16x32_bf16 v[50:53], v[164:167], v[188:191], v[50:53]
	v_mfma_f32_16x16x32_bf16 v[30:33], v[156:159], v[200:203], v[30:33]
	v_mfma_f32_16x16x32_bf16 v[26:29], v[164:167], v[200:203], v[26:29]
	v_mfma_f32_16x16x32_bf16 v[14:17], v[156:159], v[208:211], v[14:17]
	v_mfma_f32_16x16x32_bf16 v[10:13], v[164:167], v[208:211], v[10:13]
	v_mfma_f32_16x16x32_bf16 v[6:9], v[156:159], v[216:219], v[6:9]
	v_mfma_f32_16x16x32_bf16 v[2:5], v[164:167], v[216:219], v[2:5]
	s_setprio 0
	s_setprio 1
	v_mfma_f32_16x16x32_bf16 v[66:69], v[168:171], v[184:187], v[66:69]
	v_mfma_f32_16x16x32_bf16 v[70:73], v[176:179], v[184:187], v[70:73]
	v_mfma_f32_16x16x32_bf16 v[42:45], v[168:171], v[192:195], v[42:45]
	v_mfma_f32_16x16x32_bf16 v[46:49], v[176:179], v[192:195], v[46:49]
	v_mfma_f32_16x16x32_bf16 v[34:37], v[168:171], v[204:207], v[34:37]
	v_mfma_f32_16x16x32_bf16 v[38:41], v[176:179], v[204:207], v[38:41]
	v_mfma_f32_16x16x32_bf16 v[18:21], v[168:171], v[212:215], v[18:21]
	v_mfma_f32_16x16x32_bf16 v[22:25], v[176:179], v[212:215], v[22:25]
	v_mfma_f32_16x16x32_bf16 v[66:69], v[172:175], v[188:191], v[66:69]
	v_mfma_f32_16x16x32_bf16 v[70:73], v[180:183], v[188:191], v[70:73]
	v_mfma_f32_16x16x32_bf16 v[42:45], v[172:175], v[200:203], v[42:45]
	v_mfma_f32_16x16x32_bf16 v[46:49], v[180:183], v[200:203], v[46:49]
	v_mfma_f32_16x16x32_bf16 v[34:37], v[172:175], v[208:211], v[34:37]
	v_mfma_f32_16x16x32_bf16 v[38:41], v[180:183], v[208:211], v[38:41]
	v_mfma_f32_16x16x32_bf16 v[18:21], v[172:175], v[216:219], v[18:21]
	v_mfma_f32_16x16x32_bf16 v[22:25], v[180:183], v[216:219], v[22:25]
	s_setprio 0
	s_barrier
	ds_read_b128 v[152:155], v150
	ds_read_b128 v[156:159], v150 offset:1024
	ds_read_b128 v[160:163], v150 offset:2048
	ds_read_b128 v[164:167], v150 offset:3072
	ds_read_b128 v[168:171], v151
	ds_read_b128 v[172:175], v151 offset:1024
	ds_read_b128 v[176:179], v151 offset:2048
	ds_read_b128 v[180:183], v151 offset:3072
	s_add_u32 s14, s14, 0x80000
	s_addc_u32 s15, s15, 0
	s_mov_b32 m0, s20
	v_lshl_add_u64 v[226:227], s[14:15], 0, v[132:133]
	ds_read_b128 v[184:187], v149 offset:32768
	ds_read_b128 v[188:191], v149 offset:33792
	ds_read_b128 v[192:195], v149 offset:34816
	ds_read_b128 v[200:203], v149 offset:35840
	ds_read_b128 v[204:207], v149 offset:36864
	ds_read_b128 v[208:211], v149 offset:37888
	ds_read_b128 v[212:215], v149 offset:38912
	ds_read_b128 v[216:219], v149 offset:39936
	global_load_lds_dwordx4 v[226:227], off
	v_lshl_add_u64 v[226:227], s[14:15], 0, v[136:137]
	s_mov_b32 m0, s21
	s_nop 0
	global_load_lds_dwordx4 v[226:227], off
	s_waitcnt vmcnt(8)
	s_waitcnt lgkmcnt(0)
	s_barrier
	s_setprio 1
	s_waitcnt lgkmcnt(0)
	v_mfma_f32_16x16x32_bf16 v[126:129], v[152:155], v[184:187], v[126:129]
	v_mfma_f32_16x16x32_bf16 v[122:125], v[160:163], v[184:187], v[122:125]
	v_mfma_f32_16x16x32_bf16 v[114:117], v[152:155], v[192:195], v[114:117]
	v_mfma_f32_16x16x32_bf16 v[106:109], v[160:163], v[192:195], v[106:109]
	v_mfma_f32_16x16x32_bf16 v[98:101], v[152:155], v[204:207], v[98:101]
	v_mfma_f32_16x16x32_bf16 v[90:93], v[160:163], v[204:207], v[90:93]
	v_mfma_f32_16x16x32_bf16 v[82:85], v[152:155], v[212:215], v[82:85]
	v_mfma_f32_16x16x32_bf16 v[74:77], v[160:163], v[212:215], v[74:77]
	v_mfma_f32_16x16x32_bf16 v[126:129], v[156:159], v[188:191], v[126:129]
	v_mfma_f32_16x16x32_bf16 v[122:125], v[164:167], v[188:191], v[122:125]
	v_mfma_f32_16x16x32_bf16 v[114:117], v[156:159], v[200:203], v[114:117]
	v_mfma_f32_16x16x32_bf16 v[106:109], v[164:167], v[200:203], v[106:109]
	v_mfma_f32_16x16x32_bf16 v[98:101], v[156:159], v[208:211], v[98:101]
	v_mfma_f32_16x16x32_bf16 v[90:93], v[164:167], v[208:211], v[90:93]
	v_mfma_f32_16x16x32_bf16 v[82:85], v[156:159], v[216:219], v[82:85]
	v_mfma_f32_16x16x32_bf16 v[74:77], v[164:167], v[216:219], v[74:77]
	s_setprio 0
	s_setprio 1
	v_mfma_f32_16x16x32_bf16 v[118:121], v[168:171], v[184:187], v[118:121]
	v_mfma_f32_16x16x32_bf16 v[110:113], v[176:179], v[184:187], v[110:113]
	v_mfma_f32_16x16x32_bf16 v[102:105], v[168:171], v[192:195], v[102:105]
	v_mfma_f32_16x16x32_bf16 v[94:97], v[176:179], v[192:195], v[94:97]
	v_mfma_f32_16x16x32_bf16 v[86:89], v[168:171], v[204:207], v[86:89]
	v_mfma_f32_16x16x32_bf16 v[78:81], v[176:179], v[204:207], v[78:81]
	v_mfma_f32_16x16x32_bf16 v[62:65], v[168:171], v[212:215], v[62:65]
	v_mfma_f32_16x16x32_bf16 v[58:61], v[176:179], v[212:215], v[58:61]
	v_mfma_f32_16x16x32_bf16 v[118:121], v[172:175], v[188:191], v[118:121]
	v_mfma_f32_16x16x32_bf16 v[110:113], v[180:183], v[188:191], v[110:113]
	v_mfma_f32_16x16x32_bf16 v[102:105], v[172:175], v[200:203], v[102:105]
	v_mfma_f32_16x16x32_bf16 v[94:97], v[180:183], v[200:203], v[94:97]
	v_mfma_f32_16x16x32_bf16 v[86:89], v[172:175], v[208:211], v[86:89]
	v_mfma_f32_16x16x32_bf16 v[78:81], v[180:183], v[208:211], v[78:81]
	v_mfma_f32_16x16x32_bf16 v[62:65], v[172:175], v[216:219], v[62:65]
	v_mfma_f32_16x16x32_bf16 v[58:61], v[180:183], v[216:219], v[58:61]
	s_setprio 0
	s_barrier
; #define PG8_STAGE(bufoff, gbase, voff) do { _Pragma("unroll") for (int _i = 0; _i < 2; ++_i) \
;         __builtin_amdgcn_global_load_lds((const unsigned*)((const char*)(gbase) + (voff)[_i]), (LAS unsigned*)(lds + (bufoff) + ldsw + _i * 8192), 16, 0, 0); } while (0)
; #define PG8_LDA(dst, b, h) do { if constexpr (F8) { _Pragma("unroll") for (int m = 0; m < 4; ++m) dst##8[m] = PG8_LD8(lds, PG8_SA(b, h) + aoff + m * 2048); } \
;         else { _Pragma("unroll") for (int m = 0; m < 4; ++m) _Pragma("unroll") for (int k = 0; k < 2; ++k) dst[m][k] = *(const LAS bf16x8*)(lds + PG8_SA(b, h) + aoff + m * 2048 + k * 1024); } } while (0)
; #define PG8_WAIT_V(n) asm volatile("s_waitcnt vmcnt(" #n ")" ::: "memory")
; #define PG8_WAIT_L(n) asm volatile("s_waitcnt lgkmcnt(" #n ")" ::: "memory")
; #define PG8_BAR __builtin_amdgcn_s_barrier()
; #define PG8_SCHED __builtin_amdgcn_sched_barrier(0)
; template <bool GATHER, bool F8, class Epi, class Sched>
; __device__ __forceinline__ void gemm_phase(LAS unsigned char* lds, const int nt, const unsigned lda, const unsigned ldb, const Sched& S, const Epi& E) {
;     ...
;             PG8_LDA(At, 1, 1); PG8_STAGE(PG8_SB(1, 0), b3, voffB); PG8_STAGE(PG8_SB(1, 1), b3 + hB, voffB); PG8_STAGE(PG8_SA(1, 0), a3, w0);
;             PG8_WAIT_V(8); PG8_WAIT_L(0); PG8_BAR; PG8_MMA(1, 0, At, B0); PG8_MMA(1, 1, At, B1); PG8_BAR; PG8_SCHED;
;         }
;         if (wr == 0) PG8_BAR;
	s_mov_b32 m0, s34
	v_lshl_add_u64 v[196:197], v[196:197], 0, s[8:9]
	s_add_u32 s12, s12, 0x80080
	ds_read_b128 v[184:187], v149 offset:49152
	ds_read_b128 v[188:191], v149 offset:50176
	ds_read_b128 v[192:195], v149 offset:51200
	ds_read_b128 v[200:203], v149 offset:52224
	ds_read_b128 v[204:207], v149 offset:53248
	ds_read_b128 v[208:211], v149 offset:54272
	ds_read_b128 v[212:215], v149 offset:55296
	ds_read_b128 v[216:219], v149 offset:56320
	global_load_lds_dwordx4 v[196:197], off
	v_lshl_add_u64 v[196:197], v[220:221], 0, s[8:9]
	s_mov_b32 m0, s35
	s_addc_u32 s13, s13, 0
	global_load_lds_dwordx4 v[196:197], off
	v_lshl_add_u64 v[196:197], s[12:13], 0, v[134:135]
	s_mov_b32 m0, s36
	s_nop 0
	global_load_lds_dwordx4 v[196:197], off
	v_lshl_add_u64 v[196:197], s[12:13], 0, v[138:139]
	s_mov_b32 m0, s37
	s_nop 0
	global_load_lds_dwordx4 v[196:197], off
	v_lshl_add_u64 v[196:197], v[222:223], 0, s[8:9]
	s_mov_b32 m0, s22
	s_nop 0
	global_load_lds_dwordx4 v[196:197], off
	v_lshl_add_u64 v[196:197], v[224:225], 0, s[8:9]
	s_mov_b32 m0, s23
	s_nop 0
	global_load_lds_dwordx4 v[196:197], off
	s_waitcnt vmcnt(8)
	s_waitcnt lgkmcnt(0)
	s_barrier
	s_setprio 1
	s_waitcnt lgkmcnt(0)
	v_mfma_f32_16x16x32_bf16 v[54:57], v[152:155], v[184:187], v[54:57]
	v_mfma_f32_16x16x32_bf16 v[50:53], v[160:163], v[184:187], v[50:53]
	v_mfma_f32_16x16x32_bf16 v[30:33], v[152:155], v[192:195], v[30:33]
	v_mfma_f32_16x16x32_bf16 v[26:29], v[160:163], v[192:195], v[26:29]
	v_mfma_f32_16x16x32_bf16 v[14:17], v[152:155], v[204:207], v[14:17]
	v_mfma_f32_16x16x32_bf16 v[10:13], v[160:163], v[204:207], v[10:13]
	v_mfma_f32_16x16x32_bf16 v[6:9], v[152:155], v[212:215], v[6:9]
	v_mfma_f32_16x16x32_bf16 v[2:5], v[160:163], v[212:215], v[2:5]
	v_mfma_f32_16x16x32_bf16 v[54:57], v[156:159], v[188:191], v[54:57]
	v_mfma_f32_16x16x32_bf16 v[50:53], v[164:167], v[188:191], v[50:53]
	v_mfma_f32_16x16x32_bf16 v[30:33], v[156:159], v[200:203], v[30:33]
	v_mfma_f32_16x16x32_bf16 v[26:29], v[164:167], v[200:203], v[26:29]
	v_mfma_f32_16x16x32_bf16 v[14:17], v[156:159], v[208:211], v[14:17]
	v_mfma_f32_16x16x32_bf16 v[10:13], v[164:167], v[208:211], v[10:13]
	v_mfma_f32_16x16x32_bf16 v[6:9], v[156:159], v[216:219], v[6:9]
	v_mfma_f32_16x16x32_bf16 v[2:5], v[164:167], v[216:219], v[2:5]
	s_setprio 0
	s_setprio 1
	v_mfma_f32_16x16x32_bf16 v[66:69], v[168:171], v[184:187], v[66:69]
	v_mfma_f32_16x16x32_bf16 v[70:73], v[176:179], v[184:187], v[70:73]
	v_mfma_f32_16x16x32_bf16 v[42:45], v[168:171], v[192:195], v[42:45]
	v_mfma_f32_16x16x32_bf16 v[46:49], v[176:179], v[192:195], v[46:49]
	v_mfma_f32_16x16x32_bf16 v[34:37], v[168:171], v[204:207], v[34:37]
	v_mfma_f32_16x16x32_bf16 v[38:41], v[176:179], v[204:207], v[38:41]
	v_mfma_f32_16x16x32_bf16 v[18:21], v[168:171], v[212:215], v[18:21]
	v_mfma_f32_16x16x32_bf16 v[22:25], v[176:179], v[212:215], v[22:25]
	v_mfma_f32_16x16x32_bf16 v[66:69], v[172:175], v[188:191], v[66:69]
	v_mfma_f32_16x16x32_bf16 v[70:73], v[180:183], v[188:191], v[70:73]
	v_mfma_f32_16x16x32_bf16 v[42:45], v[172:175], v[200:203], v[42:45]
	v_mfma_f32_16x16x32_bf16 v[46:49], v[180:183], v[200:203], v[46:49]
	v_mfma_f32_16x16x32_bf16 v[34:37], v[172:175], v[208:211], v[34:37]
	v_mfma_f32_16x16x32_bf16 v[38:41], v[180:183], v[208:211], v[38:41]
	v_mfma_f32_16x16x32_bf16 v[18:21], v[172:175], v[216:219], v[18:21]
	v_mfma_f32_16x16x32_bf16 v[22:25], v[180:183], v[216:219], v[22:25]
	s_setprio 0
	s_add_i32 s26, s26, 2
	s_add_u32 s10, s10, 0x100
	s_addc_u32 s11, s11, 0
	s_cmp_gt_u32 s26, 29
	s_barrier
	s_cbranch_scc0 .LBB0_1152
	s_cmpk_lt_u32 s18, 0x100
	s_cbranch_scc0 .LBB0_1155
	s_barrier

; #define PG8_STAGE(bufoff, gbase, voff) do { _Pragma("unroll") for (int _i = 0; _i < 2; ++_i) \
;         __builtin_amdgcn_global_load_lds((const unsigned*)((const char*)(gbase) + (voff)[_i]), (LAS unsigned*)(lds + (bufoff) + ldsw + _i * 8192), 16, 0, 0); } while (0)
; #define PG8_LDA(dst, b, h) do { if constexpr (F8) { _Pragma("unroll") for (int m = 0; m < 4; ++m) dst##8[m] = PG8_LD8(lds, PG8_SA(b, h) + aoff + m * 2048); } \
;         else { _Pragma("unroll") for (int m = 0; m < 4; ++m) _Pragma("unroll") for (int k = 0; k < 2; ++k) dst[m][k] = *(const LAS bf16x8*)(lds + PG8_SA(b, h) + aoff + m * 2048 + k * 1024); } } while (0)
; #define PG8_WAIT_V(n) asm volatile("s_waitcnt vmcnt(" #n ")" ::: "memory")
; #define PG8_WAIT_L(n) asm volatile("s_waitcnt lgkmcnt(" #n ")" ::: "memory")
; #define PG8_BAR __builtin_amdgcn_s_barrier()
; #define PG8_SCHED __builtin_amdgcn_sched_barrier(0)
; template <bool GATHER, bool F8, class Epi, class Sched>
; __device__ __forceinline__ void gemm_phase(LAS unsigned char* lds, const int nt, const unsigned lda, const unsigned ldb, const Sched& S, const Epi& E) {
;     ...
;         for (int t = 0; t < nt; t += 2) {
;             const bool last = (t == nt - 2);
;             const char* a1 = cA + (size_t)(t + 1) * kstep;
;             const char* a2 = last ? nA : cA + (size_t)(t + 2) * kstep; const char* b2 = last ? nB : cB + (size_t)(t + 2) * kstep;
;             const char* a3 = a2 + kstep; const char* b3 = b2 + kstep;
;             unsigned w0[2], w1[2];
;             if constexpr (GATHER) {
; #pragma unroll
;                 for (int i = 0; i < 2; ++i) { w0[i] = last ? vN0[i] : vA0[i]; w1[i] = last ? vN1[i] : vA1[i]; }
;             } else {
; #pragma unroll
;                 for (int i = 0; i < 2; ++i) { w0[i] = voffA[i]; w1[i] = voffA[i]; }
;             }
;             PG8_LDB(B0, 0, 0); PG8_LDB(B1, 0, 1); PG8_SCHED; PG8_LDA(At, 0, 0); PG8_STAGE(PG8_SA(1, 1), a1 + hA, vA1);
;             PG8_WAIT_V(8); PG8_WAIT_L(0); PG8_BAR; PG8_MMA(0, 0, At, B0); PG8_MMA(0, 1, At, B1); PG8_BAR; PG8_SCHED;
;             PG8_LDA(At, 0, 1); PG8_STAGE(PG8_SB(0, 0), b2, voffB); PG8_STAGE(PG8_SB(0, 1), b2 + hB, voffB); PG8_STAGE(PG8_SA(0, 0), a2, w0);
;             PG8_WAIT_V(8); PG8_WAIT_L(0); PG8_BAR; PG8_MMA(1, 0, At, B0); PG8_MMA(1, 1, At, B1); PG8_BAR; PG8_SCHED;
.LBB0_1432:
	ds_read_b128 v[130:133], v184
	ds_read_b128 v[134:137], v184 offset:1024
	ds_read_b128 v[138:141], v184 offset:2048
	ds_read_b128 v[142:145], v184 offset:3072
	ds_read_b128 v[146:149], v185
	ds_read_b128 v[150:153], v185 offset:1024
	ds_read_b128 v[170:173], v185 offset:2048
	ds_read_b128 v[174:177], v185 offset:3072
	s_add_u32 s28, s26, 0xfffe0080
	s_addc_u32 s29, s27, -1
	s_cmp_eq_u32 s53, 4
	s_cselect_b32 s31, s1, s29
	s_cselect_b32 s30, s0, s28
	s_cselect_b32 s29, s23, s34
	s_cselect_b32 s28, s22, s25
	s_add_i32 m0, s40, 0xc000
	ds_read_b128 v[178:181], v186
	ds_read_b128 v[190:193], v186 offset:1024
	ds_read_b128 v[194:197], v186 offset:2048
	ds_read_b128 v[200:203], v186 offset:3072
	ds_read_b128 v[204:207], v186 offset:4096
	ds_read_b128 v[208:211], v186 offset:5120
	ds_read_b128 v[212:215], v186 offset:6144
	ds_read_b128 v[216:219], v186 offset:7168
	global_load_lds_dwordx4 v162, s[26:27]
	s_add_i32 m0, s40, 0xe000
	s_nop 0
	global_load_lds_dwordx4 v164, s[26:27]
	s_waitcnt vmcnt(8)
	s_waitcnt lgkmcnt(0)
	s_barrier
	s_setprio 1
	s_waitcnt lgkmcnt(0)
	v_mfma_f32_16x16x32_bf16 v[126:129], v[130:133], v[178:181], v[126:129]
	v_mfma_f32_16x16x32_bf16 v[122:125], v[138:141], v[178:181], v[122:125]
	v_mfma_f32_16x16x32_bf16 v[110:113], v[130:133], v[194:197], v[110:113]
	v_mfma_f32_16x16x32_bf16 v[106:109], v[138:141], v[194:197], v[106:109]
	v_mfma_f32_16x16x32_bf16 v[94:97], v[130:133], v[204:207], v[94:97]
	v_mfma_f32_16x16x32_bf16 v[90:93], v[138:141], v[204:207], v[90:93]
	v_mfma_f32_16x16x32_bf16 v[78:81], v[130:133], v[212:215], v[78:81]
	v_mfma_f32_16x16x32_bf16 v[74:77], v[138:141], v[212:215], v[74:77]
	v_mfma_f32_16x16x32_bf16 v[126:129], v[134:137], v[190:193], v[126:129]
	v_mfma_f32_16x16x32_bf16 v[122:125], v[142:145], v[190:193], v[122:125]
	v_mfma_f32_16x16x32_bf16 v[110:113], v[134:137], v[200:203], v[110:113]
	v_mfma_f32_16x16x32_bf16 v[106:109], v[142:145], v[200:203], v[106:109]
	v_mfma_f32_16x16x32_bf16 v[94:97], v[134:137], v[208:211], v[94:97]
	v_mfma_f32_16x16x32_bf16 v[90:93], v[142:145], v[208:211], v[90:93]
	v_mfma_f32_16x16x32_bf16 v[78:81], v[134:137], v[216:219], v[78:81]
	v_mfma_f32_16x16x32_bf16 v[74:77], v[142:145], v[216:219], v[74:77]
	s_setprio 0
	s_setprio 1
	v_mfma_f32_16x16x32_bf16 v[118:121], v[146:149], v[178:181], v[118:121]
	v_mfma_f32_16x16x32_bf16 v[114:117], v[170:173], v[178:181], v[114:117]
	v_mfma_f32_16x16x32_bf16 v[102:105], v[146:149], v[194:197], v[102:105]
	v_mfma_f32_16x16x32_bf16 v[98:101], v[170:173], v[194:197], v[98:101]
	v_mfma_f32_16x16x32_bf16 v[86:89], v[146:149], v[204:207], v[86:89]
	v_mfma_f32_16x16x32_bf16 v[82:85], v[170:173], v[204:207], v[82:85]
	v_mfma_f32_16x16x32_bf16 v[70:73], v[146:149], v[212:215], v[70:73]
	v_mfma_f32_16x16x32_bf16 v[66:69], v[170:173], v[212:215], v[66:69]
	v_mfma_f32_16x16x32_bf16 v[118:121], v[150:153], v[190:193], v[118:121]
	v_mfma_f32_16x16x32_bf16 v[114:117], v[174:177], v[190:193], v[114:117]
	v_mfma_f32_16x16x32_bf16 v[102:105], v[150:153], v[200:203], v[102:105]
	v_mfma_f32_16x16x32_bf16 v[98:101], v[174:177], v[200:203], v[98:101]
	v_mfma_f32_16x16x32_bf16 v[86:89], v[150:153], v[208:211], v[86:89]
	v_mfma_f32_16x16x32_bf16 v[82:85], v[174:177], v[208:211], v[82:85]
	v_mfma_f32_16x16x32_bf16 v[70:73], v[150:153], v[216:219], v[70:73]
	v_mfma_f32_16x16x32_bf16 v[66:69], v[174:177], v[216:219], v[66:69]
	s_setprio 0
	s_barrier
	s_add_i32 s54, s48, s39
	s_mov_b32 m0, s54
	ds_read_b128 v[178:181], v186 offset:16384
	ds_read_b128 v[190:193], v186 offset:17408
	ds_read_b128 v[194:197], v186 offset:18432
	ds_read_b128 v[200:203], v186 offset:19456
	ds_read_b128 v[204:207], v186 offset:20480
	ds_read_b128 v[208:211], v186 offset:21504
	ds_read_b128 v[212:215], v186 offset:22528
	ds_read_b128 v[216:219], v186 offset:23552
	global_load_lds_dwordx4 v156, s[28:29]
	s_add_i32 m0, s54, 0x2000
	s_add_u32 s54, s28, 0x20000
	s_addc_u32 s55, s29, 0
	s_add_i32 s56, s49, s39
	global_load_lds_dwordx4 v160, s[28:29]
	s_mov_b32 m0, s56
	s_nop 0
	global_load_lds_dwordx4 v156, s[54:55]
	s_add_i32 m0, s56, 0x2000
	s_nop 0
	global_load_lds_dwordx4 v160, s[54:55]
	s_mov_b32 m0, s40
	s_nop 0
	s_mov_b64 s[98:99], s[30:31]
	global_load_lds_dwordx4 v154, s[30:31]
	s_mov_b32 m0, s41
	s_nop 0
	global_load_lds_dwordx4 v158, s[30:31]
	s_waitcnt vmcnt(8)
	s_waitcnt lgkmcnt(0)
	s_barrier
	s_setprio 1
	s_waitcnt lgkmcnt(0)
	v_mfma_f32_16x16x32_bf16 v[54:57], v[130:133], v[178:181], v[54:57]
	v_mfma_f32_16x16x32_bf16 v[50:53], v[138:141], v[178:181], v[50:53]
	v_mfma_f32_16x16x32_bf16 v[46:49], v[130:133], v[194:197], v[46:49]
	v_mfma_f32_16x16x32_bf16 v[34:37], v[138:141], v[194:197], v[34:37]
	v_mfma_f32_16x16x32_bf16 v[22:25], v[130:133], v[204:207], v[22:25]
	v_mfma_f32_16x16x32_bf16 v[18:21], v[138:141], v[204:207], v[18:21]
	v_mfma_f32_16x16x32_bf16 v[6:9], v[130:133], v[212:215], v[6:9]
	v_mfma_f32_16x16x32_bf16 v[2:5], v[138:141], v[212:215], v[2:5]
	v_mfma_f32_16x16x32_bf16 v[54:57], v[134:137], v[190:193], v[54:57]
	v_mfma_f32_16x16x32_bf16 v[50:53], v[142:145], v[190:193], v[50:53]
	v_mfma_f32_16x16x32_bf16 v[46:49], v[134:137], v[200:203], v[46:49]
	v_mfma_f32_16x16x32_bf16 v[34:37], v[142:145], v[200:203], v[34:37]
	v_mfma_f32_16x16x32_bf16 v[22:25], v[134:137], v[208:211], v[22:25]
	v_mfma_f32_16x16x32_bf16 v[18:21], v[142:145], v[208:211], v[18:21]
	v_mfma_f32_16x16x32_bf16 v[6:9], v[134:137], v[216:219], v[6:9]
	v_mfma_f32_16x16x32_bf16 v[2:5], v[142:145], v[216:219], v[2:5]
	s_setprio 0
	s_setprio 1
	v_mfma_f32_16x16x32_bf16 v[62:65], v[146:149], v[178:181], v[62:65]
	v_mfma_f32_16x16x32_bf16 v[58:61], v[170:173], v[178:181], v[58:61]
	v_mfma_f32_16x16x32_bf16 v[42:45], v[146:149], v[194:197], v[42:45]
	v_mfma_f32_16x16x32_bf16 v[38:41], v[170:173], v[194:197], v[38:41]
	v_mfma_f32_16x16x32_bf16 v[30:33], v[146:149], v[204:207], v[30:33]
	v_mfma_f32_16x16x32_bf16 v[26:29], v[170:173], v[204:207], v[26:29]
	v_mfma_f32_16x16x32_bf16 v[14:17], v[146:149], v[212:215], v[14:17]
	v_mfma_f32_16x16x32_bf16 v[10:13], v[170:173], v[212:215], v[10:13]
	v_mfma_f32_16x16x32_bf16 v[62:65], v[150:153], v[190:193], v[62:65]
	v_mfma_f32_16x16x32_bf16 v[58:61], v[174:177], v[190:193], v[58:61]
	v_mfma_f32_16x16x32_bf16 v[42:45], v[150:153], v[200:203], v[42:45]
	v_mfma_f32_16x16x32_bf16 v[38:41], v[174:177], v[200:203], v[38:41]
	v_mfma_f32_16x16x32_bf16 v[30:33], v[150:153], v[208:211], v[30:33]
	v_mfma_f32_16x16x32_bf16 v[26:29], v[174:177], v[208:211], v[26:29]
	v_mfma_f32_16x16x32_bf16 v[14:17], v[150:153], v[216:219], v[14:17]
	v_mfma_f32_16x16x32_bf16 v[10:13], v[174:177], v[216:219], v[10:13]
	s_setprio 0
	s_barrier
; #define PG8_STAGE(bufoff, gbase, voff) do { _Pragma("unroll") for (int _i = 0; _i < 2; ++_i) \
;         __builtin_amdgcn_global_load_lds((const unsigned*)((const char*)(gbase) + (voff)[_i]), (LAS unsigned*)(lds + (bufoff) + ldsw + _i * 8192), 16, 0, 0); } while (0)
; #define PG8_LDA(dst, b, h) do { if constexpr (F8) { _Pragma("unroll") for (int m = 0; m < 4; ++m) dst##8[m] = PG8_LD8(lds, PG8_SA(b, h) + aoff + m * 2048); } \
;         else { _Pragma("unroll") for (int m = 0; m < 4; ++m) _Pragma("unroll") for (int k = 0; k < 2; ++k) dst[m][k] = *(const LAS bf16x8*)(lds + PG8_SA(b, h) + aoff + m * 2048 + k * 1024); } } while (0)
; #define PG8_LDB(dst, b, h) do { if constexpr (F8) { _Pragma("unroll") for (int n = 0; n < 2; ++n) dst##8[n] = PG8_LD8(ldsB, PG8_SBR(b, h) + boff + n * 2048); } \
;         else { _Pragma("unroll") for (int n = 0; n < 2; ++n) _Pragma("unroll") for (int k = 0; k < 2; ++k) dst[n][k] = *(const LAS bf16x8*)(ldsB + PG8_SBR(b, h) + boff + n * 2048 + k * 1024); } } while (0)
; #define PG8_WAIT_V(n) asm volatile("s_waitcnt vmcnt(" #n ")" ::: "memory")
; #define PG8_WAIT_L(n) asm volatile("s_waitcnt lgkmcnt(" #n ")" ::: "memory")
; #define PG8_BAR __builtin_amdgcn_s_barrier()
; #define PG8_SCHED __builtin_amdgcn_sched_barrier(0)
; template <bool GATHER, bool F8, class Epi, class Sched>
; __device__ __forceinline__ void gemm_phase(LAS unsigned char* lds, const int nt, const unsigned lda, const unsigned ldb, const Sched& S, const Epi& E) {
;     ...
;             PG8_LDB(B0, 1, 0); PG8_LDB(B1, 1, 1); PG8_SCHED; PG8_LDA(At, 1, 0); PG8_STAGE(PG8_SA(0, 1), a2 + hA, w1);
;             PG8_WAIT_V(8); PG8_WAIT_L(0); PG8_BAR; PG8_MMA(0, 0, At, B0); PG8_MMA(0, 1, At, B1); PG8_BAR; PG8_SCHED;
;             PG8_LDA(At, 1, 1); PG8_STAGE(PG8_SB(1, 0), b3, voffB); PG8_STAGE(PG8_SB(1, 1), b3 + hB, voffB); PG8_STAGE(PG8_SA(1, 0), a3, w0);
;             PG8_WAIT_V(8); PG8_WAIT_L(0); PG8_BAR; PG8_MMA(1, 0, At, B0); PG8_MMA(1, 1, At, B1); PG8_BAR; PG8_SCHED;
;         }
;         if (wr == 0) PG8_BAR;
	s_add_i32 s54, 0, 0x18000
	s_add_i32 s55, 0, 0x1c000
	v_add_u32_e32 v142, s54, v182
	v_add_u32_e32 v174, s55, v182
	ds_read_b128 v[130:133], v142
	ds_read_b128 v[134:137], v142 offset:1024
	ds_read_b128 v[138:141], v142 offset:2048
	ds_read_b128 v[142:145], v142 offset:3072
	ds_read_b128 v[146:149], v174
	ds_read_b128 v[150:153], v174 offset:1024
	ds_read_b128 v[170:173], v174 offset:2048
	ds_read_b128 v[174:177], v174 offset:3072
	s_add_u32 s30, s30, 0x20000
	s_addc_u32 s31, s31, 0
	s_mov_b32 m0, s42
	ds_read_b128 v[178:181], v186 offset:32768
	ds_read_b128 v[190:193], v186 offset:33792
	ds_read_b128 v[194:197], v186 offset:34816
	ds_read_b128 v[200:203], v186 offset:35840
	ds_read_b128 v[204:207], v186 offset:36864
	ds_read_b128 v[208:211], v186 offset:37888
	ds_read_b128 v[212:215], v186 offset:38912
	ds_read_b128 v[216:219], v186 offset:39936
	global_load_lds_dwordx4 v154, s[30:31]
	s_mov_b32 m0, s43
	s_nop 0
	global_load_lds_dwordx4 v158, s[30:31]
	s_waitcnt vmcnt(8)
	s_waitcnt lgkmcnt(0)
	s_barrier
	s_setprio 1
	s_waitcnt lgkmcnt(0)
	v_mfma_f32_16x16x32_bf16 v[126:129], v[130:133], v[178:181], v[126:129]
	v_mfma_f32_16x16x32_bf16 v[122:125], v[138:141], v[178:181], v[122:125]
	v_mfma_f32_16x16x32_bf16 v[110:113], v[130:133], v[194:197], v[110:113]
	v_mfma_f32_16x16x32_bf16 v[106:109], v[138:141], v[194:197], v[106:109]
	v_mfma_f32_16x16x32_bf16 v[94:97], v[130:133], v[204:207], v[94:97]
	v_mfma_f32_16x16x32_bf16 v[90:93], v[138:141], v[204:207], v[90:93]
	v_mfma_f32_16x16x32_bf16 v[78:81], v[130:133], v[212:215], v[78:81]
	v_mfma_f32_16x16x32_bf16 v[74:77], v[138:141], v[212:215], v[74:77]
	v_mfma_f32_16x16x32_bf16 v[126:129], v[134:137], v[190:193], v[126:129]
	v_mfma_f32_16x16x32_bf16 v[122:125], v[142:145], v[190:193], v[122:125]
	v_mfma_f32_16x16x32_bf16 v[110:113], v[134:137], v[200:203], v[110:113]
	v_mfma_f32_16x16x32_bf16 v[106:109], v[142:145], v[200:203], v[106:109]
	v_mfma_f32_16x16x32_bf16 v[94:97], v[134:137], v[208:211], v[94:97]
	v_mfma_f32_16x16x32_bf16 v[90:93], v[142:145], v[208:211], v[90:93]
	v_mfma_f32_16x16x32_bf16 v[78:81], v[134:137], v[216:219], v[78:81]
	v_mfma_f32_16x16x32_bf16 v[74:77], v[142:145], v[216:219], v[74:77]
	s_setprio 0
	s_setprio 1
	v_mfma_f32_16x16x32_bf16 v[118:121], v[146:149], v[178:181], v[118:121]
	v_mfma_f32_16x16x32_bf16 v[114:117], v[170:173], v[178:181], v[114:117]
	v_mfma_f32_16x16x32_bf16 v[102:105], v[146:149], v[194:197], v[102:105]
	v_mfma_f32_16x16x32_bf16 v[98:101], v[170:173], v[194:197], v[98:101]
	v_mfma_f32_16x16x32_bf16 v[86:89], v[146:149], v[204:207], v[86:89]
	v_mfma_f32_16x16x32_bf16 v[82:85], v[170:173], v[204:207], v[82:85]
	v_mfma_f32_16x16x32_bf16 v[70:73], v[146:149], v[212:215], v[70:73]
	v_mfma_f32_16x16x32_bf16 v[66:69], v[170:173], v[212:215], v[66:69]
	v_mfma_f32_16x16x32_bf16 v[118:121], v[150:153], v[190:193], v[118:121]
	v_mfma_f32_16x16x32_bf16 v[114:117], v[174:177], v[190:193], v[114:117]
	v_mfma_f32_16x16x32_bf16 v[102:105], v[150:153], v[200:203], v[102:105]
	v_mfma_f32_16x16x32_bf16 v[98:101], v[174:177], v[200:203], v[98:101]
	v_mfma_f32_16x16x32_bf16 v[86:89], v[150:153], v[208:211], v[86:89]
	v_mfma_f32_16x16x32_bf16 v[82:85], v[174:177], v[208:211], v[82:85]
	v_mfma_f32_16x16x32_bf16 v[70:73], v[150:153], v[216:219], v[70:73]
	v_mfma_f32_16x16x32_bf16 v[66:69], v[174:177], v[216:219], v[66:69]
	s_setprio 0
	s_barrier
	s_add_i32 s30, s54, s39
	s_add_i32 m0, s30, 0xffffff80
	ds_read_b128 v[178:181], v186 offset:49152
	ds_read_b128 v[190:193], v186 offset:50176
	ds_read_b128 v[194:197], v186 offset:51200
	ds_read_b128 v[200:203], v186 offset:52224
	ds_read_b128 v[204:207], v186 offset:53248
	ds_read_b128 v[208:211], v186 offset:54272
	ds_read_b128 v[212:215], v186 offset:55296
	ds_read_b128 v[216:219], v186 offset:56320
	global_load_lds_dwordx4 v156, s[28:29] offset:128
	s_add_i32 m0, s30, 0x1f80
	s_add_i32 s30, s55, s39
	global_load_lds_dwordx4 v160, s[28:29] offset:128
	s_add_u32 s28, s28, 0x20080
	s_addc_u32 s29, s29, 0
	s_mov_b32 m0, s30
	s_nop 0
	global_load_lds_dwordx4 v156, s[28:29]
	s_add_i32 m0, s30, 0x2000
	s_nop 0
	global_load_lds_dwordx4 v160, s[28:29]
	s_add_i32 m0, s45, 0xffffff80
	s_nop 0
	global_load_lds_dwordx4 v154, s[98:99] offset:128
	s_add_i32 m0, s46, 0xffffff80
	s_nop 0
	global_load_lds_dwordx4 v158, s[98:99] offset:128
	s_waitcnt vmcnt(8)
	s_waitcnt lgkmcnt(0)
	s_barrier
	s_setprio 1
	s_waitcnt lgkmcnt(0)
	v_mfma_f32_16x16x32_bf16 v[54:57], v[130:133], v[178:181], v[54:57]
	v_mfma_f32_16x16x32_bf16 v[50:53], v[138:141], v[178:181], v[50:53]
	v_mfma_f32_16x16x32_bf16 v[46:49], v[130:133], v[194:197], v[46:49]
	v_mfma_f32_16x16x32_bf16 v[34:37], v[138:141], v[194:197], v[34:37]
	v_mfma_f32_16x16x32_bf16 v[22:25], v[130:133], v[204:207], v[22:25]
	v_mfma_f32_16x16x32_bf16 v[18:21], v[138:141], v[204:207], v[18:21]
	v_mfma_f32_16x16x32_bf16 v[6:9], v[130:133], v[212:215], v[6:9]
	v_mfma_f32_16x16x32_bf16 v[2:5], v[138:141], v[212:215], v[2:5]
	v_mfma_f32_16x16x32_bf16 v[54:57], v[134:137], v[190:193], v[54:57]
	v_mfma_f32_16x16x32_bf16 v[50:53], v[142:145], v[190:193], v[50:53]
	v_mfma_f32_16x16x32_bf16 v[46:49], v[134:137], v[200:203], v[46:49]
	v_mfma_f32_16x16x32_bf16 v[34:37], v[142:145], v[200:203], v[34:37]
	v_mfma_f32_16x16x32_bf16 v[22:25], v[134:137], v[208:211], v[22:25]
	v_mfma_f32_16x16x32_bf16 v[18:21], v[142:145], v[208:211], v[18:21]
	v_mfma_f32_16x16x32_bf16 v[6:9], v[134:137], v[216:219], v[6:9]
	v_mfma_f32_16x16x32_bf16 v[2:5], v[142:145], v[216:219], v[2:5]
	s_setprio 0
	s_setprio 1
	v_mfma_f32_16x16x32_bf16 v[62:65], v[146:149], v[178:181], v[62:65]
	v_mfma_f32_16x16x32_bf16 v[58:61], v[170:173], v[178:181], v[58:61]
	v_mfma_f32_16x16x32_bf16 v[42:45], v[146:149], v[194:197], v[42:45]
	v_mfma_f32_16x16x32_bf16 v[38:41], v[170:173], v[194:197], v[38:41]
	v_mfma_f32_16x16x32_bf16 v[30:33], v[146:149], v[204:207], v[30:33]
	v_mfma_f32_16x16x32_bf16 v[26:29], v[170:173], v[204:207], v[26:29]
	v_mfma_f32_16x16x32_bf16 v[14:17], v[146:149], v[212:215], v[14:17]
	v_mfma_f32_16x16x32_bf16 v[10:13], v[170:173], v[212:215], v[10:13]
	v_mfma_f32_16x16x32_bf16 v[62:65], v[150:153], v[190:193], v[62:65]
	v_mfma_f32_16x16x32_bf16 v[58:61], v[174:177], v[190:193], v[58:61]
	v_mfma_f32_16x16x32_bf16 v[42:45], v[150:153], v[200:203], v[42:45]
	v_mfma_f32_16x16x32_bf16 v[38:41], v[174:177], v[200:203], v[38:41]
	v_mfma_f32_16x16x32_bf16 v[30:33], v[150:153], v[208:211], v[30:33]
	v_mfma_f32_16x16x32_bf16 v[26:29], v[174:177], v[208:211], v[26:29]
	v_mfma_f32_16x16x32_bf16 v[14:17], v[150:153], v[216:219], v[14:17]
	v_mfma_f32_16x16x32_bf16 v[10:13], v[174:177], v[216:219], v[10:13]
	s_setprio 0
	s_add_i32 s53, s53, 2
	s_add_u32 s26, s26, 0x100
	s_addc_u32 s27, s27, 0
	s_add_u32 s25, s25, 0x100
	s_addc_u32 s34, s34, 0
	s_cmp_gt_u32 s53, 5
	s_barrier
	s_cbranch_scc0 .LBB0_1432
	s_and_b64 vcc, exec, s[20:21]
	s_cbranch_vccz .LBB0_1435
	s_barrier

; #define PG8_STAGE(bufoff, gbase, voff) do { _Pragma("unroll") for (int _i = 0; _i < 2; ++_i) \
;         __builtin_amdgcn_global_load_lds((const unsigned*)((const char*)(gbase) + (voff)[_i]), (LAS unsigned*)(lds + (bufoff) + ldsw + _i * 8192), 16, 0, 0); } while (0)
; #define PG8_LDA(dst, b, h) do { if constexpr (F8) { _Pragma("unroll") for (int m = 0; m < 4; ++m) dst##8[m] = PG8_LD8(lds, PG8_SA(b, h) + aoff + m * 2048); } \
;         else { _Pragma("unroll") for (int m = 0; m < 4; ++m) _Pragma("unroll") for (int k = 0; k < 2; ++k) dst[m][k] = *(const LAS bf16x8*)(lds + PG8_SA(b, h) + aoff + m * 2048 + k * 1024); } } while (0)
; #define PG8_LDB(dst, b, h) do { if constexpr (F8) { _Pragma("unroll") for (int n = 0; n < 2; ++n) dst##8[n] = PG8_LD8(ldsB, PG8_SBR(b, h) + boff + n * 2048); } \
;         else { _Pragma("unroll") for (int n = 0; n < 2; ++n) _Pragma("unroll") for (int k = 0; k < 2; ++k) dst[n][k] = *(const LAS bf16x8*)(ldsB + PG8_SBR(b, h) + boff + n * 2048 + k * 1024); } } while (0)
; #define PG8_WAIT_V(n) asm volatile("s_waitcnt vmcnt(" #n ")" ::: "memory")
; #define PG8_WAIT_L(n) asm volatile("s_waitcnt lgkmcnt(" #n ")" ::: "memory")
; #define PG8_BAR __builtin_amdgcn_s_barrier()
; #define PG8_SCHED __builtin_amdgcn_sched_barrier(0)
; template <bool GATHER, bool F8, class Epi, class Sched>
; __device__ __forceinline__ void gemm_phase(LAS unsigned char* lds, const int nt, const unsigned lda, const unsigned ldb, const Sched& S, const Epi& E) {
;     ...
;                 for (int i = 0; i < 2; ++i) { w0[i] = last ? vN0[i] : vA0[i]; w1[i] = last ? vN1[i] : vA1[i]; }
;             } else {
; #pragma unroll
;                 for (int i = 0; i < 2; ++i) { w0[i] = voffA[i]; w1[i] = voffA[i]; }
;             }
;             PG8_LDB(B0, 0, 0); PG8_LDB(B1, 0, 1); PG8_SCHED; PG8_LDA(At, 0, 0); PG8_STAGE(PG8_SA(1, 1), a1 + hA, vA1);
;             PG8_WAIT_V(8); PG8_WAIT_L(0); PG8_BAR; PG8_MMA(0, 0, At, B0); PG8_MMA(0, 1, At, B1); PG8_BAR; PG8_SCHED;
;             PG8_LDA(At, 0, 1); PG8_STAGE(PG8_SB(0, 0), b2, voffB); PG8_STAGE(PG8_SB(0, 1), b2 + hB, voffB); PG8_STAGE(PG8_SA(0, 0), a2, w0);
;             PG8_WAIT_V(8); PG8_WAIT_L(0); PG8_BAR; PG8_MMA(1, 0, At, B0); PG8_MMA(1, 1, At, B1); PG8_BAR; PG8_SCHED;
.Lp10_not_last:
	s_and_b64 s[34:35], vcc, exec
	v_cndmask_b32_e32 v164, v209, v208, vcc
	s_cselect_b32 s37, s23, s37
	s_cselect_b32 s36, s22, s36
	v_cndmask_b32_e32 v173, v172, v205, vcc
	v_cndmask_b32_e32 v242, v170, v207, vcc
	v_cndmask_b32_e32 v175, v174, v206, vcc
	s_cselect_b32 s35, s25, s68
	s_cselect_b32 s34, s24, s67
	s_add_i32 m0, s40, 0xbf80
	ds_read_b128 v[180:183], v202
	ds_read_b128 v[184:187], v202 offset:1024
	ds_read_b128 v[210:213], v202 offset:2048
	ds_read_b128 v[214:217], v202 offset:3072
	ds_read_b128 v[218:221], v202 offset:4096
	ds_read_b128 v[222:225], v202 offset:5120
	ds_read_b128 v[226:229], v202 offset:6144
	ds_read_b128 v[230:233], v202 offset:7168
	global_load_lds_dwordx4 v172, s[100:101] offset:128
	s_add_i32 m0, s40, 0xdf80
	s_nop 0
	global_load_lds_dwordx4 v174, s[100:101] offset:128
	s_waitcnt vmcnt(8)
	s_waitcnt lgkmcnt(0)
	s_barrier
	s_setprio 1
	s_waitcnt lgkmcnt(0)
	v_mfma_scale_f32_16x16x128_f8f6f4 v[158:161], v[18:25], v[180:187], v[158:161], v203, v203 op_sel_hi:[0,0,0]
	v_mfma_scale_f32_16x16x128_f8f6f4 v[150:153], v[26:33], v[180:187], v[150:153], v203, v203 op_sel_hi:[0,0,0]
	v_mfma_scale_f32_16x16x128_f8f6f4 v[142:145], v[18:25], v[210:217], v[142:145], v203, v203 op_sel_hi:[0,0,0]
	v_mfma_scale_f32_16x16x128_f8f6f4 v[134:137], v[26:33], v[210:217], v[134:137], v203, v203 op_sel_hi:[0,0,0]
	v_mfma_scale_f32_16x16x128_f8f6f4 v[126:129], v[18:25], v[218:225], v[126:129], v203, v203 op_sel_hi:[0,0,0]
	v_mfma_scale_f32_16x16x128_f8f6f4 v[118:121], v[26:33], v[218:225], v[118:121], v203, v203 op_sel_hi:[0,0,0]
	v_mfma_scale_f32_16x16x128_f8f6f4 v[110:113], v[18:25], v[226:233], v[110:113], v203, v203 op_sel_hi:[0,0,0]
	v_mfma_scale_f32_16x16x128_f8f6f4 v[102:105], v[26:33], v[226:233], v[102:105], v203, v203 op_sel_hi:[0,0,0]
	s_setprio 0
	s_setprio 1
	v_mfma_scale_f32_16x16x128_f8f6f4 v[154:157], v[2:9], v[180:187], v[154:157], v203, v203 op_sel_hi:[0,0,0]
	v_mfma_scale_f32_16x16x128_f8f6f4 v[146:149], v[10:17], v[180:187], v[146:149], v203, v203 op_sel_hi:[0,0,0]
	v_mfma_scale_f32_16x16x128_f8f6f4 v[138:141], v[2:9], v[210:217], v[138:141], v203, v203 op_sel_hi:[0,0,0]
	v_mfma_scale_f32_16x16x128_f8f6f4 v[130:133], v[10:17], v[210:217], v[130:133], v203, v203 op_sel_hi:[0,0,0]
	v_mfma_scale_f32_16x16x128_f8f6f4 v[122:125], v[2:9], v[218:225], v[122:125], v203, v203 op_sel_hi:[0,0,0]
	v_mfma_scale_f32_16x16x128_f8f6f4 v[114:117], v[10:17], v[218:225], v[114:117], v203, v203 op_sel_hi:[0,0,0]
	v_mfma_scale_f32_16x16x128_f8f6f4 v[106:109], v[2:9], v[226:233], v[106:109], v203, v203 op_sel_hi:[0,0,0]
	v_mfma_scale_f32_16x16x128_f8f6f4 v[98:101], v[10:17], v[226:233], v[98:101], v203, v203 op_sel_hi:[0,0,0]
	s_setprio 0
	s_barrier
	s_mov_b32 m0, s41
	s_add_u32 s68, s34, 0x40000
	ds_read_b128 v[210:213], v202 offset:16384
	ds_read_b128 v[214:217], v202 offset:17408
	ds_read_b128 v[218:221], v202 offset:18432
	ds_read_b128 v[222:225], v202 offset:19456
	ds_read_b128 v[226:229], v202 offset:20480
	ds_read_b128 v[230:233], v202 offset:21504
	ds_read_b128 v[234:237], v202 offset:22528
	ds_read_b128 v[238:241], v202 offset:23552
	global_load_lds_dwordx4 v166, s[34:35]
	s_mov_b32 m0, s42
	s_addc_u32 s69, s35, 0
	global_load_lds_dwordx4 v168, s[34:35]
	s_mov_b32 m0, s43
	s_nop 0
	global_load_lds_dwordx4 v166, s[68:69]
	s_mov_b32 m0, s44
	s_nop 0
	global_load_lds_dwordx4 v168, s[68:69]
	s_mov_b32 m0, s40
	s_nop 0
	global_load_lds_dwordx4 v164, s[36:37]
	s_mov_b32 m0, s45
	s_nop 0
	global_load_lds_dwordx4 v242, s[36:37]
	s_waitcnt vmcnt(8)
	s_waitcnt lgkmcnt(0)
	s_barrier
	s_setprio 1
	s_waitcnt lgkmcnt(0)
	v_mfma_scale_f32_16x16x128_f8f6f4 v[94:97], v[18:25], v[210:217], v[94:97], v203, v203 op_sel_hi:[0,0,0]
	v_mfma_scale_f32_16x16x128_f8f6f4 v[86:89], v[26:33], v[210:217], v[86:89], v203, v203 op_sel_hi:[0,0,0]
	v_mfma_scale_f32_16x16x128_f8f6f4 v[78:81], v[18:25], v[218:225], v[78:81], v203, v203 op_sel_hi:[0,0,0]
	v_mfma_scale_f32_16x16x128_f8f6f4 v[70:73], v[26:33], v[218:225], v[70:73], v203, v203 op_sel_hi:[0,0,0]
	v_mfma_scale_f32_16x16x128_f8f6f4 v[54:57], v[18:25], v[226:233], v[54:57], v203, v203 op_sel_hi:[0,0,0]
	v_mfma_scale_f32_16x16x128_f8f6f4 v[50:53], v[26:33], v[226:233], v[50:53], v203, v203 op_sel_hi:[0,0,0]
	v_mfma_scale_f32_16x16x128_f8f6f4 v[38:41], v[18:25], v[234:241], v[38:41], v203, v203 op_sel_hi:[0,0,0]
	v_mfma_scale_f32_16x16x128_f8f6f4 v[34:37], v[26:33], v[234:241], v[34:37], v203, v203 op_sel_hi:[0,0,0]
	s_setprio 0
	s_setprio 1
	v_mfma_scale_f32_16x16x128_f8f6f4 v[90:93], v[2:9], v[210:217], v[90:93], v203, v203 op_sel_hi:[0,0,0]
	v_mfma_scale_f32_16x16x128_f8f6f4 v[82:85], v[10:17], v[210:217], v[82:85], v203, v203 op_sel_hi:[0,0,0]
	v_mfma_scale_f32_16x16x128_f8f6f4 v[74:77], v[2:9], v[218:225], v[74:77], v203, v203 op_sel_hi:[0,0,0]
	v_mfma_scale_f32_16x16x128_f8f6f4 v[62:65], v[10:17], v[218:225], v[62:65], v203, v203 op_sel_hi:[0,0,0]
	v_mfma_scale_f32_16x16x128_f8f6f4 v[66:69], v[2:9], v[226:233], v[66:69], v203, v203 op_sel_hi:[0,0,0]
	v_mfma_scale_f32_16x16x128_f8f6f4 v[58:61], v[10:17], v[226:233], v[58:61], v203, v203 op_sel_hi:[0,0,0]
	v_mfma_scale_f32_16x16x128_f8f6f4 v[46:49], v[2:9], v[234:241], v[46:49], v203, v203 op_sel_hi:[0,0,0]
	v_mfma_scale_f32_16x16x128_f8f6f4 v[42:45], v[10:17], v[234:241], v[42:45], v203, v203 op_sel_hi:[0,0,0]
	s_setprio 0
	s_barrier
; #define PG8_STAGE(bufoff, gbase, voff) do { _Pragma("unroll") for (int _i = 0; _i < 2; ++_i) \
;         __builtin_amdgcn_global_load_lds((const unsigned*)((const char*)(gbase) + (voff)[_i]), (LAS unsigned*)(lds + (bufoff) + ldsw + _i * 8192), 16, 0, 0); } while (0)
; #define PG8_LDA(dst, b, h) do { if constexpr (F8) { _Pragma("unroll") for (int m = 0; m < 4; ++m) dst##8[m] = PG8_LD8(lds, PG8_SA(b, h) + aoff + m * 2048); } \
;         else { _Pragma("unroll") for (int m = 0; m < 4; ++m) _Pragma("unroll") for (int k = 0; k < 2; ++k) dst[m][k] = *(const LAS bf16x8*)(lds + PG8_SA(b, h) + aoff + m * 2048 + k * 1024); } } while (0)
; #define PG8_LDB(dst, b, h) do { if constexpr (F8) { _Pragma("unroll") for (int n = 0; n < 2; ++n) dst##8[n] = PG8_LD8(ldsB, PG8_SBR(b, h) + boff + n * 2048); } \
;         else { _Pragma("unroll") for (int n = 0; n < 2; ++n) _Pragma("unroll") for (int k = 0; k < 2; ++k) dst[n][k] = *(const LAS bf16x8*)(ldsB + PG8_SBR(b, h) + boff + n * 2048 + k * 1024); } } while (0)
; #define PG8_WAIT_V(n) asm volatile("s_waitcnt vmcnt(" #n ")" ::: "memory")
; #define PG8_WAIT_L(n) asm volatile("s_waitcnt lgkmcnt(" #n ")" ::: "memory")
; #define PG8_BAR __builtin_amdgcn_s_barrier()
; #define PG8_SCHED __builtin_amdgcn_sched_barrier(0)
; template <bool GATHER, bool F8, class Epi, class Sched>
; __device__ __forceinline__ void gemm_phase(LAS unsigned char* lds, const int nt, const unsigned lda, const unsigned ldb, const Sched& S, const Epi& E) {
;     ...
;             PG8_LDB(B0, 1, 0); PG8_LDB(B1, 1, 1); PG8_SCHED; PG8_LDA(At, 1, 0); PG8_STAGE(PG8_SA(0, 1), a2 + hA, w1);
;             PG8_WAIT_V(8); PG8_WAIT_L(0); PG8_BAR; PG8_MMA(0, 0, At, B0); PG8_MMA(0, 1, At, B1); PG8_BAR; PG8_SCHED;
;             PG8_LDA(At, 1, 1); PG8_STAGE(PG8_SB(1, 0), b3, voffB); PG8_STAGE(PG8_SB(1, 1), b3 + hB, voffB); PG8_STAGE(PG8_SA(1, 0), a3, w0);
;             PG8_WAIT_V(8); PG8_WAIT_L(0); PG8_BAR; PG8_MMA(1, 0, At, B0); PG8_MMA(1, 1, At, B1); PG8_BAR; PG8_SCHED;
;         }
;         if (wr == 0) PG8_BAR;
	ds_read_b128 v[2:5], v201 offset:32768
	ds_read_b128 v[6:9], v201 offset:33792
	ds_read_b128 v[10:13], v201 offset:34816
	ds_read_b128 v[14:17], v201 offset:35840
	ds_read_b128 v[18:21], v201 offset:49152
	ds_read_b128 v[22:25], v201 offset:50176
	ds_read_b128 v[26:29], v201 offset:51200
	ds_read_b128 v[30:33], v201 offset:52224
	s_mov_b32 m0, s46
	ds_read_b128 v[210:213], v202 offset:32768
	ds_read_b128 v[214:217], v202 offset:33792
	ds_read_b128 v[218:221], v202 offset:34816
	ds_read_b128 v[222:225], v202 offset:35840
	ds_read_b128 v[226:229], v202 offset:36864
	ds_read_b128 v[230:233], v202 offset:37888
	ds_read_b128 v[234:237], v202 offset:38912
	ds_read_b128 v[238:241], v202 offset:39936
	global_load_lds_dwordx4 v173, s[36:37]
	s_mov_b32 m0, s47
	s_nop 0
	global_load_lds_dwordx4 v175, s[36:37]
	s_waitcnt vmcnt(8)
	s_waitcnt lgkmcnt(0)
	s_barrier
	s_setprio 1
	s_waitcnt lgkmcnt(0)
	v_mfma_scale_f32_16x16x128_f8f6f4 v[158:161], v[2:9], v[210:217], v[158:161], v203, v203 op_sel_hi:[0,0,0]
	v_mfma_scale_f32_16x16x128_f8f6f4 v[150:153], v[10:17], v[210:217], v[150:153], v203, v203 op_sel_hi:[0,0,0]
	v_mfma_scale_f32_16x16x128_f8f6f4 v[142:145], v[2:9], v[218:225], v[142:145], v203, v203 op_sel_hi:[0,0,0]
	v_mfma_scale_f32_16x16x128_f8f6f4 v[134:137], v[10:17], v[218:225], v[134:137], v203, v203 op_sel_hi:[0,0,0]
	v_mfma_scale_f32_16x16x128_f8f6f4 v[126:129], v[2:9], v[226:233], v[126:129], v203, v203 op_sel_hi:[0,0,0]
	v_mfma_scale_f32_16x16x128_f8f6f4 v[118:121], v[10:17], v[226:233], v[118:121], v203, v203 op_sel_hi:[0,0,0]
	v_mfma_scale_f32_16x16x128_f8f6f4 v[110:113], v[2:9], v[234:241], v[110:113], v203, v203 op_sel_hi:[0,0,0]
	v_mfma_scale_f32_16x16x128_f8f6f4 v[102:105], v[10:17], v[234:241], v[102:105], v203, v203 op_sel_hi:[0,0,0]
	s_setprio 0
	s_setprio 1
	v_mfma_scale_f32_16x16x128_f8f6f4 v[154:157], v[18:25], v[210:217], v[154:157], v203, v203 op_sel_hi:[0,0,0]
	v_mfma_scale_f32_16x16x128_f8f6f4 v[146:149], v[26:33], v[210:217], v[146:149], v203, v203 op_sel_hi:[0,0,0]
	v_mfma_scale_f32_16x16x128_f8f6f4 v[138:141], v[18:25], v[218:225], v[138:141], v203, v203 op_sel_hi:[0,0,0]
	v_mfma_scale_f32_16x16x128_f8f6f4 v[130:133], v[26:33], v[218:225], v[130:133], v203, v203 op_sel_hi:[0,0,0]
	v_mfma_scale_f32_16x16x128_f8f6f4 v[122:125], v[18:25], v[226:233], v[122:125], v203, v203 op_sel_hi:[0,0,0]
	v_mfma_scale_f32_16x16x128_f8f6f4 v[114:117], v[26:33], v[226:233], v[114:117], v203, v203 op_sel_hi:[0,0,0]
	v_mfma_scale_f32_16x16x128_f8f6f4 v[106:109], v[18:25], v[234:241], v[106:109], v203, v203 op_sel_hi:[0,0,0]
	v_mfma_scale_f32_16x16x128_f8f6f4 v[98:101], v[26:33], v[234:241], v[98:101], v203, v203 op_sel_hi:[0,0,0]
	s_setprio 0
	s_barrier
	s_add_i32 m0, s50, 0xffffff80
	ds_read_b128 v[210:213], v202 offset:49152
	ds_read_b128 v[214:217], v202 offset:50176
	ds_read_b128 v[218:221], v202 offset:51200
	ds_read_b128 v[222:225], v202 offset:52224
	ds_read_b128 v[226:229], v202 offset:53248
	ds_read_b128 v[230:233], v202 offset:54272
	ds_read_b128 v[234:237], v202 offset:55296
	ds_read_b128 v[238:241], v202 offset:56320
	global_load_lds_dwordx4 v166, s[34:35] offset:128
	s_add_i32 m0, s51, 0xffffff80
	s_nop 0
	global_load_lds_dwordx4 v168, s[34:35] offset:128
	s_add_u32 s34, s34, 0x40080
	s_addc_u32 s35, s35, 0
	s_mov_b32 m0, s54
	s_nop 0
	global_load_lds_dwordx4 v166, s[34:35]
	s_mov_b32 m0, s55
	s_nop 0
	global_load_lds_dwordx4 v168, s[34:35]
	s_add_i32 m0, s52, 0xffffff80
	s_nop 0
	global_load_lds_dwordx4 v164, s[36:37] offset:128
	s_add_i32 m0, s53, 0xffffff80
	s_nop 0
	global_load_lds_dwordx4 v242, s[36:37] offset:128
	s_waitcnt vmcnt(8)
	s_waitcnt lgkmcnt(0)
	s_barrier
	s_setprio 1
	s_waitcnt lgkmcnt(0)
	v_mfma_scale_f32_16x16x128_f8f6f4 v[94:97], v[2:9], v[210:217], v[94:97], v203, v203 op_sel_hi:[0,0,0]
	v_mfma_scale_f32_16x16x128_f8f6f4 v[86:89], v[10:17], v[210:217], v[86:89], v203, v203 op_sel_hi:[0,0,0]
	v_mfma_scale_f32_16x16x128_f8f6f4 v[78:81], v[2:9], v[218:225], v[78:81], v203, v203 op_sel_hi:[0,0,0]
	v_mfma_scale_f32_16x16x128_f8f6f4 v[70:73], v[10:17], v[218:225], v[70:73], v203, v203 op_sel_hi:[0,0,0]
	v_mfma_scale_f32_16x16x128_f8f6f4 v[54:57], v[2:9], v[226:233], v[54:57], v203, v203 op_sel_hi:[0,0,0]
	v_mfma_scale_f32_16x16x128_f8f6f4 v[50:53], v[10:17], v[226:233], v[50:53], v203, v203 op_sel_hi:[0,0,0]
	v_mfma_scale_f32_16x16x128_f8f6f4 v[38:41], v[2:9], v[234:241], v[38:41], v203, v203 op_sel_hi:[0,0,0]
	v_mfma_scale_f32_16x16x128_f8f6f4 v[34:37], v[10:17], v[234:241], v[34:37], v203, v203 op_sel_hi:[0,0,0]
	s_setprio 0
	s_setprio 1
	v_mfma_scale_f32_16x16x128_f8f6f4 v[90:93], v[18:25], v[210:217], v[90:93], v203, v203 op_sel_hi:[0,0,0]
	v_mfma_scale_f32_16x16x128_f8f6f4 v[82:85], v[26:33], v[210:217], v[82:85], v203, v203 op_sel_hi:[0,0,0]
	v_mfma_scale_f32_16x16x128_f8f6f4 v[74:77], v[18:25], v[218:225], v[74:77], v203, v203 op_sel_hi:[0,0,0]
	v_mfma_scale_f32_16x16x128_f8f6f4 v[62:65], v[26:33], v[218:225], v[62:65], v203, v203 op_sel_hi:[0,0,0]
	v_mfma_scale_f32_16x16x128_f8f6f4 v[66:69], v[18:25], v[226:233], v[66:69], v203, v203 op_sel_hi:[0,0,0]
	v_mfma_scale_f32_16x16x128_f8f6f4 v[58:61], v[26:33], v[226:233], v[58:61], v203, v203 op_sel_hi:[0,0,0]
	v_mfma_scale_f32_16x16x128_f8f6f4 v[46:49], v[18:25], v[234:241], v[46:49], v203, v203 op_sel_hi:[0,0,0]
	v_mfma_scale_f32_16x16x128_f8f6f4 v[42:45], v[26:33], v[234:241], v[42:45], v203, v203 op_sel_hi:[0,0,0]
	s_setprio 0
	s_add_i32 s39, s39, 2
	s_add_u32 s0, s0, 0x100
	s_addc_u32 s1, s1, 0
	s_cmp_gt_u32 s39, 13
	s_barrier
	s_cbranch_scc0 .LBB0_1927
	s_and_b64 vcc, exec, s[12:13]
	s_cbranch_vccz .LBB0_1930
	s_barrier

; #define PG8_STAGE(bufoff, gbase, voff) do { _Pragma("unroll") for (int _i = 0; _i < 2; ++_i) \
;         __builtin_amdgcn_global_load_lds((const unsigned*)((const char*)(gbase) + (voff)[_i]), (LAS unsigned*)(lds + (bufoff) + ldsw + _i * 8192), 16, 0, 0); } while (0)
; #define PG8_LDA(dst, b, h) do { if constexpr (F8) { _Pragma("unroll") for (int m = 0; m < 4; ++m) dst##8[m] = PG8_LD8(lds, PG8_SA(b, h) + aoff + m * 2048); } \
;         else { _Pragma("unroll") for (int m = 0; m < 4; ++m) _Pragma("unroll") for (int k = 0; k < 2; ++k) dst[m][k] = *(const LAS bf16x8*)(lds + PG8_SA(b, h) + aoff + m * 2048 + k * 1024); } } while (0)
; #define PG8_WAIT_V(n) asm volatile("s_waitcnt vmcnt(" #n ")" ::: "memory")
; #define PG8_WAIT_L(n) asm volatile("s_waitcnt lgkmcnt(" #n ")" ::: "memory")
; #define PG8_BAR __builtin_amdgcn_s_barrier()
; #define PG8_SCHED __builtin_amdgcn_sched_barrier(0)
; template <bool GATHER, bool F8, class Epi, class Sched>
; __device__ __forceinline__ void gemm_phase(LAS unsigned char* lds, const int nt, const unsigned lda, const unsigned ldb, const Sched& S, const Epi& E) {
;     ...
;         for (int t = 0; t < nt; t += 2) {
;             const bool last = (t == nt - 2);
;             const char* a1 = cA + (size_t)(t + 1) * kstep;
;             const char* a2 = last ? nA : cA + (size_t)(t + 2) * kstep; const char* b2 = last ? nB : cB + (size_t)(t + 2) * kstep;
;             const char* a3 = a2 + kstep; const char* b3 = b2 + kstep;
;             unsigned w0[2], w1[2];
;             if constexpr (GATHER) {
; #pragma unroll
;                 for (int i = 0; i < 2; ++i) { w0[i] = last ? vN0[i] : vA0[i]; w1[i] = last ? vN1[i] : vA1[i]; }
;             } else {
; #pragma unroll
;                 for (int i = 0; i < 2; ++i) { w0[i] = voffA[i]; w1[i] = voffA[i]; }
;             }
;             PG8_LDB(B0, 0, 0); PG8_LDB(B1, 0, 1); PG8_SCHED; PG8_LDA(At, 0, 0); PG8_STAGE(PG8_SA(1, 1), a1 + hA, vA1);
;             PG8_WAIT_V(8); PG8_WAIT_L(0); PG8_BAR; PG8_MMA(0, 0, At, B0); PG8_MMA(0, 1, At, B1); PG8_BAR; PG8_SCHED;
;             PG8_LDA(At, 0, 1); PG8_STAGE(PG8_SB(0, 0), b2, voffB); PG8_STAGE(PG8_SB(0, 1), b2 + hB, voffB); PG8_STAGE(PG8_SA(0, 0), a2, w0);
;             PG8_WAIT_V(8); PG8_WAIT_L(0); PG8_BAR; PG8_MMA(1, 0, At, B0); PG8_MMA(1, 1, At, B1); PG8_BAR; PG8_SCHED;
.LBB0_2018:
	ds_read_b128 v[18:21], v186
	ds_read_b128 v[22:25], v186 offset:1024
	ds_read_b128 v[26:29], v186 offset:2048
	ds_read_b128 v[30:33], v186 offset:3072
	ds_read_b128 v[2:5], v186 offset:16384
	ds_read_b128 v[6:9], v186 offset:17408
	ds_read_b128 v[10:13], v186 offset:18432
	ds_read_b128 v[14:17], v186 offset:19456
	s_add_u32 s28, s26, 0xfffc0080
	s_addc_u32 s29, s27, -1
	s_cmp_eq_u32 s58, 12
	s_cselect_b32 s31, s25, s29
	s_cselect_b32 s30, s24, s28
	s_cselect_b32 s29, s23, s12
	s_cselect_b32 s28, s22, s7
	s_add_i32 m0, s1, 0xc000
	ds_read_b128 v[174:177], v187
	ds_read_b128 v[178:181], v187 offset:1024
	ds_read_b128 v[190:193], v187 offset:2048
	ds_read_b128 v[194:197], v187 offset:3072
	ds_read_b128 v[200:203], v187 offset:4096
	ds_read_b128 v[204:207], v187 offset:5120
	ds_read_b128 v[208:211], v187 offset:6144
	ds_read_b128 v[212:215], v187 offset:7168
	global_load_lds_dwordx4 v170, s[26:27]
	s_add_i32 m0, s1, 0xe000
	s_nop 0
	global_load_lds_dwordx4 v172, s[26:27]
	s_waitcnt vmcnt(8)
	s_waitcnt lgkmcnt(0)
	s_barrier
	s_setprio 1
	s_waitcnt lgkmcnt(0)
	v_mfma_scale_f32_16x16x128_f8f6f4 v[158:161], v[18:25], v[174:181], v[158:161], v188, v188 op_sel_hi:[0,0,0]
	v_mfma_scale_f32_16x16x128_f8f6f4 v[154:157], v[26:33], v[174:181], v[154:157], v188, v188 op_sel_hi:[0,0,0]
	v_mfma_scale_f32_16x16x128_f8f6f4 v[142:145], v[18:25], v[190:197], v[142:145], v188, v188 op_sel_hi:[0,0,0]
	v_mfma_scale_f32_16x16x128_f8f6f4 v[138:141], v[26:33], v[190:197], v[138:141], v188, v188 op_sel_hi:[0,0,0]
	v_mfma_scale_f32_16x16x128_f8f6f4 v[126:129], v[18:25], v[200:207], v[126:129], v188, v188 op_sel_hi:[0,0,0]
	v_mfma_scale_f32_16x16x128_f8f6f4 v[122:125], v[26:33], v[200:207], v[122:125], v188, v188 op_sel_hi:[0,0,0]
	v_mfma_scale_f32_16x16x128_f8f6f4 v[110:113], v[18:25], v[208:215], v[110:113], v188, v188 op_sel_hi:[0,0,0]
	v_mfma_scale_f32_16x16x128_f8f6f4 v[106:109], v[26:33], v[208:215], v[106:109], v188, v188 op_sel_hi:[0,0,0]
	s_setprio 0
	s_setprio 1
	v_mfma_scale_f32_16x16x128_f8f6f4 v[150:153], v[2:9], v[174:181], v[150:153], v188, v188 op_sel_hi:[0,0,0]
	v_mfma_scale_f32_16x16x128_f8f6f4 v[146:149], v[10:17], v[174:181], v[146:149], v188, v188 op_sel_hi:[0,0,0]
	v_mfma_scale_f32_16x16x128_f8f6f4 v[134:137], v[2:9], v[190:197], v[134:137], v188, v188 op_sel_hi:[0,0,0]
	v_mfma_scale_f32_16x16x128_f8f6f4 v[130:133], v[10:17], v[190:197], v[130:133], v188, v188 op_sel_hi:[0,0,0]
	v_mfma_scale_f32_16x16x128_f8f6f4 v[118:121], v[2:9], v[200:207], v[118:121], v188, v188 op_sel_hi:[0,0,0]
	v_mfma_scale_f32_16x16x128_f8f6f4 v[114:117], v[10:17], v[200:207], v[114:117], v188, v188 op_sel_hi:[0,0,0]
	v_mfma_scale_f32_16x16x128_f8f6f4 v[102:105], v[2:9], v[208:215], v[102:105], v188, v188 op_sel_hi:[0,0,0]
	v_mfma_scale_f32_16x16x128_f8f6f4 v[98:101], v[10:17], v[208:215], v[98:101], v188, v188 op_sel_hi:[0,0,0]
	s_setprio 0
	s_barrier
	s_mov_b32 m0, s35
	s_add_u32 s60, s28, 0x40000
	ds_read_b128 v[190:193], v187 offset:16384
	ds_read_b128 v[194:197], v187 offset:17408
	ds_read_b128 v[200:203], v187 offset:18432
	ds_read_b128 v[204:207], v187 offset:19456
	ds_read_b128 v[208:211], v187 offset:20480
	ds_read_b128 v[212:215], v187 offset:21504
	ds_read_b128 v[216:219], v187 offset:22528
	ds_read_b128 v[220:223], v187 offset:23552
	global_load_lds_dwordx4 v166, s[28:29]
	s_mov_b32 m0, s36
	s_addc_u32 s61, s29, 0
	global_load_lds_dwordx4 v162, s[28:29]
	s_mov_b32 m0, s37
	s_nop 0
	global_load_lds_dwordx4 v166, s[60:61]
	s_mov_b32 m0, s38
	s_nop 0
	global_load_lds_dwordx4 v162, s[60:61]
	s_mov_b32 m0, s1
	s_nop 0
	s_mov_b64 s[98:99], s[30:31]
	global_load_lds_dwordx4 v168, s[30:31]
	s_mov_b32 m0, s39
	s_nop 0
	global_load_lds_dwordx4 v164, s[30:31]
	s_waitcnt vmcnt(8)
	s_waitcnt lgkmcnt(0)
	s_barrier
	s_setprio 1
	s_waitcnt lgkmcnt(0)
	v_mfma_scale_f32_16x16x128_f8f6f4 v[86:89], v[18:25], v[190:197], v[86:89], v188, v188 op_sel_hi:[0,0,0]
	v_mfma_scale_f32_16x16x128_f8f6f4 v[82:85], v[26:33], v[190:197], v[82:85], v188, v188 op_sel_hi:[0,0,0]
	v_mfma_scale_f32_16x16x128_f8f6f4 v[70:73], v[18:25], v[200:207], v[70:73], v188, v188 op_sel_hi:[0,0,0]
	v_mfma_scale_f32_16x16x128_f8f6f4 v[66:69], v[26:33], v[200:207], v[66:69], v188, v188 op_sel_hi:[0,0,0]
	v_mfma_scale_f32_16x16x128_f8f6f4 v[54:57], v[18:25], v[208:215], v[54:57], v188, v188 op_sel_hi:[0,0,0]
	v_mfma_scale_f32_16x16x128_f8f6f4 v[42:45], v[26:33], v[208:215], v[42:45], v188, v188 op_sel_hi:[0,0,0]
	v_mfma_scale_f32_16x16x128_f8f6f4 v[38:41], v[18:25], v[216:223], v[38:41], v188, v188 op_sel_hi:[0,0,0]
	v_mfma_scale_f32_16x16x128_f8f6f4 v[34:37], v[26:33], v[216:223], v[34:37], v188, v188 op_sel_hi:[0,0,0]
	s_setprio 0
	s_setprio 1
	v_mfma_scale_f32_16x16x128_f8f6f4 v[94:97], v[2:9], v[190:197], v[94:97], v188, v188 op_sel_hi:[0,0,0]
	v_mfma_scale_f32_16x16x128_f8f6f4 v[90:93], v[10:17], v[190:197], v[90:93], v188, v188 op_sel_hi:[0,0,0]
	v_mfma_scale_f32_16x16x128_f8f6f4 v[78:81], v[2:9], v[200:207], v[78:81], v188, v188 op_sel_hi:[0,0,0]
	v_mfma_scale_f32_16x16x128_f8f6f4 v[74:77], v[10:17], v[200:207], v[74:77], v188, v188 op_sel_hi:[0,0,0]
	v_mfma_scale_f32_16x16x128_f8f6f4 v[62:65], v[2:9], v[208:215], v[62:65], v188, v188 op_sel_hi:[0,0,0]
	v_mfma_scale_f32_16x16x128_f8f6f4 v[58:61], v[10:17], v[208:215], v[58:61], v188, v188 op_sel_hi:[0,0,0]
	v_mfma_scale_f32_16x16x128_f8f6f4 v[50:53], v[2:9], v[216:223], v[50:53], v188, v188 op_sel_hi:[0,0,0]
	v_mfma_scale_f32_16x16x128_f8f6f4 v[46:49], v[10:17], v[216:223], v[46:49], v188, v188 op_sel_hi:[0,0,0]
	s_setprio 0
	s_barrier
; #define PG8_STAGE(bufoff, gbase, voff) do { _Pragma("unroll") for (int _i = 0; _i < 2; ++_i) \
;         __builtin_amdgcn_global_load_lds((const unsigned*)((const char*)(gbase) + (voff)[_i]), (LAS unsigned*)(lds + (bufoff) + ldsw + _i * 8192), 16, 0, 0); } while (0)
; #define PG8_LDA(dst, b, h) do { if constexpr (F8) { _Pragma("unroll") for (int m = 0; m < 4; ++m) dst##8[m] = PG8_LD8(lds, PG8_SA(b, h) + aoff + m * 2048); } \
;         else { _Pragma("unroll") for (int m = 0; m < 4; ++m) _Pragma("unroll") for (int k = 0; k < 2; ++k) dst[m][k] = *(const LAS bf16x8*)(lds + PG8_SA(b, h) + aoff + m * 2048 + k * 1024); } } while (0)
; #define PG8_LDB(dst, b, h) do { if constexpr (F8) { _Pragma("unroll") for (int n = 0; n < 2; ++n) dst##8[n] = PG8_LD8(ldsB, PG8_SBR(b, h) + boff + n * 2048); } \
;         else { _Pragma("unroll") for (int n = 0; n < 2; ++n) _Pragma("unroll") for (int k = 0; k < 2; ++k) dst[n][k] = *(const LAS bf16x8*)(ldsB + PG8_SBR(b, h) + boff + n * 2048 + k * 1024); } } while (0)
; #define PG8_WAIT_V(n) asm volatile("s_waitcnt vmcnt(" #n ")" ::: "memory")
; #define PG8_WAIT_L(n) asm volatile("s_waitcnt lgkmcnt(" #n ")" ::: "memory")
; #define PG8_BAR __builtin_amdgcn_s_barrier()
; #define PG8_SCHED __builtin_amdgcn_sched_barrier(0)
; template <bool GATHER, bool F8, class Epi, class Sched>
; __device__ __forceinline__ void gemm_phase(LAS unsigned char* lds, const int nt, const unsigned lda, const unsigned ldb, const Sched& S, const Epi& E) {
;     ...
;             PG8_LDB(B0, 1, 0); PG8_LDB(B1, 1, 1); PG8_SCHED; PG8_LDA(At, 1, 0); PG8_STAGE(PG8_SA(0, 1), a2 + hA, w1);
;             PG8_WAIT_V(8); PG8_WAIT_L(0); PG8_BAR; PG8_MMA(0, 0, At, B0); PG8_MMA(0, 1, At, B1); PG8_BAR; PG8_SCHED;
;             PG8_LDA(At, 1, 1); PG8_STAGE(PG8_SB(1, 0), b3, voffB); PG8_STAGE(PG8_SB(1, 1), b3 + hB, voffB); PG8_STAGE(PG8_SA(1, 0), a3, w0);
;             PG8_WAIT_V(8); PG8_WAIT_L(0); PG8_BAR; PG8_MMA(1, 0, At, B0); PG8_MMA(1, 1, At, B1); PG8_BAR; PG8_SCHED;
;         }
;         if (wr == 0) PG8_BAR;
	ds_read_b128 v[2:5], v186 offset:32768
	ds_read_b128 v[6:9], v186 offset:33792
	ds_read_b128 v[10:13], v186 offset:34816
	ds_read_b128 v[14:17], v186 offset:35840
	ds_read_b128 v[18:21], v186 offset:49152
	ds_read_b128 v[22:25], v186 offset:50176
	ds_read_b128 v[26:29], v186 offset:51200
	ds_read_b128 v[30:33], v186 offset:52224
	s_add_u32 s30, s30, 0x40000
	s_addc_u32 s31, s31, 0
	s_mov_b32 m0, s40
	ds_read_b128 v[190:193], v187 offset:32768
	ds_read_b128 v[194:197], v187 offset:33792
	ds_read_b128 v[200:203], v187 offset:34816
	ds_read_b128 v[204:207], v187 offset:35840
	ds_read_b128 v[208:211], v187 offset:36864
	ds_read_b128 v[212:215], v187 offset:37888
	ds_read_b128 v[216:219], v187 offset:38912
	ds_read_b128 v[220:223], v187 offset:39936
	global_load_lds_dwordx4 v168, s[30:31]
	s_mov_b32 m0, s41
	s_nop 0
	global_load_lds_dwordx4 v164, s[30:31]
	s_waitcnt vmcnt(8)
	s_waitcnt lgkmcnt(0)
	s_barrier
	s_setprio 1
	s_waitcnt lgkmcnt(0)
	v_mfma_scale_f32_16x16x128_f8f6f4 v[158:161], v[2:9], v[190:197], v[158:161], v188, v188 op_sel_hi:[0,0,0]
	v_mfma_scale_f32_16x16x128_f8f6f4 v[154:157], v[10:17], v[190:197], v[154:157], v188, v188 op_sel_hi:[0,0,0]
	v_mfma_scale_f32_16x16x128_f8f6f4 v[142:145], v[2:9], v[200:207], v[142:145], v188, v188 op_sel_hi:[0,0,0]
	v_mfma_scale_f32_16x16x128_f8f6f4 v[138:141], v[10:17], v[200:207], v[138:141], v188, v188 op_sel_hi:[0,0,0]
	v_mfma_scale_f32_16x16x128_f8f6f4 v[126:129], v[2:9], v[208:215], v[126:129], v188, v188 op_sel_hi:[0,0,0]
	v_mfma_scale_f32_16x16x128_f8f6f4 v[122:125], v[10:17], v[208:215], v[122:125], v188, v188 op_sel_hi:[0,0,0]
	v_mfma_scale_f32_16x16x128_f8f6f4 v[110:113], v[2:9], v[216:223], v[110:113], v188, v188 op_sel_hi:[0,0,0]
	v_mfma_scale_f32_16x16x128_f8f6f4 v[106:109], v[10:17], v[216:223], v[106:109], v188, v188 op_sel_hi:[0,0,0]
	s_setprio 0
	s_setprio 1
	v_mfma_scale_f32_16x16x128_f8f6f4 v[150:153], v[18:25], v[190:197], v[150:153], v188, v188 op_sel_hi:[0,0,0]
	v_mfma_scale_f32_16x16x128_f8f6f4 v[146:149], v[26:33], v[190:197], v[146:149], v188, v188 op_sel_hi:[0,0,0]
	v_mfma_scale_f32_16x16x128_f8f6f4 v[134:137], v[18:25], v[200:207], v[134:137], v188, v188 op_sel_hi:[0,0,0]
	v_mfma_scale_f32_16x16x128_f8f6f4 v[130:133], v[26:33], v[200:207], v[130:133], v188, v188 op_sel_hi:[0,0,0]
	v_mfma_scale_f32_16x16x128_f8f6f4 v[118:121], v[18:25], v[208:215], v[118:121], v188, v188 op_sel_hi:[0,0,0]
	v_mfma_scale_f32_16x16x128_f8f6f4 v[114:117], v[26:33], v[208:215], v[114:117], v188, v188 op_sel_hi:[0,0,0]
	v_mfma_scale_f32_16x16x128_f8f6f4 v[102:105], v[18:25], v[216:223], v[102:105], v188, v188 op_sel_hi:[0,0,0]
	v_mfma_scale_f32_16x16x128_f8f6f4 v[98:101], v[26:33], v[216:223], v[98:101], v188, v188 op_sel_hi:[0,0,0]
	s_setprio 0
	s_barrier
	s_add_i32 m0, s43, 0xffffff80
	ds_read_b128 v[190:193], v187 offset:49152
	ds_read_b128 v[194:197], v187 offset:50176
	ds_read_b128 v[200:203], v187 offset:51200
	ds_read_b128 v[204:207], v187 offset:52224
	ds_read_b128 v[208:211], v187 offset:53248
	ds_read_b128 v[212:215], v187 offset:54272
	ds_read_b128 v[216:219], v187 offset:55296
	ds_read_b128 v[220:223], v187 offset:56320
	global_load_lds_dwordx4 v166, s[28:29] offset:128
	s_add_i32 m0, s44, 0xffffff80
	s_nop 0
	global_load_lds_dwordx4 v162, s[28:29] offset:128
	s_add_u32 s28, s28, 0x40080
	s_addc_u32 s29, s29, 0
	s_mov_b32 m0, s47
	s_nop 0
	global_load_lds_dwordx4 v166, s[28:29]
	s_mov_b32 m0, s48
	s_nop 0
	global_load_lds_dwordx4 v162, s[28:29]
	s_add_i32 m0, s45, 0xffffff80
	s_nop 0
	global_load_lds_dwordx4 v168, s[98:99] offset:128
	s_add_i32 m0, s46, 0xffffff80
	s_nop 0
	global_load_lds_dwordx4 v164, s[98:99] offset:128
	s_waitcnt vmcnt(8)
	s_waitcnt lgkmcnt(0)
	s_barrier
	s_setprio 1
	s_waitcnt lgkmcnt(0)
	v_mfma_scale_f32_16x16x128_f8f6f4 v[86:89], v[2:9], v[190:197], v[86:89], v188, v188 op_sel_hi:[0,0,0]
	v_mfma_scale_f32_16x16x128_f8f6f4 v[82:85], v[10:17], v[190:197], v[82:85], v188, v188 op_sel_hi:[0,0,0]
	v_mfma_scale_f32_16x16x128_f8f6f4 v[70:73], v[2:9], v[200:207], v[70:73], v188, v188 op_sel_hi:[0,0,0]
	v_mfma_scale_f32_16x16x128_f8f6f4 v[66:69], v[10:17], v[200:207], v[66:69], v188, v188 op_sel_hi:[0,0,0]
	v_mfma_scale_f32_16x16x128_f8f6f4 v[54:57], v[2:9], v[208:215], v[54:57], v188, v188 op_sel_hi:[0,0,0]
	v_mfma_scale_f32_16x16x128_f8f6f4 v[42:45], v[10:17], v[208:215], v[42:45], v188, v188 op_sel_hi:[0,0,0]
	v_mfma_scale_f32_16x16x128_f8f6f4 v[38:41], v[2:9], v[216:223], v[38:41], v188, v188 op_sel_hi:[0,0,0]
	v_mfma_scale_f32_16x16x128_f8f6f4 v[34:37], v[10:17], v[216:223], v[34:37], v188, v188 op_sel_hi:[0,0,0]
	s_setprio 0
	s_setprio 1
	v_mfma_scale_f32_16x16x128_f8f6f4 v[94:97], v[18:25], v[190:197], v[94:97], v188, v188 op_sel_hi:[0,0,0]
	v_mfma_scale_f32_16x16x128_f8f6f4 v[90:93], v[26:33], v[190:197], v[90:93], v188, v188 op_sel_hi:[0,0,0]
	v_mfma_scale_f32_16x16x128_f8f6f4 v[78:81], v[18:25], v[200:207], v[78:81], v188, v188 op_sel_hi:[0,0,0]
	v_mfma_scale_f32_16x16x128_f8f6f4 v[74:77], v[26:33], v[200:207], v[74:77], v188, v188 op_sel_hi:[0,0,0]
	v_mfma_scale_f32_16x16x128_f8f6f4 v[62:65], v[18:25], v[208:215], v[62:65], v188, v188 op_sel_hi:[0,0,0]
	v_mfma_scale_f32_16x16x128_f8f6f4 v[58:61], v[26:33], v[208:215], v[58:61], v188, v188 op_sel_hi:[0,0,0]
	v_mfma_scale_f32_16x16x128_f8f6f4 v[50:53], v[18:25], v[216:223], v[50:53], v188, v188 op_sel_hi:[0,0,0]
	v_mfma_scale_f32_16x16x128_f8f6f4 v[46:49], v[26:33], v[216:223], v[46:49], v188, v188 op_sel_hi:[0,0,0]
	s_setprio 0
	s_add_i32 s58, s58, 2
	s_add_u32 s26, s26, 0x100
	s_addc_u32 s27, s27, 0
	s_add_u32 s7, s7, 0x100
	s_addc_u32 s12, s12, 0
	s_cmp_gt_u32 s58, 13
	s_barrier
	s_cbranch_scc0 .LBB0_2018
	s_and_b64 vcc, exec, s[14:15]
	s_cbranch_vccz .LBB0_2021
	s_barrier
